# baseline (speedup 1.0000x reference)
.LBB3_5:
	s_waitcnt lgkmcnt(0)
	v_cvt_f16_f32_e32 v180, s7
	v_cvt_f16_f32_e32 v182, s6
	v_cvt_f16_f32_e32 v181, s28
	s_waitcnt vmcnt(3)
	v_pk_mul_f16 v183, v182, v184 op_sel_hi:[0,1]
	v_pk_mul_f16 v190, v182, v187 op_sel_hi:[0,1]
	v_pk_mul_f16 v194, v180, v187 op_sel_hi:[0,1]
	v_pk_mul_f16 v198, v181, v187 op_sel_hi:[0,1]
	v_pk_mul_f16 v188, v182, v185 op_sel_hi:[0,1]
	v_pk_mul_f16 v189, v182, v186 op_sel_hi:[0,1]
	v_pk_mul_f16 v191, v180, v184 op_sel_hi:[0,1]
	s_mov_b64 exec, s[64:65]
	buffer_load_dwordx4 v[18:21], v249, s[16:19], 0 offen
	buffer_load_dwordx4 v[6:9], v249, s[16:19], 0 offen offset:512
	s_mov_b64 exec, -1
	v_pk_mul_f16 v192, v180, v185 op_sel_hi:[0,1]
	v_pk_mul_f16 v193, v180, v186 op_sel_hi:[0,1]
	v_pk_mul_f16 v195, v181, v184 op_sel_hi:[0,1]
	v_pk_mul_f16 v196, v181, v185 op_sel_hi:[0,1]
	v_pk_mul_f16 v197, v181, v186 op_sel_hi:[0,1]
	v_pk_fma_f16 v113, v113, v187, v190
	v_pk_fma_f16 v110, v110, v184, v183
	v_pk_fma_f16 v129, v129, v187, v190
	v_pk_fma_f16 v126, v126, v184, v183
	v_pk_fma_f16 v141, v141, v187, v190
	v_pk_fma_f16 v138, v138, v184, v183
	v_pk_fma_f16 v183, v89, v187, v194
	v_pk_fma_f16 v199, v109, v187, v194
	buffer_load_dwordx4 v[30:33], v250, s[16:19], 0 offen offset:512
	buffer_load_dwordx4 v[10:13], v250, s[16:19], 0 offen offset:1024
	v_pk_fma_f16 v194, v125, v187, v194
	v_pk_fma_f16 v203, v53, v187, v198
	v_pk_fma_f16 v207, v69, v187, v198
	v_pk_fma_f16 v187, v97, v187, v198
	v_pk_maximum3_f16 v198, v113, v129, v141
	v_pk_fma_f16 v112, v112, v186, v189
	v_pk_fma_f16 v111, v111, v185, v188
	v_pk_fma_f16 v128, v128, v186, v189
	v_pk_fma_f16 v127, v127, v185, v188
	v_pk_fma_f16 v140, v140, v186, v189
	v_pk_fma_f16 v139, v139, v185, v188
	v_pk_fma_f16 v188, v88, v186, v193
	v_pk_fma_f16 v189, v87, v185, v192
	v_pk_fma_f16 v190, v86, v184, v191
	v_pk_fma_f16 v200, v108, v186, v193
	v_pk_fma_f16 v201, v107, v185, v192
	s_mov_b64 exec, s[66:67]
	buffer_load_dwordx4 v[54:57], v250, s[16:19], 0 offen offset:2048
	buffer_load_dwordx4 v[14:17], v250, s[16:19], 0 offen offset:2560
	s_mov_b64 exec, -1
	v_pk_fma_f16 v202, v106, v184, v191
	v_pk_fma_f16 v193, v124, v186, v193
	v_pk_fma_f16 v192, v123, v185, v192
	v_pk_fma_f16 v191, v122, v184, v191
	v_pk_fma_f16 v204, v52, v186, v197
	v_pk_fma_f16 v205, v51, v185, v196
	v_pk_fma_f16 v206, v50, v184, v195
	v_pk_fma_f16 v208, v68, v186, v197
	v_pk_fma_f16 v209, v67, v185, v196
	v_pk_fma_f16 v210, v66, v184, v195
	v_pk_fma_f16 v186, v96, v186, v197
	v_pk_fma_f16 v185, v95, v185, v196
	v_pk_fma_f16 v184, v94, v184, v195
	v_pk_maximum3_f16 v195, v110, v126, v138
	v_pk_maximum3_f16 v196, v111, v127, v139
	v_pk_maximum3_f16 v197, v112, v128, v140
	v_pk_maximum3_f16 v214, v183, v199, v194
	v_pk_maximum3_f16 v218, v203, v207, v187
	v_pk_maximum3_f16 v211, v190, v202, v191
	v_pk_maximum3_f16 v212, v189, v201, v192
	v_pk_maximum3_f16 v213, v188, v200, v193
	v_pk_maximum3_f16 v215, v206, v210, v184
	v_pk_maximum3_f16 v216, v205, v209, v185
	v_pk_maximum3_f16 v198, v198, v214, v218
	v_pk_maximum3_f16 v217, v204, v208, v186
	v_pk_maximum3_f16 v195, v195, v211, v215
	v_pk_maximum3_f16 v196, v196, v212, v216
	v_pk_maximum3_f16 v197, v197, v213, v217
	v_pk_add_f16 v113, v113, v198 neg_lo:[0,1] neg_hi:[0,1]
	s_mov_b64 exec, s[64:65]
	buffer_load_dwordx4 v[74:77], v251, s[16:19], 0 offen
	buffer_load_dwordx4 v[26:29], v251, s[16:19], 0 offen offset:512
	s_mov_b64 exec, -1
	v_pk_add_f16 v110, v110, v195 neg_lo:[0,1] neg_hi:[0,1]
	v_pk_add_f16 v111, v111, v196 neg_lo:[0,1] neg_hi:[0,1]
	v_pk_add_f16 v112, v112, v197 neg_lo:[0,1] neg_hi:[0,1]
	v_pk_add_f16 v126, v126, v195 neg_lo:[0,1] neg_hi:[0,1]
	v_exp_f16_sdwa v211, v110 dst_sel:WORD_0 dst_unused:UNUSED_PAD src0_sel:WORD_0
	v_exp_f16_sdwa v212, v111 dst_sel:WORD_0 dst_unused:UNUSED_PAD src0_sel:WORD_0
	v_exp_f16_sdwa v213, v112 dst_sel:WORD_0 dst_unused:UNUSED_PAD src0_sel:WORD_0
	v_exp_f16_sdwa v214, v113 dst_sel:WORD_0 dst_unused:UNUSED_PAD src0_sel:WORD_0
	v_exp_f16_sdwa v211, v110 dst_sel:WORD_1 dst_unused:UNUSED_PRESERVE src0_sel:WORD_1
	v_exp_f16_sdwa v212, v111 dst_sel:WORD_1 dst_unused:UNUSED_PRESERVE src0_sel:WORD_1
	v_exp_f16_sdwa v213, v112 dst_sel:WORD_1 dst_unused:UNUSED_PRESERVE src0_sel:WORD_1
	v_exp_f16_sdwa v214, v113 dst_sel:WORD_1 dst_unused:UNUSED_PRESERVE src0_sel:WORD_1
	v_pk_add_f16 v127, v127, v196 neg_lo:[0,1] neg_hi:[0,1]
	v_pk_add_f16 v113, v211, 0
	v_pk_fma_f16 v81, v81, v214, 0
	v_pk_add_f16 v110, v214, 0
	v_pk_add_f16 v111, v213, 0
	v_pk_add_f16 v112, v212, 0
	v_pk_fma_f16 v80, v80, v213, 0
	v_pk_fma_f16 v79, v79, v212, 0
	v_pk_fma_f16 v78, v78, v211, 0
	v_pk_add_f16 v128, v128, v197 neg_lo:[0,1] neg_hi:[0,1]
	buffer_load_dwordx4 v[98:101], v252, s[16:19], 0 offen offset:512
	buffer_load_dwordx4 v[38:41], v252, s[16:19], 0 offen offset:1024
	v_pk_add_f16 v129, v129, v198 neg_lo:[0,1] neg_hi:[0,1]
	v_exp_f16_sdwa v211, v126 dst_sel:WORD_0 dst_unused:UNUSED_PAD src0_sel:WORD_0
	v_exp_f16_sdwa v212, v127 dst_sel:WORD_0 dst_unused:UNUSED_PAD src0_sel:WORD_0
	v_exp_f16_sdwa v213, v128 dst_sel:WORD_0 dst_unused:UNUSED_PAD src0_sel:WORD_0
	v_exp_f16_sdwa v214, v129 dst_sel:WORD_0 dst_unused:UNUSED_PAD src0_sel:WORD_0
	v_exp_f16_sdwa v211, v126 dst_sel:WORD_1 dst_unused:UNUSED_PRESERVE src0_sel:WORD_1
	v_exp_f16_sdwa v212, v127 dst_sel:WORD_1 dst_unused:UNUSED_PRESERVE src0_sel:WORD_1
	v_exp_f16_sdwa v213, v128 dst_sel:WORD_1 dst_unused:UNUSED_PRESERVE src0_sel:WORD_1
	v_exp_f16_sdwa v214, v129 dst_sel:WORD_1 dst_unused:UNUSED_PRESERVE src0_sel:WORD_1
	v_pk_add_f16 v113, v113, v211
	v_pk_fma_f16 v81, v105, v214, v81
	v_pk_add_f16 v105, v141, v198 neg_lo:[0,1] neg_hi:[0,1]
	v_pk_add_f16 v112, v112, v212
	v_pk_add_f16 v111, v111, v213
	v_pk_add_f16 v110, v110, v214
	v_pk_fma_f16 v78, v102, v211, v78
	v_pk_fma_f16 v79, v103, v212, v79
	v_pk_fma_f16 v80, v104, v213, v80
	v_pk_add_f16 v102, v138, v195 neg_lo:[0,1] neg_hi:[0,1]
	v_pk_add_f16 v103, v139, v196 neg_lo:[0,1] neg_hi:[0,1]
	v_pk_add_f16 v104, v140, v197 neg_lo:[0,1] neg_hi:[0,1]
	v_exp_f16_sdwa v126, v102 dst_sel:WORD_0 dst_unused:UNUSED_PAD src0_sel:WORD_0
	v_exp_f16_sdwa v127, v103 dst_sel:WORD_0 dst_unused:UNUSED_PAD src0_sel:WORD_0
	v_exp_f16_sdwa v128, v104 dst_sel:WORD_0 dst_unused:UNUSED_PAD src0_sel:WORD_0
	v_exp_f16_sdwa v129, v105 dst_sel:WORD_0 dst_unused:UNUSED_PAD src0_sel:WORD_0
	v_exp_f16_sdwa v126, v102 dst_sel:WORD_1 dst_unused:UNUSED_PRESERVE src0_sel:WORD_1
	v_exp_f16_sdwa v127, v103 dst_sel:WORD_1 dst_unused:UNUSED_PRESERVE src0_sel:WORD_1
	v_exp_f16_sdwa v128, v104 dst_sel:WORD_1 dst_unused:UNUSED_PRESERVE src0_sel:WORD_1
	v_exp_f16_sdwa v129, v105 dst_sel:WORD_1 dst_unused:UNUSED_PRESERVE src0_sel:WORD_1
	v_pk_add_f16 v105, v113, v126
	v_pk_add_f16 v102, v110, v129
	s_mov_b64 exec, s[66:67]
	buffer_load_dwordx4 v[114:117], v252, s[16:19], 0 offen offset:2048
	buffer_load_dwordx4 v[58:61], v252, s[16:19], 0 offen offset:2560
	s_mov_b64 exec, -1
	v_pk_add_f16 v103, v111, v128
	v_pk_add_f16 v104, v112, v127
	v_pk_fma_f16 v81, v121, v129, v81
	v_pk_fma_f16 v80, v120, v128, v80
	v_pk_fma_f16 v79, v119, v127, v79
	v_pk_fma_f16 v78, v118, v126, v78
	v_pk_add_f16 v110, v190, v195 neg_lo:[0,1] neg_hi:[0,1]
	v_pk_add_f16 v111, v189, v196 neg_lo:[0,1] neg_hi:[0,1]
	v_pk_add_f16 v112, v188, v197 neg_lo:[0,1] neg_hi:[0,1]
	v_pk_add_f16 v113, v183, v198 neg_lo:[0,1] neg_hi:[0,1]
	v_exp_f16_sdwa v118, v110 dst_sel:WORD_0 dst_unused:UNUSED_PAD src0_sel:WORD_0
	v_exp_f16_sdwa v119, v111 dst_sel:WORD_0 dst_unused:UNUSED_PAD src0_sel:WORD_0
	v_exp_f16_sdwa v120, v112 dst_sel:WORD_0 dst_unused:UNUSED_PAD src0_sel:WORD_0
	v_exp_f16_sdwa v121, v113 dst_sel:WORD_0 dst_unused:UNUSED_PAD src0_sel:WORD_0
	v_exp_f16_sdwa v118, v110 dst_sel:WORD_1 dst_unused:UNUSED_PRESERVE src0_sel:WORD_1
	v_exp_f16_sdwa v119, v111 dst_sel:WORD_1 dst_unused:UNUSED_PRESERVE src0_sel:WORD_1
	v_exp_f16_sdwa v120, v112 dst_sel:WORD_1 dst_unused:UNUSED_PRESERVE src0_sel:WORD_1
	v_exp_f16_sdwa v121, v113 dst_sel:WORD_1 dst_unused:UNUSED_PRESERVE src0_sel:WORD_1
	v_pk_add_f16 v110, v202, v195 neg_lo:[0,1] neg_hi:[0,1]
	v_pk_add_f16 v105, v105, v118
	v_pk_add_f16 v104, v104, v119
	v_pk_add_f16 v103, v103, v120
	s_mov_b64 exec, s[76:77]
	buffer_load_dwordx4 v[130:133], v253, s[16:19], 0 offen
	buffer_load_dwordx4 v[70:73], v253, s[16:19], 0 offen offset:512
	s_mov_b64 exec, -1
	v_pk_add_f16 v102, v102, v121
	v_pk_fma_f16 v78, v46, v118, v78
	v_pk_fma_f16 v79, v47, v119, v79
	v_pk_fma_f16 v80, v48, v120, v80
	v_pk_fma_f16 v81, v49, v121, v81
	v_pk_add_f16 v111, v201, v196 neg_lo:[0,1] neg_hi:[0,1]
	v_pk_add_f16 v112, v200, v197 neg_lo:[0,1] neg_hi:[0,1]
	v_pk_add_f16 v113, v199, v198 neg_lo:[0,1] neg_hi:[0,1]
	v_exp_f16_sdwa v118, v110 dst_sel:WORD_0 dst_unused:UNUSED_PAD src0_sel:WORD_0
	v_exp_f16_sdwa v119, v111 dst_sel:WORD_0 dst_unused:UNUSED_PAD src0_sel:WORD_0
	v_exp_f16_sdwa v120, v112 dst_sel:WORD_0 dst_unused:UNUSED_PAD src0_sel:WORD_0
	v_exp_f16_sdwa v121, v113 dst_sel:WORD_0 dst_unused:UNUSED_PAD src0_sel:WORD_0
	v_exp_f16_sdwa v118, v110 dst_sel:WORD_1 dst_unused:UNUSED_PRESERVE src0_sel:WORD_1
	v_exp_f16_sdwa v119, v111 dst_sel:WORD_1 dst_unused:UNUSED_PRESERVE src0_sel:WORD_1
	v_exp_f16_sdwa v120, v112 dst_sel:WORD_1 dst_unused:UNUSED_PRESERVE src0_sel:WORD_1
	v_exp_f16_sdwa v121, v113 dst_sel:WORD_1 dst_unused:UNUSED_PRESERVE src0_sel:WORD_1
	v_pk_add_f16 v110, v191, v195 neg_lo:[0,1] neg_hi:[0,1]
	v_pk_add_f16 v105, v105, v118
	v_pk_add_f16 v102, v102, v121
	v_pk_add_f16 v103, v103, v120
	v_pk_add_f16 v104, v104, v119
	v_pk_fma_f16 v81, v65, v121, v81
	v_pk_fma_f16 v80, v64, v120, v80
	s_mov_b64 exec, s[70:71]
	buffer_load_dwordx4 v[134:137], v254, s[16:19], 0 offen offset:512
	buffer_load_dwordx4 v[90:93], v254, s[16:19], 0 offen offset:1024
	s_mov_b64 exec, -1
	v_pk_fma_f16 v79, v63, v119, v79
	v_pk_fma_f16 v78, v62, v118, v78
	v_pk_add_f16 v111, v192, v196 neg_lo:[0,1] neg_hi:[0,1]
	v_pk_add_f16 v112, v193, v197 neg_lo:[0,1] neg_hi:[0,1]
	v_pk_add_f16 v113, v194, v198 neg_lo:[0,1] neg_hi:[0,1]
	v_exp_f16_sdwa v118, v110 dst_sel:WORD_0 dst_unused:UNUSED_PAD src0_sel:WORD_0
	v_exp_f16_sdwa v119, v111 dst_sel:WORD_0 dst_unused:UNUSED_PAD src0_sel:WORD_0
	v_exp_f16_sdwa v120, v112 dst_sel:WORD_0 dst_unused:UNUSED_PAD src0_sel:WORD_0
	v_exp_f16_sdwa v121, v113 dst_sel:WORD_0 dst_unused:UNUSED_PAD src0_sel:WORD_0
	v_exp_f16_sdwa v118, v110 dst_sel:WORD_1 dst_unused:UNUSED_PRESERVE src0_sel:WORD_1
	v_exp_f16_sdwa v119, v111 dst_sel:WORD_1 dst_unused:UNUSED_PRESERVE src0_sel:WORD_1
	v_exp_f16_sdwa v120, v112 dst_sel:WORD_1 dst_unused:UNUSED_PRESERVE src0_sel:WORD_1
	v_exp_f16_sdwa v121, v113 dst_sel:WORD_1 dst_unused:UNUSED_PRESERVE src0_sel:WORD_1
	v_pk_add_f16 v110, v206, v195 neg_lo:[0,1] neg_hi:[0,1]
	v_pk_add_f16 v105, v105, v118
	v_pk_add_f16 v104, v104, v119
	v_pk_add_f16 v103, v103, v120
	v_pk_add_f16 v102, v102, v121
	v_pk_fma_f16 v78, v82, v118, v78
	v_pk_fma_f16 v79, v83, v119, v79
	v_pk_fma_f16 v80, v84, v120, v80
	v_pk_fma_f16 v81, v85, v121, v81
	s_mov_b64 exec, s[78:79]
	buffer_load_dwordx4 v[142:145], v254, s[16:19], 0 offen offset:2048
	buffer_load_dwordx4 v[2:5], v254, s[16:19], 0 offen offset:2560
	s_mov_b64 exec, -1
	v_pk_add_f16 v111, v205, v196 neg_lo:[0,1] neg_hi:[0,1]
	v_pk_add_f16 v112, v204, v197 neg_lo:[0,1] neg_hi:[0,1]
	v_pk_add_f16 v113, v203, v198 neg_lo:[0,1] neg_hi:[0,1]
	v_exp_f16_sdwa v118, v110 dst_sel:WORD_0 dst_unused:UNUSED_PAD src0_sel:WORD_0
	v_exp_f16_sdwa v119, v111 dst_sel:WORD_0 dst_unused:UNUSED_PAD src0_sel:WORD_0
	v_exp_f16_sdwa v120, v112 dst_sel:WORD_0 dst_unused:UNUSED_PAD src0_sel:WORD_0
	v_exp_f16_sdwa v121, v113 dst_sel:WORD_0 dst_unused:UNUSED_PAD src0_sel:WORD_0
	v_exp_f16_sdwa v118, v110 dst_sel:WORD_1 dst_unused:UNUSED_PRESERVE src0_sel:WORD_1
	v_exp_f16_sdwa v119, v111 dst_sel:WORD_1 dst_unused:UNUSED_PRESERVE src0_sel:WORD_1
	v_exp_f16_sdwa v120, v112 dst_sel:WORD_1 dst_unused:UNUSED_PRESERVE src0_sel:WORD_1
	v_exp_f16_sdwa v121, v113 dst_sel:WORD_1 dst_unused:UNUSED_PRESERVE src0_sel:WORD_1
	v_pk_add_f16 v110, v210, v195 neg_lo:[0,1] neg_hi:[0,1]
	v_pk_add_f16 v105, v105, v118
	v_pk_add_f16 v102, v102, v121
	v_pk_add_f16 v103, v103, v120
	v_pk_add_f16 v104, v104, v119
	v_pk_fma_f16 v81, v25, v121, v81
	v_pk_fma_f16 v80, v24, v120, v80
	v_pk_fma_f16 v79, v23, v119, v79
	v_pk_fma_f16 v78, v22, v118, v78
	v_pk_add_f16 v111, v209, v196 neg_lo:[0,1] neg_hi:[0,1]
	v_pk_add_f16 v112, v208, v197 neg_lo:[0,1] neg_hi:[0,1]
	v_pk_add_f16 v113, v207, v198 neg_lo:[0,1] neg_hi:[0,1]
	v_exp_f16_sdwa v118, v110 dst_sel:WORD_0 dst_unused:UNUSED_PAD src0_sel:WORD_0
	v_exp_f16_sdwa v119, v111 dst_sel:WORD_0 dst_unused:UNUSED_PAD src0_sel:WORD_0
	v_exp_f16_sdwa v120, v112 dst_sel:WORD_0 dst_unused:UNUSED_PAD src0_sel:WORD_0
	v_exp_f16_sdwa v121, v113 dst_sel:WORD_0 dst_unused:UNUSED_PAD src0_sel:WORD_0
	v_exp_f16_sdwa v118, v110 dst_sel:WORD_1 dst_unused:UNUSED_PRESERVE src0_sel:WORD_1
	v_exp_f16_sdwa v119, v111 dst_sel:WORD_1 dst_unused:UNUSED_PRESERVE src0_sel:WORD_1
	v_exp_f16_sdwa v120, v112 dst_sel:WORD_1 dst_unused:UNUSED_PRESERVE src0_sel:WORD_1
	v_exp_f16_sdwa v121, v113 dst_sel:WORD_1 dst_unused:UNUSED_PRESERVE src0_sel:WORD_1
	v_pk_add_f16 v110, v184, v195 neg_lo:[0,1] neg_hi:[0,1]
	v_pk_add_f16 v105, v105, v118
	v_pk_add_f16 v104, v104, v119
	v_pk_add_f16 v103, v103, v120
	v_pk_add_f16 v102, v102, v121
	v_pk_fma_f16 v78, v34, v118, v78
	v_pk_fma_f16 v79, v35, v119, v79
	v_pk_fma_f16 v80, v36, v120, v80
	v_pk_fma_f16 v81, v37, v121, v81
	v_pk_add_f16 v111, v185, v196 neg_lo:[0,1] neg_hi:[0,1]
	v_pk_add_f16 v112, v186, v197 neg_lo:[0,1] neg_hi:[0,1]
	v_pk_add_f16 v113, v187, v198 neg_lo:[0,1] neg_hi:[0,1]
	v_exp_f16_sdwa v118, v110 dst_sel:WORD_0 dst_unused:UNUSED_PAD src0_sel:WORD_0
	v_exp_f16_sdwa v119, v111 dst_sel:WORD_0 dst_unused:UNUSED_PAD src0_sel:WORD_0
	v_exp_f16_sdwa v120, v112 dst_sel:WORD_0 dst_unused:UNUSED_PAD src0_sel:WORD_0
	v_exp_f16_sdwa v121, v113 dst_sel:WORD_0 dst_unused:UNUSED_PAD src0_sel:WORD_0
	v_exp_f16_sdwa v118, v110 dst_sel:WORD_1 dst_unused:UNUSED_PRESERVE src0_sel:WORD_1
	v_exp_f16_sdwa v119, v111 dst_sel:WORD_1 dst_unused:UNUSED_PRESERVE src0_sel:WORD_1
	v_exp_f16_sdwa v120, v112 dst_sel:WORD_1 dst_unused:UNUSED_PRESERVE src0_sel:WORD_1
	v_exp_f16_sdwa v121, v113 dst_sel:WORD_1 dst_unused:UNUSED_PRESERVE src0_sel:WORD_1
	v_pk_add_f16 v105, v105, v118
	v_pk_add_f16 v104, v104, v119
	v_rcp_f16_e32 v110, v105
	v_rcp_f16_sdwa v105, v105 dst_sel:DWORD dst_unused:UNUSED_PAD src0_sel:WORD_1
	v_pk_add_f16 v103, v103, v120
	v_rcp_f16_e32 v111, v104
	v_rcp_f16_sdwa v104, v104 dst_sel:DWORD dst_unused:UNUSED_PAD src0_sel:WORD_1
	v_pk_add_f16 v102, v102, v121
	v_rcp_f16_e32 v112, v103
	v_rcp_f16_sdwa v103, v103 dst_sel:DWORD dst_unused:UNUSED_PAD src0_sel:WORD_1
	v_rcp_f16_e32 v113, v102
	v_rcp_f16_sdwa v102, v102 dst_sel:DWORD dst_unused:UNUSED_PAD src0_sel:WORD_1
	v_pk_fma_f16 v78, v42, v118, v78
	v_pack_b32_f16 v105, v110, v105
	v_pk_fma_f16 v79, v43, v119, v79
	v_pk_mul_f16 v110, v78, v105
	v_pack_b32_f16 v78, v111, v104
	v_pk_fma_f16 v80, v44, v120, v80
	v_pk_mul_f16 v111, v79, v78
	v_pack_b32_f16 v78, v112, v103
	v_pk_fma_f16 v81, v45, v121, v81
	v_pk_mul_f16 v112, v80, v78
	v_pack_b32_f16 v78, v113, v102
	v_pk_mul_f16 v113, v81, v78
	s_waitcnt vmcnt(12)
	v_pk_mul_f16 v78, v182, v154 op_sel_hi:[0,1]
	v_pk_mul_f16 v81, v182, v157 op_sel_hi:[0,1]
	v_pk_mul_f16 v105, v180, v157 op_sel_hi:[0,1]
	v_pk_mul_f16 v121, v181, v157 op_sel_hi:[0,1]
	v_pk_mul_f16 v79, v182, v155 op_sel_hi:[0,1]
	v_pk_mul_f16 v80, v182, v156 op_sel_hi:[0,1]
	v_pk_mul_f16 v102, v180, v154 op_sel_hi:[0,1]
	v_pk_mul_f16 v103, v180, v155 op_sel_hi:[0,1]
	v_pk_mul_f16 v104, v180, v156 op_sel_hi:[0,1]
	v_pk_mul_f16 v118, v181, v154 op_sel_hi:[0,1]
	v_pk_mul_f16 v119, v181, v155 op_sel_hi:[0,1]
	v_pk_mul_f16 v120, v181, v156 op_sel_hi:[0,1]
	v_pk_fma_f16 v89, v89, v157, v81
	v_pk_fma_f16 v86, v86, v154, v78
	v_pk_fma_f16 v109, v109, v157, v81
	v_pk_fma_f16 v106, v106, v154, v78
	v_pk_fma_f16 v81, v125, v157, v81
	v_pk_fma_f16 v78, v122, v154, v78
	v_pk_fma_f16 v122, v53, v157, v105
	v_pk_fma_f16 v126, v69, v157, v105
	v_pk_fma_f16 v105, v97, v157, v105
	v_pk_fma_f16 v138, v21, v157, v121
	v_pk_fma_f16 v183, v33, v157, v121
	v_pk_fma_f16 v121, v57, v157, v121
	v_pk_maximum3_f16 v157, v89, v109, v81
	v_pk_fma_f16 v88, v88, v156, v80
	v_pk_fma_f16 v87, v87, v155, v79
	v_pk_fma_f16 v108, v108, v156, v80
	v_pk_fma_f16 v107, v107, v155, v79
	v_pk_fma_f16 v80, v124, v156, v80
	v_pk_fma_f16 v79, v123, v155, v79
	v_pk_fma_f16 v123, v52, v156, v104
	v_pk_fma_f16 v124, v51, v155, v103
	v_pk_fma_f16 v125, v50, v154, v102
	v_pk_fma_f16 v127, v68, v156, v104
	v_pk_fma_f16 v128, v67, v155, v103
	v_pk_fma_f16 v129, v66, v154, v102
	v_pk_fma_f16 v104, v96, v156, v104
	v_pk_fma_f16 v103, v95, v155, v103
	v_pk_fma_f16 v102, v94, v154, v102
	v_pk_fma_f16 v139, v20, v156, v120
	v_pk_fma_f16 v140, v19, v155, v119
	v_pk_fma_f16 v141, v18, v154, v118
	v_pk_fma_f16 v184, v32, v156, v120
	v_pk_fma_f16 v185, v31, v155, v119
	v_pk_fma_f16 v186, v30, v154, v118
	v_pk_fma_f16 v120, v56, v156, v120
	v_pk_fma_f16 v119, v55, v155, v119
	v_pk_fma_f16 v118, v54, v154, v118
	v_pk_maximum3_f16 v154, v86, v106, v78
	v_pk_maximum3_f16 v155, v87, v107, v79
	v_pk_maximum3_f16 v156, v88, v108, v80
	v_pk_maximum3_f16 v190, v122, v126, v105
	v_pk_maximum3_f16 v194, v138, v183, v121
	v_pk_maximum3_f16 v187, v125, v129, v102
	v_pk_maximum3_f16 v188, v124, v128, v103
	v_pk_maximum3_f16 v189, v123, v127, v104
	v_pk_maximum3_f16 v191, v141, v186, v118
	v_pk_maximum3_f16 v192, v140, v185, v119
	v_pk_maximum3_f16 v157, v157, v190, v194
	v_pk_maximum3_f16 v193, v139, v184, v120
	v_pk_maximum3_f16 v154, v154, v187, v191
	v_pk_maximum3_f16 v155, v155, v188, v192
	v_pk_maximum3_f16 v156, v156, v189, v193
	v_pk_add_f16 v89, v89, v157 neg_lo:[0,1] neg_hi:[0,1]
	v_pk_add_f16 v86, v86, v154 neg_lo:[0,1] neg_hi:[0,1]
	v_pk_add_f16 v87, v87, v155 neg_lo:[0,1] neg_hi:[0,1]
	v_pk_add_f16 v88, v88, v156 neg_lo:[0,1] neg_hi:[0,1]
	v_pk_add_f16 v106, v106, v154 neg_lo:[0,1] neg_hi:[0,1]
	v_exp_f16_sdwa v187, v86 dst_sel:WORD_0 dst_unused:UNUSED_PAD src0_sel:WORD_0
	v_exp_f16_sdwa v188, v87 dst_sel:WORD_0 dst_unused:UNUSED_PAD src0_sel:WORD_0
	v_exp_f16_sdwa v189, v88 dst_sel:WORD_0 dst_unused:UNUSED_PAD src0_sel:WORD_0
	v_exp_f16_sdwa v190, v89 dst_sel:WORD_0 dst_unused:UNUSED_PAD src0_sel:WORD_0
	v_exp_f16_sdwa v187, v86 dst_sel:WORD_1 dst_unused:UNUSED_PRESERVE src0_sel:WORD_1
	v_exp_f16_sdwa v188, v87 dst_sel:WORD_1 dst_unused:UNUSED_PRESERVE src0_sel:WORD_1
	v_exp_f16_sdwa v189, v88 dst_sel:WORD_1 dst_unused:UNUSED_PRESERVE src0_sel:WORD_1
	v_exp_f16_sdwa v190, v89 dst_sel:WORD_1 dst_unused:UNUSED_PRESERVE src0_sel:WORD_1
	v_pk_add_f16 v107, v107, v155 neg_lo:[0,1] neg_hi:[0,1]
	v_pk_add_f16 v89, v187, 0
	v_pk_fma_f16 v49, v49, v190, 0
	v_pk_add_f16 v86, v190, 0
	v_pk_add_f16 v87, v189, 0
	v_pk_add_f16 v88, v188, 0
	v_pk_fma_f16 v48, v48, v189, 0
	v_pk_fma_f16 v47, v47, v188, 0
	v_pk_fma_f16 v46, v46, v187, 0
	v_pk_add_f16 v108, v108, v156 neg_lo:[0,1] neg_hi:[0,1]
	v_pk_add_f16 v109, v109, v157 neg_lo:[0,1] neg_hi:[0,1]
	v_exp_f16_sdwa v187, v106 dst_sel:WORD_0 dst_unused:UNUSED_PAD src0_sel:WORD_0
	v_exp_f16_sdwa v188, v107 dst_sel:WORD_0 dst_unused:UNUSED_PAD src0_sel:WORD_0
	v_exp_f16_sdwa v189, v108 dst_sel:WORD_0 dst_unused:UNUSED_PAD src0_sel:WORD_0
	v_exp_f16_sdwa v190, v109 dst_sel:WORD_0 dst_unused:UNUSED_PAD src0_sel:WORD_0
	v_exp_f16_sdwa v187, v106 dst_sel:WORD_1 dst_unused:UNUSED_PRESERVE src0_sel:WORD_1
	v_exp_f16_sdwa v188, v107 dst_sel:WORD_1 dst_unused:UNUSED_PRESERVE src0_sel:WORD_1
	v_exp_f16_sdwa v189, v108 dst_sel:WORD_1 dst_unused:UNUSED_PRESERVE src0_sel:WORD_1
	v_exp_f16_sdwa v190, v109 dst_sel:WORD_1 dst_unused:UNUSED_PRESERVE src0_sel:WORD_1
	v_pk_add_f16 v89, v89, v187
	v_pk_fma_f16 v49, v65, v190, v49
	v_pk_add_f16 v65, v81, v157 neg_lo:[0,1] neg_hi:[0,1]
	v_pk_add_f16 v88, v88, v188
	v_pk_add_f16 v87, v87, v189
	v_pk_add_f16 v86, v86, v190
	v_pk_fma_f16 v46, v62, v187, v46
	v_pk_fma_f16 v47, v63, v188, v47
	v_pk_fma_f16 v48, v64, v189, v48
	v_pk_add_f16 v62, v78, v154 neg_lo:[0,1] neg_hi:[0,1]
	v_pk_add_f16 v63, v79, v155 neg_lo:[0,1] neg_hi:[0,1]
	v_pk_add_f16 v64, v80, v156 neg_lo:[0,1] neg_hi:[0,1]
	v_exp_f16_sdwa v78, v62 dst_sel:WORD_0 dst_unused:UNUSED_PAD src0_sel:WORD_0
	v_exp_f16_sdwa v79, v63 dst_sel:WORD_0 dst_unused:UNUSED_PAD src0_sel:WORD_0
	v_exp_f16_sdwa v80, v64 dst_sel:WORD_0 dst_unused:UNUSED_PAD src0_sel:WORD_0
	v_exp_f16_sdwa v81, v65 dst_sel:WORD_0 dst_unused:UNUSED_PAD src0_sel:WORD_0
	v_exp_f16_sdwa v78, v62 dst_sel:WORD_1 dst_unused:UNUSED_PRESERVE src0_sel:WORD_1
	v_exp_f16_sdwa v79, v63 dst_sel:WORD_1 dst_unused:UNUSED_PRESERVE src0_sel:WORD_1
	v_exp_f16_sdwa v80, v64 dst_sel:WORD_1 dst_unused:UNUSED_PRESERVE src0_sel:WORD_1
	v_exp_f16_sdwa v81, v65 dst_sel:WORD_1 dst_unused:UNUSED_PRESERVE src0_sel:WORD_1
	v_pk_add_f16 v65, v89, v78
	v_pk_add_f16 v62, v86, v81
	v_pk_add_f16 v63, v87, v80
	v_pk_add_f16 v64, v88, v79
	v_pk_fma_f16 v49, v85, v81, v49
	v_pk_fma_f16 v48, v84, v80, v48
	v_pk_fma_f16 v47, v83, v79, v47
	v_pk_fma_f16 v46, v82, v78, v46
	v_pk_add_f16 v78, v125, v154 neg_lo:[0,1] neg_hi:[0,1]
	v_pk_add_f16 v79, v124, v155 neg_lo:[0,1] neg_hi:[0,1]
	v_pk_add_f16 v80, v123, v156 neg_lo:[0,1] neg_hi:[0,1]
	v_pk_add_f16 v81, v122, v157 neg_lo:[0,1] neg_hi:[0,1]
	v_exp_f16_sdwa v82, v78 dst_sel:WORD_0 dst_unused:UNUSED_PAD src0_sel:WORD_0
	v_exp_f16_sdwa v83, v79 dst_sel:WORD_0 dst_unused:UNUSED_PAD src0_sel:WORD_0
	v_exp_f16_sdwa v84, v80 dst_sel:WORD_0 dst_unused:UNUSED_PAD src0_sel:WORD_0
	v_exp_f16_sdwa v85, v81 dst_sel:WORD_0 dst_unused:UNUSED_PAD src0_sel:WORD_0
	v_exp_f16_sdwa v82, v78 dst_sel:WORD_1 dst_unused:UNUSED_PRESERVE src0_sel:WORD_1
	v_exp_f16_sdwa v83, v79 dst_sel:WORD_1 dst_unused:UNUSED_PRESERVE src0_sel:WORD_1
	v_exp_f16_sdwa v84, v80 dst_sel:WORD_1 dst_unused:UNUSED_PRESERVE src0_sel:WORD_1
	v_exp_f16_sdwa v85, v81 dst_sel:WORD_1 dst_unused:UNUSED_PRESERVE src0_sel:WORD_1
	v_pk_add_f16 v78, v129, v154 neg_lo:[0,1] neg_hi:[0,1]
	v_pk_add_f16 v65, v65, v82
	v_pk_add_f16 v64, v64, v83
	v_pk_add_f16 v63, v63, v84
	v_pk_add_f16 v62, v62, v85
	v_pk_fma_f16 v46, v22, v82, v46
	v_pk_fma_f16 v47, v23, v83, v47
	v_pk_fma_f16 v48, v24, v84, v48
	v_pk_fma_f16 v49, v25, v85, v49
	v_pk_add_f16 v79, v128, v155 neg_lo:[0,1] neg_hi:[0,1]
	v_pk_add_f16 v80, v127, v156 neg_lo:[0,1] neg_hi:[0,1]
	v_pk_add_f16 v81, v126, v157 neg_lo:[0,1] neg_hi:[0,1]
	v_exp_f16_sdwa v82, v78 dst_sel:WORD_0 dst_unused:UNUSED_PAD src0_sel:WORD_0
	v_exp_f16_sdwa v83, v79 dst_sel:WORD_0 dst_unused:UNUSED_PAD src0_sel:WORD_0
	v_exp_f16_sdwa v84, v80 dst_sel:WORD_0 dst_unused:UNUSED_PAD src0_sel:WORD_0
	v_exp_f16_sdwa v85, v81 dst_sel:WORD_0 dst_unused:UNUSED_PAD src0_sel:WORD_0
	v_exp_f16_sdwa v82, v78 dst_sel:WORD_1 dst_unused:UNUSED_PRESERVE src0_sel:WORD_1
	v_exp_f16_sdwa v83, v79 dst_sel:WORD_1 dst_unused:UNUSED_PRESERVE src0_sel:WORD_1
	v_exp_f16_sdwa v84, v80 dst_sel:WORD_1 dst_unused:UNUSED_PRESERVE src0_sel:WORD_1
	v_exp_f16_sdwa v85, v81 dst_sel:WORD_1 dst_unused:UNUSED_PRESERVE src0_sel:WORD_1
	v_pk_add_f16 v78, v102, v154 neg_lo:[0,1] neg_hi:[0,1]
	v_pk_add_f16 v65, v65, v82
	v_pk_add_f16 v62, v62, v85
	v_pk_add_f16 v63, v63, v84
	v_pk_add_f16 v64, v64, v83
	v_pk_fma_f16 v49, v37, v85, v49
	v_pk_fma_f16 v48, v36, v84, v48
	v_pk_fma_f16 v47, v35, v83, v47
	v_pk_fma_f16 v46, v34, v82, v46
	v_pk_add_f16 v79, v103, v155 neg_lo:[0,1] neg_hi:[0,1]
	v_pk_add_f16 v80, v104, v156 neg_lo:[0,1] neg_hi:[0,1]
	v_pk_add_f16 v81, v105, v157 neg_lo:[0,1] neg_hi:[0,1]
	v_exp_f16_sdwa v82, v78 dst_sel:WORD_0 dst_unused:UNUSED_PAD src0_sel:WORD_0
	v_exp_f16_sdwa v83, v79 dst_sel:WORD_0 dst_unused:UNUSED_PAD src0_sel:WORD_0
	v_exp_f16_sdwa v84, v80 dst_sel:WORD_0 dst_unused:UNUSED_PAD src0_sel:WORD_0
	v_exp_f16_sdwa v85, v81 dst_sel:WORD_0 dst_unused:UNUSED_PAD src0_sel:WORD_0
	v_exp_f16_sdwa v82, v78 dst_sel:WORD_1 dst_unused:UNUSED_PRESERVE src0_sel:WORD_1
	v_exp_f16_sdwa v83, v79 dst_sel:WORD_1 dst_unused:UNUSED_PRESERVE src0_sel:WORD_1
	v_exp_f16_sdwa v84, v80 dst_sel:WORD_1 dst_unused:UNUSED_PRESERVE src0_sel:WORD_1
	v_exp_f16_sdwa v85, v81 dst_sel:WORD_1 dst_unused:UNUSED_PRESERVE src0_sel:WORD_1
	v_pk_add_f16 v78, v141, v154 neg_lo:[0,1] neg_hi:[0,1]
	v_pk_add_f16 v65, v65, v82
	v_pk_add_f16 v64, v64, v83
	v_pk_add_f16 v63, v63, v84
	v_pk_add_f16 v62, v62, v85
	v_pk_fma_f16 v46, v42, v82, v46
	v_pk_fma_f16 v47, v43, v83, v47
	v_pk_fma_f16 v48, v44, v84, v48
	v_pk_fma_f16 v49, v45, v85, v49
	v_pk_add_f16 v79, v140, v155 neg_lo:[0,1] neg_hi:[0,1]
	v_pk_add_f16 v80, v139, v156 neg_lo:[0,1] neg_hi:[0,1]
	v_pk_add_f16 v81, v138, v157 neg_lo:[0,1] neg_hi:[0,1]
	v_exp_f16_sdwa v82, v78 dst_sel:WORD_0 dst_unused:UNUSED_PAD src0_sel:WORD_0
	v_exp_f16_sdwa v83, v79 dst_sel:WORD_0 dst_unused:UNUSED_PAD src0_sel:WORD_0
	v_exp_f16_sdwa v84, v80 dst_sel:WORD_0 dst_unused:UNUSED_PAD src0_sel:WORD_0
	v_exp_f16_sdwa v85, v81 dst_sel:WORD_0 dst_unused:UNUSED_PAD src0_sel:WORD_0
	v_exp_f16_sdwa v82, v78 dst_sel:WORD_1 dst_unused:UNUSED_PRESERVE src0_sel:WORD_1
	v_exp_f16_sdwa v83, v79 dst_sel:WORD_1 dst_unused:UNUSED_PRESERVE src0_sel:WORD_1
	v_exp_f16_sdwa v84, v80 dst_sel:WORD_1 dst_unused:UNUSED_PRESERVE src0_sel:WORD_1
	v_exp_f16_sdwa v85, v81 dst_sel:WORD_1 dst_unused:UNUSED_PRESERVE src0_sel:WORD_1
	v_pk_add_f16 v78, v186, v154 neg_lo:[0,1] neg_hi:[0,1]
	v_pk_add_f16 v65, v65, v82
	v_pk_add_f16 v62, v62, v85
	v_pk_add_f16 v63, v63, v84
	v_pk_add_f16 v64, v64, v83
	v_pk_fma_f16 v49, v9, v85, v49
	v_pk_fma_f16 v48, v8, v84, v48
	v_pk_fma_f16 v47, v7, v83, v47
	v_pk_fma_f16 v46, v6, v82, v46
	v_pk_add_f16 v79, v185, v155 neg_lo:[0,1] neg_hi:[0,1]
	v_pk_add_f16 v80, v184, v156 neg_lo:[0,1] neg_hi:[0,1]
	v_pk_add_f16 v81, v183, v157 neg_lo:[0,1] neg_hi:[0,1]
	v_exp_f16_sdwa v82, v78 dst_sel:WORD_0 dst_unused:UNUSED_PAD src0_sel:WORD_0
	v_exp_f16_sdwa v83, v79 dst_sel:WORD_0 dst_unused:UNUSED_PAD src0_sel:WORD_0
	v_exp_f16_sdwa v84, v80 dst_sel:WORD_0 dst_unused:UNUSED_PAD src0_sel:WORD_0
	v_exp_f16_sdwa v85, v81 dst_sel:WORD_0 dst_unused:UNUSED_PAD src0_sel:WORD_0
	v_exp_f16_sdwa v82, v78 dst_sel:WORD_1 dst_unused:UNUSED_PRESERVE src0_sel:WORD_1
	v_exp_f16_sdwa v83, v79 dst_sel:WORD_1 dst_unused:UNUSED_PRESERVE src0_sel:WORD_1
	v_exp_f16_sdwa v84, v80 dst_sel:WORD_1 dst_unused:UNUSED_PRESERVE src0_sel:WORD_1
	v_exp_f16_sdwa v85, v81 dst_sel:WORD_1 dst_unused:UNUSED_PRESERVE src0_sel:WORD_1
	v_pk_add_f16 v78, v118, v154 neg_lo:[0,1] neg_hi:[0,1]
	v_pk_add_f16 v65, v65, v82
	v_pk_add_f16 v64, v64, v83
	v_pk_add_f16 v63, v63, v84
	v_pk_add_f16 v62, v62, v85
	v_pk_fma_f16 v46, v10, v82, v46
	v_pk_fma_f16 v47, v11, v83, v47
	v_pk_fma_f16 v48, v12, v84, v48
	v_pk_fma_f16 v49, v13, v85, v49
	v_pk_add_f16 v79, v119, v155 neg_lo:[0,1] neg_hi:[0,1]
	v_pk_add_f16 v80, v120, v156 neg_lo:[0,1] neg_hi:[0,1]
	v_pk_add_f16 v81, v121, v157 neg_lo:[0,1] neg_hi:[0,1]
	v_exp_f16_sdwa v82, v78 dst_sel:WORD_0 dst_unused:UNUSED_PAD src0_sel:WORD_0
	v_exp_f16_sdwa v83, v79 dst_sel:WORD_0 dst_unused:UNUSED_PAD src0_sel:WORD_0
	v_exp_f16_sdwa v84, v80 dst_sel:WORD_0 dst_unused:UNUSED_PAD src0_sel:WORD_0
	v_exp_f16_sdwa v85, v81 dst_sel:WORD_0 dst_unused:UNUSED_PAD src0_sel:WORD_0
	v_exp_f16_sdwa v82, v78 dst_sel:WORD_1 dst_unused:UNUSED_PRESERVE src0_sel:WORD_1
	v_exp_f16_sdwa v83, v79 dst_sel:WORD_1 dst_unused:UNUSED_PRESERVE src0_sel:WORD_1
	v_exp_f16_sdwa v84, v80 dst_sel:WORD_1 dst_unused:UNUSED_PRESERVE src0_sel:WORD_1
	v_exp_f16_sdwa v85, v81 dst_sel:WORD_1 dst_unused:UNUSED_PRESERVE src0_sel:WORD_1
	v_pk_add_f16 v65, v65, v82
	v_pk_add_f16 v64, v64, v83
	v_rcp_f16_e32 v78, v65
	v_rcp_f16_sdwa v65, v65 dst_sel:DWORD dst_unused:UNUSED_PAD src0_sel:WORD_1
	v_pk_add_f16 v63, v63, v84
	v_rcp_f16_e32 v79, v64
	v_rcp_f16_sdwa v64, v64 dst_sel:DWORD dst_unused:UNUSED_PAD src0_sel:WORD_1
	v_pk_add_f16 v62, v62, v85
	v_rcp_f16_e32 v80, v63
	v_rcp_f16_sdwa v81, v63 dst_sel:DWORD dst_unused:UNUSED_PAD src0_sel:WORD_1
	v_pk_fma_f16 v47, v15, v83, v47
	v_pk_fma_f16 v46, v14, v82, v46
	v_rcp_f16_e32 v82, v62
	v_rcp_f16_sdwa v83, v62 dst_sel:DWORD dst_unused:UNUSED_PAD src0_sel:WORD_1
	v_pack_b32_f16 v62, v78, v65
	v_pk_mul_f16 v62, v46, v62
	v_pack_b32_f16 v46, v79, v64
	v_pk_fma_f16 v48, v16, v84, v48
	v_pk_mul_f16 v63, v47, v46
	v_pack_b32_f16 v46, v80, v81
	v_pk_fma_f16 v49, v17, v85, v49
	v_pk_mul_f16 v64, v48, v46
	v_pack_b32_f16 v46, v82, v83
	v_pk_mul_f16 v65, v49, v46
	s_waitcnt vmcnt(6)
	v_pk_mul_f16 v46, v182, v150 op_sel_hi:[0,1]
	v_pk_mul_f16 v47, v182, v151 op_sel_hi:[0,1]
	v_pk_mul_f16 v48, v182, v152 op_sel_hi:[0,1]
	v_pk_mul_f16 v49, v182, v153 op_sel_hi:[0,1]
	v_pk_mul_f16 v78, v180, v150 op_sel_hi:[0,1]
	v_pk_mul_f16 v82, v181, v150 op_sel_hi:[0,1]
	v_pk_fma_f16 v50, v50, v150, v46
	v_pk_fma_f16 v66, v66, v150, v46
	v_pk_fma_f16 v46, v94, v150, v46
	v_pk_mul_f16 v79, v180, v151 op_sel_hi:[0,1]
	v_pk_maximum3_f16 v118, v50, v66, v46
	v_pk_mul_f16 v80, v180, v152 op_sel_hi:[0,1]
	v_pk_mul_f16 v81, v180, v153 op_sel_hi:[0,1]
	v_pk_mul_f16 v83, v181, v151 op_sel_hi:[0,1]
	v_pk_mul_f16 v84, v181, v152 op_sel_hi:[0,1]
	v_pk_mul_f16 v85, v181, v153 op_sel_hi:[0,1]
	v_pk_fma_f16 v53, v53, v153, v49
	v_pk_fma_f16 v52, v52, v152, v48
	v_pk_fma_f16 v51, v51, v151, v47
	v_pk_fma_f16 v69, v69, v153, v49
	v_pk_fma_f16 v68, v68, v152, v48
	v_pk_fma_f16 v67, v67, v151, v47
	v_pk_fma_f16 v49, v97, v153, v49
	v_pk_fma_f16 v48, v96, v152, v48
	v_pk_fma_f16 v47, v95, v151, v47
	v_pk_fma_f16 v89, v18, v150, v78
	v_pk_fma_f16 v97, v30, v150, v78
	v_pk_fma_f16 v78, v54, v150, v78
	v_pk_fma_f16 v105, v74, v150, v82
	v_pk_fma_f16 v109, v98, v150, v82
	v_pk_fma_f16 v82, v114, v150, v82
	v_pk_maximum3_f16 v119, v51, v67, v47
	v_pk_maximum3_f16 v120, v52, v68, v48
	v_pk_maximum3_f16 v121, v53, v69, v49
	v_pk_maximum3_f16 v122, v89, v97, v78
	v_pk_fma_f16 v86, v21, v153, v81
	v_pk_maximum3_f16 v126, v105, v109, v82
	v_pk_fma_f16 v87, v20, v152, v80
	v_pk_maximum3_f16 v118, v118, v122, v126
	v_pk_fma_f16 v88, v19, v151, v79
	v_pk_fma_f16 v94, v33, v153, v81
	v_pk_fma_f16 v95, v32, v152, v80
	v_pk_fma_f16 v96, v31, v151, v79
	v_pk_fma_f16 v81, v57, v153, v81
	v_pk_fma_f16 v80, v56, v152, v80
	v_pk_fma_f16 v79, v55, v151, v79
	v_pk_fma_f16 v102, v77, v153, v85
	v_pk_fma_f16 v103, v76, v152, v84
	v_pk_fma_f16 v104, v75, v151, v83
	v_pk_fma_f16 v106, v101, v153, v85
	v_pk_fma_f16 v107, v100, v152, v84
	v_pk_fma_f16 v108, v99, v151, v83
	v_pk_fma_f16 v85, v117, v153, v85
	v_pk_fma_f16 v84, v116, v152, v84
	v_pk_fma_f16 v83, v115, v151, v83
	v_pk_maximum3_f16 v123, v88, v96, v79
	v_pk_maximum3_f16 v124, v87, v95, v80
	v_pk_maximum3_f16 v125, v86, v94, v81
	v_pk_maximum3_f16 v128, v103, v107, v84
	v_pk_maximum3_f16 v129, v102, v106, v85
	v_pk_maximum3_f16 v127, v104, v108, v83
	v_pk_maximum3_f16 v119, v119, v123, v127
	v_pk_maximum3_f16 v120, v120, v124, v128
	v_pk_maximum3_f16 v121, v121, v125, v129
	v_pk_add_f16 v50, v50, v118 neg_lo:[0,1] neg_hi:[0,1]
	v_pk_add_f16 v51, v51, v119 neg_lo:[0,1] neg_hi:[0,1]
	v_pk_add_f16 v52, v52, v120 neg_lo:[0,1] neg_hi:[0,1]
	v_pk_add_f16 v53, v53, v121 neg_lo:[0,1] neg_hi:[0,1]
	v_pk_add_f16 v66, v66, v118 neg_lo:[0,1] neg_hi:[0,1]
	v_exp_f16_sdwa v122, v50 dst_sel:WORD_0 dst_unused:UNUSED_PAD src0_sel:WORD_0
	v_exp_f16_sdwa v123, v51 dst_sel:WORD_0 dst_unused:UNUSED_PAD src0_sel:WORD_0
	v_exp_f16_sdwa v124, v52 dst_sel:WORD_0 dst_unused:UNUSED_PAD src0_sel:WORD_0
	v_exp_f16_sdwa v125, v53 dst_sel:WORD_0 dst_unused:UNUSED_PAD src0_sel:WORD_0
	v_exp_f16_sdwa v122, v50 dst_sel:WORD_1 dst_unused:UNUSED_PRESERVE src0_sel:WORD_1
	v_exp_f16_sdwa v123, v51 dst_sel:WORD_1 dst_unused:UNUSED_PRESERVE src0_sel:WORD_1
	v_exp_f16_sdwa v124, v52 dst_sel:WORD_1 dst_unused:UNUSED_PRESERVE src0_sel:WORD_1
	v_exp_f16_sdwa v125, v53 dst_sel:WORD_1 dst_unused:UNUSED_PRESERVE src0_sel:WORD_1
	v_pk_add_f16 v67, v67, v119 neg_lo:[0,1] neg_hi:[0,1]
	v_pk_add_f16 v50, v125, 0
	v_pk_fma_f16 v22, v22, v122, 0
	v_pk_add_f16 v51, v124, 0
	v_pk_add_f16 v52, v123, 0
	v_pk_add_f16 v53, v122, 0
	v_pk_fma_f16 v23, v23, v123, 0
	v_pk_fma_f16 v24, v24, v124, 0
	v_pk_fma_f16 v25, v25, v125, 0
	v_pk_add_f16 v68, v68, v120 neg_lo:[0,1] neg_hi:[0,1]
	v_pk_add_f16 v69, v69, v121 neg_lo:[0,1] neg_hi:[0,1]
	v_exp_f16_sdwa v122, v66 dst_sel:WORD_0 dst_unused:UNUSED_PAD src0_sel:WORD_0
	v_exp_f16_sdwa v123, v67 dst_sel:WORD_0 dst_unused:UNUSED_PAD src0_sel:WORD_0
	v_exp_f16_sdwa v124, v68 dst_sel:WORD_0 dst_unused:UNUSED_PAD src0_sel:WORD_0
	v_exp_f16_sdwa v125, v69 dst_sel:WORD_0 dst_unused:UNUSED_PAD src0_sel:WORD_0
	v_exp_f16_sdwa v122, v66 dst_sel:WORD_1 dst_unused:UNUSED_PRESERVE src0_sel:WORD_1
	v_exp_f16_sdwa v123, v67 dst_sel:WORD_1 dst_unused:UNUSED_PRESERVE src0_sel:WORD_1
	v_exp_f16_sdwa v124, v68 dst_sel:WORD_1 dst_unused:UNUSED_PRESERVE src0_sel:WORD_1
	v_exp_f16_sdwa v125, v69 dst_sel:WORD_1 dst_unused:UNUSED_PRESERVE src0_sel:WORD_1
	s_nop 0
	v_pk_add_f16 v50, v50, v125
	v_pk_fma_f16 v22, v34, v122, v22
	v_pk_add_f16 v34, v46, v118 neg_lo:[0,1] neg_hi:[0,1]
	v_pk_add_f16 v53, v53, v122
	v_pk_add_f16 v52, v52, v123
	v_pk_add_f16 v51, v51, v124
	v_pk_fma_f16 v25, v37, v125, v25
	v_pk_fma_f16 v24, v36, v124, v24
	v_pk_fma_f16 v23, v35, v123, v23
	v_pk_add_f16 v35, v47, v119 neg_lo:[0,1] neg_hi:[0,1]
	v_pk_add_f16 v36, v48, v120 neg_lo:[0,1] neg_hi:[0,1]
	v_pk_add_f16 v37, v49, v121 neg_lo:[0,1] neg_hi:[0,1]
	v_exp_f16_sdwa v46, v34 dst_sel:WORD_0 dst_unused:UNUSED_PAD src0_sel:WORD_0
	v_exp_f16_sdwa v47, v35 dst_sel:WORD_0 dst_unused:UNUSED_PAD src0_sel:WORD_0
	v_exp_f16_sdwa v48, v36 dst_sel:WORD_0 dst_unused:UNUSED_PAD src0_sel:WORD_0
	v_exp_f16_sdwa v49, v37 dst_sel:WORD_0 dst_unused:UNUSED_PAD src0_sel:WORD_0
	v_exp_f16_sdwa v46, v34 dst_sel:WORD_1 dst_unused:UNUSED_PRESERVE src0_sel:WORD_1
	v_exp_f16_sdwa v47, v35 dst_sel:WORD_1 dst_unused:UNUSED_PRESERVE src0_sel:WORD_1
	v_exp_f16_sdwa v48, v36 dst_sel:WORD_1 dst_unused:UNUSED_PRESERVE src0_sel:WORD_1
	v_exp_f16_sdwa v49, v37 dst_sel:WORD_1 dst_unused:UNUSED_PRESERVE src0_sel:WORD_1
	s_nop 0
	v_pk_add_f16 v34, v50, v49
	v_pk_add_f16 v35, v51, v48
	v_pk_add_f16 v36, v52, v47
	v_pk_add_f16 v37, v53, v46
	v_pk_fma_f16 v22, v42, v46, v22
	v_pk_fma_f16 v23, v43, v47, v23
	v_pk_fma_f16 v24, v44, v48, v24
	v_pk_fma_f16 v25, v45, v49, v25
	v_pk_add_f16 v42, v89, v118 neg_lo:[0,1] neg_hi:[0,1]
	v_pk_add_f16 v43, v88, v119 neg_lo:[0,1] neg_hi:[0,1]
	v_pk_add_f16 v44, v87, v120 neg_lo:[0,1] neg_hi:[0,1]
	v_pk_add_f16 v45, v86, v121 neg_lo:[0,1] neg_hi:[0,1]
	v_exp_f16_sdwa v46, v42 dst_sel:WORD_0 dst_unused:UNUSED_PAD src0_sel:WORD_0
	v_exp_f16_sdwa v47, v43 dst_sel:WORD_0 dst_unused:UNUSED_PAD src0_sel:WORD_0
	v_exp_f16_sdwa v48, v44 dst_sel:WORD_0 dst_unused:UNUSED_PAD src0_sel:WORD_0
	v_exp_f16_sdwa v49, v45 dst_sel:WORD_0 dst_unused:UNUSED_PAD src0_sel:WORD_0
	v_exp_f16_sdwa v46, v42 dst_sel:WORD_1 dst_unused:UNUSED_PRESERVE src0_sel:WORD_1
	v_exp_f16_sdwa v47, v43 dst_sel:WORD_1 dst_unused:UNUSED_PRESERVE src0_sel:WORD_1
	v_exp_f16_sdwa v48, v44 dst_sel:WORD_1 dst_unused:UNUSED_PRESERVE src0_sel:WORD_1
	v_exp_f16_sdwa v49, v45 dst_sel:WORD_1 dst_unused:UNUSED_PRESERVE src0_sel:WORD_1
	v_pk_add_f16 v42, v97, v118 neg_lo:[0,1] neg_hi:[0,1]
	v_pk_add_f16 v34, v34, v49
	v_pk_add_f16 v37, v37, v46
	v_pk_add_f16 v36, v36, v47
	v_pk_add_f16 v35, v35, v48
	v_pk_fma_f16 v25, v9, v49, v25
	v_pk_fma_f16 v24, v8, v48, v24
	v_pk_fma_f16 v23, v7, v47, v23
	v_pk_fma_f16 v22, v6, v46, v22
	v_pk_add_f16 v43, v96, v119 neg_lo:[0,1] neg_hi:[0,1]
	v_pk_add_f16 v44, v95, v120 neg_lo:[0,1] neg_hi:[0,1]
	v_pk_add_f16 v45, v94, v121 neg_lo:[0,1] neg_hi:[0,1]
	v_exp_f16_sdwa v46, v42 dst_sel:WORD_0 dst_unused:UNUSED_PAD src0_sel:WORD_0
	v_exp_f16_sdwa v47, v43 dst_sel:WORD_0 dst_unused:UNUSED_PAD src0_sel:WORD_0
	v_exp_f16_sdwa v48, v44 dst_sel:WORD_0 dst_unused:UNUSED_PAD src0_sel:WORD_0
	v_exp_f16_sdwa v49, v45 dst_sel:WORD_0 dst_unused:UNUSED_PAD src0_sel:WORD_0
	v_exp_f16_sdwa v46, v42 dst_sel:WORD_1 dst_unused:UNUSED_PRESERVE src0_sel:WORD_1
	v_exp_f16_sdwa v47, v43 dst_sel:WORD_1 dst_unused:UNUSED_PRESERVE src0_sel:WORD_1
	v_exp_f16_sdwa v48, v44 dst_sel:WORD_1 dst_unused:UNUSED_PRESERVE src0_sel:WORD_1
	v_exp_f16_sdwa v49, v45 dst_sel:WORD_1 dst_unused:UNUSED_PRESERVE src0_sel:WORD_1
	v_pk_add_f16 v42, v78, v118 neg_lo:[0,1] neg_hi:[0,1]
	v_pk_add_f16 v34, v34, v49
	v_pk_add_f16 v35, v35, v48
	v_pk_add_f16 v36, v36, v47
	v_pk_add_f16 v37, v37, v46
	v_pk_fma_f16 v22, v10, v46, v22
	v_pk_fma_f16 v23, v11, v47, v23
	v_pk_fma_f16 v24, v12, v48, v24
	v_pk_fma_f16 v25, v13, v49, v25
	v_pk_add_f16 v43, v79, v119 neg_lo:[0,1] neg_hi:[0,1]
	v_pk_add_f16 v44, v80, v120 neg_lo:[0,1] neg_hi:[0,1]
	v_pk_add_f16 v45, v81, v121 neg_lo:[0,1] neg_hi:[0,1]
	v_exp_f16_sdwa v46, v42 dst_sel:WORD_0 dst_unused:UNUSED_PAD src0_sel:WORD_0
	v_exp_f16_sdwa v47, v43 dst_sel:WORD_0 dst_unused:UNUSED_PAD src0_sel:WORD_0
	v_exp_f16_sdwa v48, v44 dst_sel:WORD_0 dst_unused:UNUSED_PAD src0_sel:WORD_0
	v_exp_f16_sdwa v49, v45 dst_sel:WORD_0 dst_unused:UNUSED_PAD src0_sel:WORD_0
	v_exp_f16_sdwa v46, v42 dst_sel:WORD_1 dst_unused:UNUSED_PRESERVE src0_sel:WORD_1
	v_exp_f16_sdwa v47, v43 dst_sel:WORD_1 dst_unused:UNUSED_PRESERVE src0_sel:WORD_1
	v_exp_f16_sdwa v48, v44 dst_sel:WORD_1 dst_unused:UNUSED_PRESERVE src0_sel:WORD_1
	v_exp_f16_sdwa v49, v45 dst_sel:WORD_1 dst_unused:UNUSED_PRESERVE src0_sel:WORD_1
	v_pk_add_f16 v42, v105, v118 neg_lo:[0,1] neg_hi:[0,1]
	v_pk_add_f16 v34, v34, v49
	v_pk_add_f16 v37, v37, v46
	v_pk_add_f16 v36, v36, v47
	v_pk_add_f16 v35, v35, v48
	v_pk_fma_f16 v25, v17, v49, v25
	v_pk_fma_f16 v24, v16, v48, v24
	v_pk_fma_f16 v23, v15, v47, v23
	v_pk_fma_f16 v22, v14, v46, v22
	v_pk_add_f16 v43, v104, v119 neg_lo:[0,1] neg_hi:[0,1]
	v_pk_add_f16 v44, v103, v120 neg_lo:[0,1] neg_hi:[0,1]
	v_pk_add_f16 v45, v102, v121 neg_lo:[0,1] neg_hi:[0,1]
	v_exp_f16_sdwa v46, v42 dst_sel:WORD_0 dst_unused:UNUSED_PAD src0_sel:WORD_0
	v_exp_f16_sdwa v47, v43 dst_sel:WORD_0 dst_unused:UNUSED_PAD src0_sel:WORD_0
	v_exp_f16_sdwa v48, v44 dst_sel:WORD_0 dst_unused:UNUSED_PAD src0_sel:WORD_0
	v_exp_f16_sdwa v49, v45 dst_sel:WORD_0 dst_unused:UNUSED_PAD src0_sel:WORD_0
	v_exp_f16_sdwa v46, v42 dst_sel:WORD_1 dst_unused:UNUSED_PRESERVE src0_sel:WORD_1
	v_exp_f16_sdwa v47, v43 dst_sel:WORD_1 dst_unused:UNUSED_PRESERVE src0_sel:WORD_1
	v_exp_f16_sdwa v48, v44 dst_sel:WORD_1 dst_unused:UNUSED_PRESERVE src0_sel:WORD_1
	v_exp_f16_sdwa v49, v45 dst_sel:WORD_1 dst_unused:UNUSED_PRESERVE src0_sel:WORD_1
	v_pk_add_f16 v42, v109, v118 neg_lo:[0,1] neg_hi:[0,1]
	v_pk_add_f16 v34, v34, v49
	v_pk_add_f16 v35, v35, v48
	v_pk_add_f16 v36, v36, v47
	v_pk_add_f16 v37, v37, v46
	v_pk_fma_f16 v22, v26, v46, v22
	v_pk_fma_f16 v23, v27, v47, v23
	v_pk_fma_f16 v24, v28, v48, v24
	v_pk_fma_f16 v25, v29, v49, v25
	v_pk_add_f16 v43, v108, v119 neg_lo:[0,1] neg_hi:[0,1]
	v_pk_add_f16 v44, v107, v120 neg_lo:[0,1] neg_hi:[0,1]
	v_pk_add_f16 v45, v106, v121 neg_lo:[0,1] neg_hi:[0,1]
	v_exp_f16_sdwa v46, v42 dst_sel:WORD_0 dst_unused:UNUSED_PAD src0_sel:WORD_0
	v_exp_f16_sdwa v47, v43 dst_sel:WORD_0 dst_unused:UNUSED_PAD src0_sel:WORD_0
	v_exp_f16_sdwa v48, v44 dst_sel:WORD_0 dst_unused:UNUSED_PAD src0_sel:WORD_0
	v_exp_f16_sdwa v49, v45 dst_sel:WORD_0 dst_unused:UNUSED_PAD src0_sel:WORD_0
	v_exp_f16_sdwa v46, v42 dst_sel:WORD_1 dst_unused:UNUSED_PRESERVE src0_sel:WORD_1
	v_exp_f16_sdwa v47, v43 dst_sel:WORD_1 dst_unused:UNUSED_PRESERVE src0_sel:WORD_1
	v_exp_f16_sdwa v48, v44 dst_sel:WORD_1 dst_unused:UNUSED_PRESERVE src0_sel:WORD_1
	v_exp_f16_sdwa v49, v45 dst_sel:WORD_1 dst_unused:UNUSED_PRESERVE src0_sel:WORD_1
	v_pk_add_f16 v42, v82, v118 neg_lo:[0,1] neg_hi:[0,1]
	v_pk_add_f16 v34, v34, v49
	v_pk_add_f16 v37, v37, v46
	v_pk_add_f16 v36, v36, v47
	v_pk_add_f16 v35, v35, v48
	v_pk_fma_f16 v25, v41, v49, v25
	v_pk_fma_f16 v24, v40, v48, v24
	v_pk_fma_f16 v23, v39, v47, v23
	v_pk_fma_f16 v22, v38, v46, v22
	v_pk_add_f16 v43, v83, v119 neg_lo:[0,1] neg_hi:[0,1]
	v_pk_add_f16 v44, v84, v120 neg_lo:[0,1] neg_hi:[0,1]
	v_pk_add_f16 v45, v85, v121 neg_lo:[0,1] neg_hi:[0,1]
	v_exp_f16_sdwa v46, v42 dst_sel:WORD_0 dst_unused:UNUSED_PAD src0_sel:WORD_0
	v_exp_f16_sdwa v47, v43 dst_sel:WORD_0 dst_unused:UNUSED_PAD src0_sel:WORD_0
	v_exp_f16_sdwa v48, v44 dst_sel:WORD_0 dst_unused:UNUSED_PAD src0_sel:WORD_0
	v_exp_f16_sdwa v49, v45 dst_sel:WORD_0 dst_unused:UNUSED_PAD src0_sel:WORD_0
	v_exp_f16_sdwa v46, v42 dst_sel:WORD_1 dst_unused:UNUSED_PRESERVE src0_sel:WORD_1
	v_exp_f16_sdwa v47, v43 dst_sel:WORD_1 dst_unused:UNUSED_PRESERVE src0_sel:WORD_1
	v_exp_f16_sdwa v48, v44 dst_sel:WORD_1 dst_unused:UNUSED_PRESERVE src0_sel:WORD_1
	v_exp_f16_sdwa v49, v45 dst_sel:WORD_1 dst_unused:UNUSED_PRESERVE src0_sel:WORD_1
	s_nop 0
	v_pk_add_f16 v34, v34, v49
	v_pk_add_f16 v35, v35, v48
	v_rcp_f16_e32 v44, v34
	v_rcp_f16_sdwa v34, v34 dst_sel:DWORD dst_unused:UNUSED_PAD src0_sel:WORD_1
	v_pk_add_f16 v36, v36, v47
	v_rcp_f16_e32 v45, v35
	v_rcp_f16_sdwa v35, v35 dst_sel:DWORD dst_unused:UNUSED_PAD src0_sel:WORD_1
	v_pk_add_f16 v37, v37, v46
	v_rcp_f16_e32 v43, v36
	v_rcp_f16_sdwa v36, v36 dst_sel:DWORD dst_unused:UNUSED_PAD src0_sel:WORD_1
	v_rcp_f16_e32 v42, v37
	v_rcp_f16_sdwa v37, v37 dst_sel:DWORD dst_unused:UNUSED_PAD src0_sel:WORD_1
	v_pk_fma_f16 v25, v61, v49, v25
	v_pack_b32_f16 v34, v44, v34
	v_pk_fma_f16 v24, v60, v48, v24
	v_pk_mul_f16 v25, v25, v34
	v_pack_b32_f16 v34, v45, v35
	v_pk_fma_f16 v23, v59, v47, v23
	v_pk_mul_f16 v24, v24, v34
	v_pack_b32_f16 v34, v43, v36
	v_pk_fma_f16 v22, v58, v46, v22
	v_pk_mul_f16 v23, v23, v34
	v_pack_b32_f16 v34, v42, v37
	v_pk_mul_f16 v22, v22, v34
	s_waitcnt vmcnt(0)
	s_cmp_eq_u32 s10, 1
	s_cbranch_scc1 .Lmydt3_1
	v_add_u32_e32 v250, 0x1b400, v171
	v_add_u32_e32 v251, 0x0, v250
	buffer_load_dwordx4 v[252:255], v251, s[16:19], 0 offen
	v_add_u32_e32 v251, 0xfffe7c00, v250
	buffer_load_dwordx4 v[252:255], v251, s[16:19], 0 offen
	v_add_u32_e32 v251, 0xfffe7e00, v250
	buffer_load_dwordx4 v[252:255], v251, s[16:19], 0 offen
	v_add_u32_e32 v251, 0xfffe8200, v250
	buffer_load_dwordx4 v[252:255], v251, s[16:19], 0 offen
	v_add_u32_e32 v251, 0xfffe8400, v250
	buffer_load_dwordx4 v[252:255], v251, s[16:19], 0 offen
	v_add_u32_e32 v251, 0xfffe8800, v250
	buffer_load_dwordx4 v[252:255], v251, s[16:19], 0 offen
	v_add_u32_e32 v251, 0xfffe8a00, v250
	buffer_load_dwordx4 v[252:255], v251, s[16:19], 0 offen
	v_add_u32_e32 v251, 0xfffffc00, v250
	buffer_load_dwordx4 v[252:255], v251, s[16:19], 0 offen
	v_add_u32_e32 v251, 0xfffffe00, v250
	buffer_load_dwordx4 v[252:255], v251, s[16:19], 0 offen
	v_add_u32_e32 v251, 0x200, v250
	buffer_load_dwordx4 v[252:255], v251, s[16:19], 0 offen
	v_add_u32_e32 v251, 0x400, v250
	buffer_load_dwordx4 v[252:255], v251, s[16:19], 0 offen
	v_add_u32_e32 v251, 0x800, v250
	buffer_load_dwordx4 v[252:255], v251, s[16:19], 0 offen
	v_add_u32_e32 v251, 0xa00, v250
	buffer_load_dwordx4 v[252:255], v251, s[16:19], 0 offen
	v_add_u32_e32 v251, 0x17c00, v250
	buffer_load_dwordx4 v[252:255], v251, s[16:19], 0 offen
	v_add_u32_e32 v251, 0x17e00, v250
	buffer_load_dwordx4 v[252:255], v251, s[16:19], 0 offen
	v_add_u32_e32 v251, 0x18200, v250
	buffer_load_dwordx4 v[252:255], v251, s[16:19], 0 offen
	v_add_u32_e32 v251, 0x18400, v250
	buffer_load_dwordx4 v[252:255], v251, s[16:19], 0 offen
	v_add_u32_e32 v251, 0x18800, v250
	buffer_load_dwordx4 v[252:255], v251, s[16:19], 0 offen
	v_add_u32_e32 v251, 0x18a00, v250
	buffer_load_dwordx4 v[252:255], v251, s[16:19], 0 offen
	v_add_u32_e32 v251, 0x18000, v250
	buffer_load_dwordx4 v[252:255], v251, s[16:19], 0 offen
	v_add_u32_e32 v251, 0x30000, v250
	buffer_load_dwordx4 v[252:255], v251, s[16:19], 0 offen
	v_add_u32_e32 v251, 0x48000, v250
	buffer_load_dwordx4 v[252:255], v251, s[16:19], 0 offen

.Lmyf_B1_7:
	s_mov_b64 exec, -1
	s_waitcnt lgkmcnt(0)
	v_cvt_f16_f32_e32 v183, s27
	v_cvt_f16_f32_e32 v185, s26
	v_cvt_f16_f32_e32 v184, s34
	s_mov_b64 s[4:5], 0
	s_waitcnt vmcnt(3)
	v_pk_mul_f16 v193, v185, v189 op_sel_hi:[0,1]
	v_pk_mul_f16 v197, v183, v189 op_sel_hi:[0,1]
	v_pk_mul_f16 v201, v184, v189 op_sel_hi:[0,1]
	v_pk_mul_f16 v190, v185, v186 op_sel_hi:[0,1]
	v_pk_mul_f16 v191, v185, v187 op_sel_hi:[0,1]
	v_pk_mul_f16 v192, v185, v188 op_sel_hi:[0,1]
	v_pk_mul_f16 v194, v183, v186 op_sel_hi:[0,1]
	s_mov_b64 exec, s[64:65]
	buffer_load_dwordx4 v[18:21], v249, s[16:19], 0 offen
	buffer_load_dwordx4 v[6:9], v249, s[16:19], 0 offen offset:512
	s_mov_b64 exec, -1
	v_pk_mul_f16 v195, v183, v187 op_sel_hi:[0,1]
	v_pk_mul_f16 v196, v183, v188 op_sel_hi:[0,1]
	v_pk_mul_f16 v198, v184, v186 op_sel_hi:[0,1]
	v_pk_mul_f16 v199, v184, v187 op_sel_hi:[0,1]
	v_pk_mul_f16 v200, v184, v188 op_sel_hi:[0,1]
	v_pk_fma_f16 v113, v113, v189, v193
	v_pk_fma_f16 v129, v129, v189, v197
	v_pk_fma_f16 v137, v137, v189, v201
	v_pk_fma_f16 v202, v85, v189, v193
	v_pk_fma_f16 v206, v109, v189, v197
	v_pk_fma_f16 v210, v125, v189, v201
	v_pk_fma_f16 v193, v53, v189, v193
	v_pk_fma_f16 v197, v69, v189, v197
	buffer_load_dwordx4 v[34:37], v250, s[16:19], 0 offen offset:512
	buffer_load_dwordx4 v[10:13], v250, s[16:19], 0 offen offset:1024
	v_pk_fma_f16 v189, v97, v189, v201
	v_pk_maximum3_f16 v201, v113, v129, v137
	v_pk_fma_f16 v112, v112, v188, v192
	v_pk_fma_f16 v111, v111, v187, v191
	v_pk_fma_f16 v110, v110, v186, v190
	v_pk_fma_f16 v128, v128, v188, v196
	v_pk_fma_f16 v127, v127, v187, v195
	v_pk_fma_f16 v126, v126, v186, v194
	v_pk_fma_f16 v136, v136, v188, v200
	v_pk_fma_f16 v135, v135, v187, v199
	v_pk_fma_f16 v134, v134, v186, v198
	v_pk_fma_f16 v203, v84, v188, v192
	v_pk_fma_f16 v204, v83, v187, v191
	v_pk_fma_f16 v205, v82, v186, v190
	v_pk_fma_f16 v207, v108, v188, v196
	v_pk_fma_f16 v208, v107, v187, v195
	s_mov_b64 exec, s[66:67]
	buffer_load_dwordx4 v[54:57], v250, s[16:19], 0 offen offset:2048
	buffer_load_dwordx4 v[14:17], v250, s[16:19], 0 offen offset:2560
	s_mov_b64 exec, -1
	v_pk_fma_f16 v209, v106, v186, v194
	v_pk_fma_f16 v211, v124, v188, v200
	v_pk_fma_f16 v212, v123, v187, v199
	v_pk_fma_f16 v213, v122, v186, v198
	v_pk_fma_f16 v192, v52, v188, v192
	v_pk_fma_f16 v191, v51, v187, v191
	v_pk_fma_f16 v190, v50, v186, v190
	v_pk_fma_f16 v196, v68, v188, v196
	v_pk_fma_f16 v195, v67, v187, v195
	v_pk_fma_f16 v194, v66, v186, v194
	v_pk_fma_f16 v188, v96, v188, v200
	v_pk_fma_f16 v187, v95, v187, v199
	v_pk_fma_f16 v186, v94, v186, v198
	v_pk_maximum3_f16 v198, v110, v126, v134
	v_pk_maximum3_f16 v199, v111, v127, v135
	v_pk_maximum3_f16 v200, v112, v128, v136
	v_pk_maximum3_f16 v217, v202, v206, v210
	v_pk_maximum3_f16 v221, v193, v197, v189
	v_pk_maximum3_f16 v214, v205, v209, v213
	v_pk_maximum3_f16 v215, v204, v208, v212
	v_pk_maximum3_f16 v216, v203, v207, v211
	v_pk_maximum3_f16 v218, v190, v194, v186
	v_pk_maximum3_f16 v219, v191, v195, v187
	v_pk_maximum3_f16 v201, v201, v217, v221
	v_pk_maximum3_f16 v220, v192, v196, v188
	v_pk_maximum3_f16 v198, v198, v214, v218
	v_pk_maximum3_f16 v199, v199, v215, v219
	v_pk_maximum3_f16 v200, v200, v216, v220
	v_pk_add_f16 v113, v113, v201 neg_lo:[0,1] neg_hi:[0,1]
	s_mov_b64 exec, s[64:65]
	buffer_load_dwordx4 v[74:77], v251, s[16:19], 0 offen
	buffer_load_dwordx4 v[26:29], v251, s[16:19], 0 offen offset:512
	s_mov_b64 exec, -1
	v_pk_add_f16 v110, v110, v198 neg_lo:[0,1] neg_hi:[0,1]
	v_pk_add_f16 v111, v111, v199 neg_lo:[0,1] neg_hi:[0,1]
	v_pk_add_f16 v112, v112, v200 neg_lo:[0,1] neg_hi:[0,1]
	v_pk_add_f16 v126, v126, v198 neg_lo:[0,1] neg_hi:[0,1]
	v_exp_f16_sdwa v214, v110 dst_sel:WORD_0 dst_unused:UNUSED_PAD src0_sel:WORD_0
	v_exp_f16_sdwa v215, v111 dst_sel:WORD_0 dst_unused:UNUSED_PAD src0_sel:WORD_0
	v_exp_f16_sdwa v216, v112 dst_sel:WORD_0 dst_unused:UNUSED_PAD src0_sel:WORD_0
	v_exp_f16_sdwa v217, v113 dst_sel:WORD_0 dst_unused:UNUSED_PAD src0_sel:WORD_0
	v_exp_f16_sdwa v214, v110 dst_sel:WORD_1 dst_unused:UNUSED_PRESERVE src0_sel:WORD_1
	v_exp_f16_sdwa v215, v111 dst_sel:WORD_1 dst_unused:UNUSED_PRESERVE src0_sel:WORD_1
	v_exp_f16_sdwa v216, v112 dst_sel:WORD_1 dst_unused:UNUSED_PRESERVE src0_sel:WORD_1
	v_exp_f16_sdwa v217, v113 dst_sel:WORD_1 dst_unused:UNUSED_PRESERVE src0_sel:WORD_1
	v_pk_add_f16 v127, v127, v199 neg_lo:[0,1] neg_hi:[0,1]
	v_pk_add_f16 v113, v214, 0
	v_pk_fma_f16 v73, v73, v217, 0
	v_pk_add_f16 v110, v217, 0
	v_pk_add_f16 v111, v216, 0
	v_pk_add_f16 v112, v215, 0
	v_pk_fma_f16 v72, v72, v216, 0
	v_pk_fma_f16 v71, v71, v215, 0
	v_pk_fma_f16 v70, v70, v214, 0
	v_pk_add_f16 v128, v128, v200 neg_lo:[0,1] neg_hi:[0,1]
	buffer_load_dwordx4 v[102:105], v252, s[16:19], 0 offen offset:512
	buffer_load_dwordx4 v[38:41], v252, s[16:19], 0 offen offset:1024
	v_pk_add_f16 v129, v129, v201 neg_lo:[0,1] neg_hi:[0,1]
	v_exp_f16_sdwa v214, v126 dst_sel:WORD_0 dst_unused:UNUSED_PAD src0_sel:WORD_0
	v_exp_f16_sdwa v215, v127 dst_sel:WORD_0 dst_unused:UNUSED_PAD src0_sel:WORD_0
	v_exp_f16_sdwa v216, v128 dst_sel:WORD_0 dst_unused:UNUSED_PAD src0_sel:WORD_0
	v_exp_f16_sdwa v217, v129 dst_sel:WORD_0 dst_unused:UNUSED_PAD src0_sel:WORD_0
	v_exp_f16_sdwa v214, v126 dst_sel:WORD_1 dst_unused:UNUSED_PRESERVE src0_sel:WORD_1
	v_exp_f16_sdwa v215, v127 dst_sel:WORD_1 dst_unused:UNUSED_PRESERVE src0_sel:WORD_1
	v_exp_f16_sdwa v216, v128 dst_sel:WORD_1 dst_unused:UNUSED_PRESERVE src0_sel:WORD_1
	v_exp_f16_sdwa v217, v129 dst_sel:WORD_1 dst_unused:UNUSED_PRESERVE src0_sel:WORD_1
	v_pk_add_f16 v113, v113, v214
	v_pk_fma_f16 v73, v101, v217, v73
	v_pk_add_f16 v101, v137, v201 neg_lo:[0,1] neg_hi:[0,1]
	v_pk_add_f16 v112, v112, v215
	v_pk_add_f16 v111, v111, v216
	v_pk_add_f16 v110, v110, v217
	v_pk_fma_f16 v70, v98, v214, v70
	v_pk_fma_f16 v71, v99, v215, v71
	v_pk_fma_f16 v72, v100, v216, v72
	v_pk_add_f16 v98, v134, v198 neg_lo:[0,1] neg_hi:[0,1]
	v_pk_add_f16 v99, v135, v199 neg_lo:[0,1] neg_hi:[0,1]
	v_pk_add_f16 v100, v136, v200 neg_lo:[0,1] neg_hi:[0,1]
	v_exp_f16_sdwa v126, v98 dst_sel:WORD_0 dst_unused:UNUSED_PAD src0_sel:WORD_0
	v_exp_f16_sdwa v127, v99 dst_sel:WORD_0 dst_unused:UNUSED_PAD src0_sel:WORD_0
	v_exp_f16_sdwa v128, v100 dst_sel:WORD_0 dst_unused:UNUSED_PAD src0_sel:WORD_0
	v_exp_f16_sdwa v129, v101 dst_sel:WORD_0 dst_unused:UNUSED_PAD src0_sel:WORD_0
	v_exp_f16_sdwa v126, v98 dst_sel:WORD_1 dst_unused:UNUSED_PRESERVE src0_sel:WORD_1
	v_exp_f16_sdwa v127, v99 dst_sel:WORD_1 dst_unused:UNUSED_PRESERVE src0_sel:WORD_1
	v_exp_f16_sdwa v128, v100 dst_sel:WORD_1 dst_unused:UNUSED_PRESERVE src0_sel:WORD_1
	v_exp_f16_sdwa v129, v101 dst_sel:WORD_1 dst_unused:UNUSED_PRESERVE src0_sel:WORD_1
	v_pk_add_f16 v101, v113, v126
	v_pk_add_f16 v98, v110, v129
	s_mov_b64 exec, s[66:67]
	buffer_load_dwordx4 v[118:121], v252, s[16:19], 0 offen offset:2048
	buffer_load_dwordx4 v[58:61], v252, s[16:19], 0 offen offset:2560
	s_mov_b64 exec, -1
	v_pk_add_f16 v99, v111, v128
	v_pk_add_f16 v100, v112, v127
	v_pk_fma_f16 v73, v117, v129, v73
	v_pk_fma_f16 v72, v116, v128, v72
	v_pk_fma_f16 v71, v115, v127, v71
	v_pk_fma_f16 v70, v114, v126, v70
	v_pk_add_f16 v110, v205, v198 neg_lo:[0,1] neg_hi:[0,1]
	v_pk_add_f16 v111, v204, v199 neg_lo:[0,1] neg_hi:[0,1]
	v_pk_add_f16 v112, v203, v200 neg_lo:[0,1] neg_hi:[0,1]
	v_pk_add_f16 v113, v202, v201 neg_lo:[0,1] neg_hi:[0,1]
	v_exp_f16_sdwa v114, v110 dst_sel:WORD_0 dst_unused:UNUSED_PAD src0_sel:WORD_0
	v_exp_f16_sdwa v115, v111 dst_sel:WORD_0 dst_unused:UNUSED_PAD src0_sel:WORD_0
	v_exp_f16_sdwa v116, v112 dst_sel:WORD_0 dst_unused:UNUSED_PAD src0_sel:WORD_0
	v_exp_f16_sdwa v117, v113 dst_sel:WORD_0 dst_unused:UNUSED_PAD src0_sel:WORD_0
	v_exp_f16_sdwa v114, v110 dst_sel:WORD_1 dst_unused:UNUSED_PRESERVE src0_sel:WORD_1
	v_exp_f16_sdwa v115, v111 dst_sel:WORD_1 dst_unused:UNUSED_PRESERVE src0_sel:WORD_1
	v_exp_f16_sdwa v116, v112 dst_sel:WORD_1 dst_unused:UNUSED_PRESERVE src0_sel:WORD_1
	v_exp_f16_sdwa v117, v113 dst_sel:WORD_1 dst_unused:UNUSED_PRESERVE src0_sel:WORD_1
	v_pk_add_f16 v110, v209, v198 neg_lo:[0,1] neg_hi:[0,1]
	v_pk_add_f16 v101, v101, v114
	v_pk_add_f16 v100, v100, v115
	v_pk_add_f16 v99, v99, v116
	s_mov_b64 exec, s[76:77]
	buffer_load_dwordx4 v[130:133], v253, s[16:19], 0 offen
	buffer_load_dwordx4 v[78:81], v253, s[16:19], 0 offen offset:512
	s_mov_b64 exec, -1
	v_pk_add_f16 v98, v98, v117
	v_pk_fma_f16 v70, v42, v114, v70
	v_pk_fma_f16 v71, v43, v115, v71
	v_pk_fma_f16 v72, v44, v116, v72
	v_pk_fma_f16 v73, v45, v117, v73
	v_pk_add_f16 v111, v208, v199 neg_lo:[0,1] neg_hi:[0,1]
	v_pk_add_f16 v112, v207, v200 neg_lo:[0,1] neg_hi:[0,1]
	v_pk_add_f16 v113, v206, v201 neg_lo:[0,1] neg_hi:[0,1]
	v_exp_f16_sdwa v114, v110 dst_sel:WORD_0 dst_unused:UNUSED_PAD src0_sel:WORD_0
	v_exp_f16_sdwa v115, v111 dst_sel:WORD_0 dst_unused:UNUSED_PAD src0_sel:WORD_0
	v_exp_f16_sdwa v116, v112 dst_sel:WORD_0 dst_unused:UNUSED_PAD src0_sel:WORD_0
	v_exp_f16_sdwa v117, v113 dst_sel:WORD_0 dst_unused:UNUSED_PAD src0_sel:WORD_0
	v_exp_f16_sdwa v114, v110 dst_sel:WORD_1 dst_unused:UNUSED_PRESERVE src0_sel:WORD_1
	v_exp_f16_sdwa v115, v111 dst_sel:WORD_1 dst_unused:UNUSED_PRESERVE src0_sel:WORD_1
	v_exp_f16_sdwa v116, v112 dst_sel:WORD_1 dst_unused:UNUSED_PRESERVE src0_sel:WORD_1
	v_exp_f16_sdwa v117, v113 dst_sel:WORD_1 dst_unused:UNUSED_PRESERVE src0_sel:WORD_1
	v_pk_add_f16 v110, v213, v198 neg_lo:[0,1] neg_hi:[0,1]
	v_pk_add_f16 v101, v101, v114
	v_pk_add_f16 v98, v98, v117
	v_pk_add_f16 v99, v99, v116
	v_pk_add_f16 v100, v100, v115
	v_pk_fma_f16 v73, v65, v117, v73
	v_pk_fma_f16 v72, v64, v116, v72
	s_mov_b64 exec, s[70:71]
	buffer_load_dwordx4 v[138:141], v254, s[16:19], 0 offen offset:512
	buffer_load_dwordx4 v[90:93], v254, s[16:19], 0 offen offset:1024
	s_mov_b64 exec, -1
	v_pk_fma_f16 v71, v63, v115, v71
	v_pk_fma_f16 v70, v62, v114, v70
	v_pk_add_f16 v111, v212, v199 neg_lo:[0,1] neg_hi:[0,1]
	v_pk_add_f16 v112, v211, v200 neg_lo:[0,1] neg_hi:[0,1]
	v_pk_add_f16 v113, v210, v201 neg_lo:[0,1] neg_hi:[0,1]
	v_exp_f16_sdwa v114, v110 dst_sel:WORD_0 dst_unused:UNUSED_PAD src0_sel:WORD_0
	v_exp_f16_sdwa v115, v111 dst_sel:WORD_0 dst_unused:UNUSED_PAD src0_sel:WORD_0
	v_exp_f16_sdwa v116, v112 dst_sel:WORD_0 dst_unused:UNUSED_PAD src0_sel:WORD_0
	v_exp_f16_sdwa v117, v113 dst_sel:WORD_0 dst_unused:UNUSED_PAD src0_sel:WORD_0
	v_exp_f16_sdwa v114, v110 dst_sel:WORD_1 dst_unused:UNUSED_PRESERVE src0_sel:WORD_1
	v_exp_f16_sdwa v115, v111 dst_sel:WORD_1 dst_unused:UNUSED_PRESERVE src0_sel:WORD_1
	v_exp_f16_sdwa v116, v112 dst_sel:WORD_1 dst_unused:UNUSED_PRESERVE src0_sel:WORD_1
	v_exp_f16_sdwa v117, v113 dst_sel:WORD_1 dst_unused:UNUSED_PRESERVE src0_sel:WORD_1
	v_pk_add_f16 v110, v190, v198 neg_lo:[0,1] neg_hi:[0,1]
	v_pk_add_f16 v101, v101, v114
	v_pk_add_f16 v100, v100, v115
	v_pk_add_f16 v99, v99, v116
	v_pk_add_f16 v98, v98, v117
	v_pk_fma_f16 v70, v86, v114, v70
	v_pk_fma_f16 v71, v87, v115, v71
	v_pk_fma_f16 v72, v88, v116, v72
	v_pk_fma_f16 v73, v89, v117, v73
	s_mov_b64 exec, s[78:79]
	buffer_load_dwordx4 v[142:145], v254, s[16:19], 0 offen offset:2048
	buffer_load_dwordx4 v[2:5], v254, s[16:19], 0 offen offset:2560
	s_mov_b64 exec, -1
	v_pk_add_f16 v111, v191, v199 neg_lo:[0,1] neg_hi:[0,1]
	v_pk_add_f16 v112, v192, v200 neg_lo:[0,1] neg_hi:[0,1]
	v_pk_add_f16 v113, v193, v201 neg_lo:[0,1] neg_hi:[0,1]
	v_exp_f16_sdwa v114, v110 dst_sel:WORD_0 dst_unused:UNUSED_PAD src0_sel:WORD_0
	v_exp_f16_sdwa v115, v111 dst_sel:WORD_0 dst_unused:UNUSED_PAD src0_sel:WORD_0
	v_exp_f16_sdwa v116, v112 dst_sel:WORD_0 dst_unused:UNUSED_PAD src0_sel:WORD_0
	v_exp_f16_sdwa v117, v113 dst_sel:WORD_0 dst_unused:UNUSED_PAD src0_sel:WORD_0
	v_exp_f16_sdwa v114, v110 dst_sel:WORD_1 dst_unused:UNUSED_PRESERVE src0_sel:WORD_1
	v_exp_f16_sdwa v115, v111 dst_sel:WORD_1 dst_unused:UNUSED_PRESERVE src0_sel:WORD_1
	v_exp_f16_sdwa v116, v112 dst_sel:WORD_1 dst_unused:UNUSED_PRESERVE src0_sel:WORD_1
	v_exp_f16_sdwa v117, v113 dst_sel:WORD_1 dst_unused:UNUSED_PRESERVE src0_sel:WORD_1
	v_pk_add_f16 v110, v194, v198 neg_lo:[0,1] neg_hi:[0,1]
	v_pk_add_f16 v101, v101, v114
	v_pk_add_f16 v98, v98, v117
	v_pk_add_f16 v99, v99, v116
	v_pk_add_f16 v100, v100, v115
	v_pk_fma_f16 v73, v25, v117, v73
	v_pk_fma_f16 v72, v24, v116, v72
	v_pk_fma_f16 v71, v23, v115, v71
	v_pk_fma_f16 v70, v22, v114, v70
	v_pk_add_f16 v111, v195, v199 neg_lo:[0,1] neg_hi:[0,1]
	v_pk_add_f16 v112, v196, v200 neg_lo:[0,1] neg_hi:[0,1]
	v_pk_add_f16 v113, v197, v201 neg_lo:[0,1] neg_hi:[0,1]
	v_exp_f16_sdwa v114, v110 dst_sel:WORD_0 dst_unused:UNUSED_PAD src0_sel:WORD_0
	v_exp_f16_sdwa v115, v111 dst_sel:WORD_0 dst_unused:UNUSED_PAD src0_sel:WORD_0
	v_exp_f16_sdwa v116, v112 dst_sel:WORD_0 dst_unused:UNUSED_PAD src0_sel:WORD_0
	v_exp_f16_sdwa v117, v113 dst_sel:WORD_0 dst_unused:UNUSED_PAD src0_sel:WORD_0
	v_exp_f16_sdwa v114, v110 dst_sel:WORD_1 dst_unused:UNUSED_PRESERVE src0_sel:WORD_1
	v_exp_f16_sdwa v115, v111 dst_sel:WORD_1 dst_unused:UNUSED_PRESERVE src0_sel:WORD_1
	v_exp_f16_sdwa v116, v112 dst_sel:WORD_1 dst_unused:UNUSED_PRESERVE src0_sel:WORD_1
	v_exp_f16_sdwa v117, v113 dst_sel:WORD_1 dst_unused:UNUSED_PRESERVE src0_sel:WORD_1
	v_pk_add_f16 v110, v186, v198 neg_lo:[0,1] neg_hi:[0,1]
	v_pk_add_f16 v101, v101, v114
	v_pk_add_f16 v100, v100, v115
	v_pk_add_f16 v99, v99, v116
	v_pk_add_f16 v98, v98, v117
	v_pk_fma_f16 v70, v30, v114, v70
	v_pk_fma_f16 v71, v31, v115, v71
	v_pk_fma_f16 v72, v32, v116, v72
	v_pk_fma_f16 v73, v33, v117, v73
	v_pk_add_f16 v111, v187, v199 neg_lo:[0,1] neg_hi:[0,1]
	v_pk_add_f16 v112, v188, v200 neg_lo:[0,1] neg_hi:[0,1]
	v_pk_add_f16 v113, v189, v201 neg_lo:[0,1] neg_hi:[0,1]
	v_exp_f16_sdwa v114, v110 dst_sel:WORD_0 dst_unused:UNUSED_PAD src0_sel:WORD_0
	v_exp_f16_sdwa v115, v111 dst_sel:WORD_0 dst_unused:UNUSED_PAD src0_sel:WORD_0
	v_exp_f16_sdwa v116, v112 dst_sel:WORD_0 dst_unused:UNUSED_PAD src0_sel:WORD_0
	v_exp_f16_sdwa v117, v113 dst_sel:WORD_0 dst_unused:UNUSED_PAD src0_sel:WORD_0
	v_exp_f16_sdwa v114, v110 dst_sel:WORD_1 dst_unused:UNUSED_PRESERVE src0_sel:WORD_1
	v_exp_f16_sdwa v115, v111 dst_sel:WORD_1 dst_unused:UNUSED_PRESERVE src0_sel:WORD_1
	v_exp_f16_sdwa v116, v112 dst_sel:WORD_1 dst_unused:UNUSED_PRESERVE src0_sel:WORD_1
	v_exp_f16_sdwa v117, v113 dst_sel:WORD_1 dst_unused:UNUSED_PRESERVE src0_sel:WORD_1
	v_pk_add_f16 v101, v101, v114
	v_pk_add_f16 v100, v100, v115
	v_rcp_f16_e32 v110, v101
	v_rcp_f16_sdwa v101, v101 dst_sel:DWORD dst_unused:UNUSED_PAD src0_sel:WORD_1
	v_pk_add_f16 v99, v99, v116
	v_rcp_f16_e32 v111, v100
	v_rcp_f16_sdwa v100, v100 dst_sel:DWORD dst_unused:UNUSED_PAD src0_sel:WORD_1
	v_pk_add_f16 v98, v98, v117
	v_rcp_f16_e32 v112, v99
	v_rcp_f16_sdwa v99, v99 dst_sel:DWORD dst_unused:UNUSED_PAD src0_sel:WORD_1
	v_rcp_f16_e32 v113, v98
	v_rcp_f16_sdwa v98, v98 dst_sel:DWORD dst_unused:UNUSED_PAD src0_sel:WORD_1
	v_pk_fma_f16 v70, v46, v114, v70
	v_pack_b32_f16 v101, v110, v101
	v_pk_fma_f16 v71, v47, v115, v71
	v_pk_mul_f16 v110, v70, v101
	v_pack_b32_f16 v70, v111, v100
	v_pk_fma_f16 v72, v48, v116, v72
	v_pk_mul_f16 v111, v71, v70
	v_pack_b32_f16 v70, v112, v99
	v_pk_fma_f16 v73, v49, v117, v73
	v_pk_mul_f16 v112, v72, v70
	v_pack_b32_f16 v70, v113, v98
	v_pk_mul_f16 v113, v73, v70
	s_waitcnt vmcnt(12)
	v_pk_mul_f16 v73, v185, v157 op_sel_hi:[0,1]
	v_pk_mul_f16 v101, v183, v157 op_sel_hi:[0,1]
	v_pk_mul_f16 v117, v184, v157 op_sel_hi:[0,1]
	v_pk_mul_f16 v70, v185, v154 op_sel_hi:[0,1]
	v_pk_mul_f16 v71, v185, v155 op_sel_hi:[0,1]
	v_pk_mul_f16 v72, v185, v156 op_sel_hi:[0,1]
	v_pk_mul_f16 v98, v183, v154 op_sel_hi:[0,1]
	v_pk_mul_f16 v99, v183, v155 op_sel_hi:[0,1]
	v_pk_mul_f16 v100, v183, v156 op_sel_hi:[0,1]
	v_pk_mul_f16 v114, v184, v154 op_sel_hi:[0,1]
	v_pk_mul_f16 v115, v184, v155 op_sel_hi:[0,1]
	v_pk_mul_f16 v116, v184, v156 op_sel_hi:[0,1]
	v_pk_fma_f16 v85, v85, v157, v73
	v_pk_fma_f16 v109, v109, v157, v101
	v_pk_fma_f16 v125, v125, v157, v117
	v_pk_fma_f16 v126, v53, v157, v73
	v_pk_fma_f16 v134, v69, v157, v101
	v_pk_fma_f16 v186, v97, v157, v117
	v_pk_fma_f16 v73, v21, v157, v73
	v_pk_fma_f16 v101, v37, v157, v101
	v_pk_fma_f16 v117, v57, v157, v117
	v_pk_maximum3_f16 v157, v85, v109, v125
	v_pk_fma_f16 v84, v84, v156, v72
	v_pk_fma_f16 v83, v83, v155, v71
	v_pk_fma_f16 v82, v82, v154, v70
	v_pk_fma_f16 v108, v108, v156, v100
	v_pk_fma_f16 v107, v107, v155, v99
	v_pk_fma_f16 v106, v106, v154, v98
	v_pk_fma_f16 v124, v124, v156, v116
	v_pk_fma_f16 v123, v123, v155, v115
	v_pk_fma_f16 v122, v122, v154, v114
	v_pk_fma_f16 v127, v52, v156, v72
	v_pk_fma_f16 v128, v51, v155, v71
	v_pk_fma_f16 v129, v50, v154, v70
	v_pk_fma_f16 v135, v68, v156, v100
	v_pk_fma_f16 v136, v67, v155, v99
	v_pk_fma_f16 v137, v66, v154, v98
	v_pk_fma_f16 v187, v96, v156, v116
	v_pk_fma_f16 v188, v95, v155, v115
	v_pk_fma_f16 v189, v94, v154, v114
	v_pk_fma_f16 v72, v20, v156, v72
	v_pk_fma_f16 v71, v19, v155, v71
	v_pk_fma_f16 v70, v18, v154, v70
	v_pk_fma_f16 v100, v36, v156, v100
	v_pk_fma_f16 v99, v35, v155, v99
	v_pk_fma_f16 v98, v34, v154, v98
	v_pk_fma_f16 v116, v56, v156, v116
	v_pk_fma_f16 v115, v55, v155, v115
	v_pk_fma_f16 v114, v54, v154, v114
	v_pk_maximum3_f16 v154, v82, v106, v122
	v_pk_maximum3_f16 v155, v83, v107, v123
	v_pk_maximum3_f16 v156, v84, v108, v124
	v_pk_maximum3_f16 v193, v126, v134, v186
	v_pk_maximum3_f16 v197, v73, v101, v117
	v_pk_maximum3_f16 v190, v129, v137, v189
	v_pk_maximum3_f16 v191, v128, v136, v188
	v_pk_maximum3_f16 v192, v127, v135, v187
	v_pk_maximum3_f16 v194, v70, v98, v114
	v_pk_maximum3_f16 v195, v71, v99, v115
	v_pk_maximum3_f16 v157, v157, v193, v197
	v_pk_maximum3_f16 v196, v72, v100, v116
	v_pk_maximum3_f16 v154, v154, v190, v194
	v_pk_maximum3_f16 v155, v155, v191, v195
	v_pk_maximum3_f16 v156, v156, v192, v196
	v_pk_add_f16 v85, v85, v157 neg_lo:[0,1] neg_hi:[0,1]
	v_pk_add_f16 v82, v82, v154 neg_lo:[0,1] neg_hi:[0,1]
	v_pk_add_f16 v83, v83, v155 neg_lo:[0,1] neg_hi:[0,1]
	v_pk_add_f16 v84, v84, v156 neg_lo:[0,1] neg_hi:[0,1]
	v_pk_add_f16 v106, v106, v154 neg_lo:[0,1] neg_hi:[0,1]
	v_exp_f16_sdwa v190, v82 dst_sel:WORD_0 dst_unused:UNUSED_PAD src0_sel:WORD_0
	v_exp_f16_sdwa v191, v83 dst_sel:WORD_0 dst_unused:UNUSED_PAD src0_sel:WORD_0
	v_exp_f16_sdwa v192, v84 dst_sel:WORD_0 dst_unused:UNUSED_PAD src0_sel:WORD_0
	v_exp_f16_sdwa v193, v85 dst_sel:WORD_0 dst_unused:UNUSED_PAD src0_sel:WORD_0
	v_exp_f16_sdwa v190, v82 dst_sel:WORD_1 dst_unused:UNUSED_PRESERVE src0_sel:WORD_1
	v_exp_f16_sdwa v191, v83 dst_sel:WORD_1 dst_unused:UNUSED_PRESERVE src0_sel:WORD_1
	v_exp_f16_sdwa v192, v84 dst_sel:WORD_1 dst_unused:UNUSED_PRESERVE src0_sel:WORD_1
	v_exp_f16_sdwa v193, v85 dst_sel:WORD_1 dst_unused:UNUSED_PRESERVE src0_sel:WORD_1
	v_pk_add_f16 v107, v107, v155 neg_lo:[0,1] neg_hi:[0,1]
	v_pk_add_f16 v85, v190, 0
	v_pk_fma_f16 v45, v45, v193, 0
	v_pk_add_f16 v82, v193, 0
	v_pk_add_f16 v83, v192, 0
	v_pk_add_f16 v84, v191, 0
	v_pk_fma_f16 v44, v44, v192, 0
	v_pk_fma_f16 v43, v43, v191, 0
	v_pk_fma_f16 v42, v42, v190, 0
	v_pk_add_f16 v108, v108, v156 neg_lo:[0,1] neg_hi:[0,1]
	v_pk_add_f16 v109, v109, v157 neg_lo:[0,1] neg_hi:[0,1]
	v_pk_add_f16 v70, v70, v154 neg_lo:[0,1] neg_hi:[0,1]
	v_exp_f16_sdwa v190, v106 dst_sel:WORD_0 dst_unused:UNUSED_PAD src0_sel:WORD_0
	v_exp_f16_sdwa v191, v107 dst_sel:WORD_0 dst_unused:UNUSED_PAD src0_sel:WORD_0
	v_exp_f16_sdwa v192, v108 dst_sel:WORD_0 dst_unused:UNUSED_PAD src0_sel:WORD_0
	v_exp_f16_sdwa v193, v109 dst_sel:WORD_0 dst_unused:UNUSED_PAD src0_sel:WORD_0
	v_exp_f16_sdwa v190, v106 dst_sel:WORD_1 dst_unused:UNUSED_PRESERVE src0_sel:WORD_1
	v_exp_f16_sdwa v191, v107 dst_sel:WORD_1 dst_unused:UNUSED_PRESERVE src0_sel:WORD_1
	v_exp_f16_sdwa v192, v108 dst_sel:WORD_1 dst_unused:UNUSED_PRESERVE src0_sel:WORD_1
	v_exp_f16_sdwa v193, v109 dst_sel:WORD_1 dst_unused:UNUSED_PRESERVE src0_sel:WORD_1
	v_pk_add_f16 v71, v71, v155 neg_lo:[0,1] neg_hi:[0,1]
	v_pk_add_f16 v85, v85, v190
	v_pk_fma_f16 v45, v65, v193, v45
	v_pk_add_f16 v65, v125, v157 neg_lo:[0,1] neg_hi:[0,1]
	v_pk_add_f16 v84, v84, v191
	v_pk_add_f16 v83, v83, v192
	v_pk_add_f16 v82, v82, v193
	v_pk_fma_f16 v42, v62, v190, v42
	v_pk_fma_f16 v43, v63, v191, v43
	v_pk_fma_f16 v44, v64, v192, v44
	v_pk_add_f16 v62, v122, v154 neg_lo:[0,1] neg_hi:[0,1]
	v_pk_add_f16 v63, v123, v155 neg_lo:[0,1] neg_hi:[0,1]
	v_pk_add_f16 v64, v124, v156 neg_lo:[0,1] neg_hi:[0,1]
	v_pk_add_f16 v72, v72, v156 neg_lo:[0,1] neg_hi:[0,1]
	v_exp_f16_sdwa v106, v62 dst_sel:WORD_0 dst_unused:UNUSED_PAD src0_sel:WORD_0
	v_exp_f16_sdwa v107, v63 dst_sel:WORD_0 dst_unused:UNUSED_PAD src0_sel:WORD_0
	v_exp_f16_sdwa v108, v64 dst_sel:WORD_0 dst_unused:UNUSED_PAD src0_sel:WORD_0
	v_exp_f16_sdwa v109, v65 dst_sel:WORD_0 dst_unused:UNUSED_PAD src0_sel:WORD_0
	v_exp_f16_sdwa v106, v62 dst_sel:WORD_1 dst_unused:UNUSED_PRESERVE src0_sel:WORD_1
	v_exp_f16_sdwa v107, v63 dst_sel:WORD_1 dst_unused:UNUSED_PRESERVE src0_sel:WORD_1
	v_exp_f16_sdwa v108, v64 dst_sel:WORD_1 dst_unused:UNUSED_PRESERVE src0_sel:WORD_1
	v_exp_f16_sdwa v109, v65 dst_sel:WORD_1 dst_unused:UNUSED_PRESERVE src0_sel:WORD_1
	v_pk_add_f16 v73, v73, v157 neg_lo:[0,1] neg_hi:[0,1]
	v_pk_add_f16 v65, v85, v106
	v_pk_add_f16 v62, v82, v109
	v_pk_add_f16 v63, v83, v108
	v_pk_add_f16 v64, v84, v107
	v_pk_fma_f16 v45, v89, v109, v45
	v_pk_fma_f16 v44, v88, v108, v44
	v_pk_fma_f16 v43, v87, v107, v43
	v_pk_fma_f16 v42, v86, v106, v42
	v_pk_add_f16 v82, v129, v154 neg_lo:[0,1] neg_hi:[0,1]
	v_pk_add_f16 v83, v128, v155 neg_lo:[0,1] neg_hi:[0,1]
	v_pk_add_f16 v84, v127, v156 neg_lo:[0,1] neg_hi:[0,1]
	v_pk_add_f16 v85, v126, v157 neg_lo:[0,1] neg_hi:[0,1]
	v_exp_f16_sdwa v86, v82 dst_sel:WORD_0 dst_unused:UNUSED_PAD src0_sel:WORD_0
	v_exp_f16_sdwa v87, v83 dst_sel:WORD_0 dst_unused:UNUSED_PAD src0_sel:WORD_0
	v_exp_f16_sdwa v88, v84 dst_sel:WORD_0 dst_unused:UNUSED_PAD src0_sel:WORD_0
	v_exp_f16_sdwa v89, v85 dst_sel:WORD_0 dst_unused:UNUSED_PAD src0_sel:WORD_0
	v_exp_f16_sdwa v86, v82 dst_sel:WORD_1 dst_unused:UNUSED_PRESERVE src0_sel:WORD_1
	v_exp_f16_sdwa v87, v83 dst_sel:WORD_1 dst_unused:UNUSED_PRESERVE src0_sel:WORD_1
	v_exp_f16_sdwa v88, v84 dst_sel:WORD_1 dst_unused:UNUSED_PRESERVE src0_sel:WORD_1
	v_exp_f16_sdwa v89, v85 dst_sel:WORD_1 dst_unused:UNUSED_PRESERVE src0_sel:WORD_1
	v_pk_add_f16 v82, v137, v154 neg_lo:[0,1] neg_hi:[0,1]
	v_pk_add_f16 v65, v65, v86
	v_pk_add_f16 v64, v64, v87
	v_pk_add_f16 v63, v63, v88
	v_pk_add_f16 v62, v62, v89
	v_pk_fma_f16 v42, v22, v86, v42
	v_pk_fma_f16 v43, v23, v87, v43
	v_pk_fma_f16 v44, v24, v88, v44
	v_pk_fma_f16 v45, v25, v89, v45
	v_pk_add_f16 v83, v136, v155 neg_lo:[0,1] neg_hi:[0,1]
	v_pk_add_f16 v84, v135, v156 neg_lo:[0,1] neg_hi:[0,1]
	v_pk_add_f16 v85, v134, v157 neg_lo:[0,1] neg_hi:[0,1]
	v_exp_f16_sdwa v86, v82 dst_sel:WORD_0 dst_unused:UNUSED_PAD src0_sel:WORD_0
	v_exp_f16_sdwa v87, v83 dst_sel:WORD_0 dst_unused:UNUSED_PAD src0_sel:WORD_0
	v_exp_f16_sdwa v88, v84 dst_sel:WORD_0 dst_unused:UNUSED_PAD src0_sel:WORD_0
	v_exp_f16_sdwa v89, v85 dst_sel:WORD_0 dst_unused:UNUSED_PAD src0_sel:WORD_0
	v_exp_f16_sdwa v86, v82 dst_sel:WORD_1 dst_unused:UNUSED_PRESERVE src0_sel:WORD_1
	v_exp_f16_sdwa v87, v83 dst_sel:WORD_1 dst_unused:UNUSED_PRESERVE src0_sel:WORD_1
	v_exp_f16_sdwa v88, v84 dst_sel:WORD_1 dst_unused:UNUSED_PRESERVE src0_sel:WORD_1
	v_exp_f16_sdwa v89, v85 dst_sel:WORD_1 dst_unused:UNUSED_PRESERVE src0_sel:WORD_1
	v_pk_add_f16 v82, v189, v154 neg_lo:[0,1] neg_hi:[0,1]
	v_pk_add_f16 v65, v65, v86
	v_pk_add_f16 v62, v62, v89
	v_pk_add_f16 v63, v63, v88
	v_pk_add_f16 v64, v64, v87
	v_pk_fma_f16 v45, v33, v89, v45
	v_pk_fma_f16 v44, v32, v88, v44
	v_pk_fma_f16 v43, v31, v87, v43
	v_pk_fma_f16 v42, v30, v86, v42
	v_pk_add_f16 v83, v188, v155 neg_lo:[0,1] neg_hi:[0,1]
	v_pk_add_f16 v84, v187, v156 neg_lo:[0,1] neg_hi:[0,1]
	v_pk_add_f16 v85, v186, v157 neg_lo:[0,1] neg_hi:[0,1]
	v_exp_f16_sdwa v86, v82 dst_sel:WORD_0 dst_unused:UNUSED_PAD src0_sel:WORD_0
	v_exp_f16_sdwa v87, v83 dst_sel:WORD_0 dst_unused:UNUSED_PAD src0_sel:WORD_0
	v_exp_f16_sdwa v88, v84 dst_sel:WORD_0 dst_unused:UNUSED_PAD src0_sel:WORD_0
	v_exp_f16_sdwa v89, v85 dst_sel:WORD_0 dst_unused:UNUSED_PAD src0_sel:WORD_0
	v_exp_f16_sdwa v86, v82 dst_sel:WORD_1 dst_unused:UNUSED_PRESERVE src0_sel:WORD_1
	v_exp_f16_sdwa v87, v83 dst_sel:WORD_1 dst_unused:UNUSED_PRESERVE src0_sel:WORD_1
	v_exp_f16_sdwa v88, v84 dst_sel:WORD_1 dst_unused:UNUSED_PRESERVE src0_sel:WORD_1
	v_exp_f16_sdwa v89, v85 dst_sel:WORD_1 dst_unused:UNUSED_PRESERVE src0_sel:WORD_1
	v_exp_f16_sdwa v82, v70 dst_sel:WORD_0 dst_unused:UNUSED_PAD src0_sel:WORD_0
	v_exp_f16_sdwa v83, v71 dst_sel:WORD_0 dst_unused:UNUSED_PAD src0_sel:WORD_0
	v_exp_f16_sdwa v84, v72 dst_sel:WORD_0 dst_unused:UNUSED_PAD src0_sel:WORD_0
	v_exp_f16_sdwa v85, v73 dst_sel:WORD_0 dst_unused:UNUSED_PAD src0_sel:WORD_0
	v_exp_f16_sdwa v82, v70 dst_sel:WORD_1 dst_unused:UNUSED_PRESERVE src0_sel:WORD_1
	v_exp_f16_sdwa v83, v71 dst_sel:WORD_1 dst_unused:UNUSED_PRESERVE src0_sel:WORD_1
	v_exp_f16_sdwa v84, v72 dst_sel:WORD_1 dst_unused:UNUSED_PRESERVE src0_sel:WORD_1
	v_exp_f16_sdwa v85, v73 dst_sel:WORD_1 dst_unused:UNUSED_PRESERVE src0_sel:WORD_1
	v_pk_add_f16 v70, v98, v154 neg_lo:[0,1] neg_hi:[0,1]
	v_pk_add_f16 v65, v65, v86
	v_pk_add_f16 v64, v64, v87
	v_pk_add_f16 v63, v63, v88
	v_pk_add_f16 v62, v62, v89
	v_pk_fma_f16 v42, v46, v86, v42
	v_pk_fma_f16 v43, v47, v87, v43
	v_pk_fma_f16 v44, v48, v88, v44
	v_pk_fma_f16 v45, v49, v89, v45
	v_pk_add_f16 v65, v65, v82
	v_pk_add_f16 v62, v62, v85
	v_pk_add_f16 v63, v63, v84
	v_pk_add_f16 v64, v64, v83
	v_pk_fma_f16 v45, v9, v85, v45
	v_pk_fma_f16 v44, v8, v84, v44
	v_pk_fma_f16 v43, v7, v83, v43
	v_pk_fma_f16 v42, v6, v82, v42
	v_pk_add_f16 v71, v99, v155 neg_lo:[0,1] neg_hi:[0,1]
	v_pk_add_f16 v72, v100, v156 neg_lo:[0,1] neg_hi:[0,1]
	v_pk_add_f16 v73, v101, v157 neg_lo:[0,1] neg_hi:[0,1]
	v_exp_f16_sdwa v82, v70 dst_sel:WORD_0 dst_unused:UNUSED_PAD src0_sel:WORD_0
	v_exp_f16_sdwa v83, v71 dst_sel:WORD_0 dst_unused:UNUSED_PAD src0_sel:WORD_0
	v_exp_f16_sdwa v84, v72 dst_sel:WORD_0 dst_unused:UNUSED_PAD src0_sel:WORD_0
	v_exp_f16_sdwa v85, v73 dst_sel:WORD_0 dst_unused:UNUSED_PAD src0_sel:WORD_0
	v_exp_f16_sdwa v82, v70 dst_sel:WORD_1 dst_unused:UNUSED_PRESERVE src0_sel:WORD_1
	v_exp_f16_sdwa v83, v71 dst_sel:WORD_1 dst_unused:UNUSED_PRESERVE src0_sel:WORD_1
	v_exp_f16_sdwa v84, v72 dst_sel:WORD_1 dst_unused:UNUSED_PRESERVE src0_sel:WORD_1
	v_exp_f16_sdwa v85, v73 dst_sel:WORD_1 dst_unused:UNUSED_PRESERVE src0_sel:WORD_1
	v_pk_add_f16 v70, v114, v154 neg_lo:[0,1] neg_hi:[0,1]
	v_pk_add_f16 v65, v65, v82
	v_pk_add_f16 v64, v64, v83
	v_pk_add_f16 v63, v63, v84
	v_pk_add_f16 v62, v62, v85
	v_pk_fma_f16 v42, v10, v82, v42
	v_pk_fma_f16 v43, v11, v83, v43
	v_pk_fma_f16 v44, v12, v84, v44
	v_pk_fma_f16 v45, v13, v85, v45
	v_pk_add_f16 v71, v115, v155 neg_lo:[0,1] neg_hi:[0,1]
	v_pk_add_f16 v72, v116, v156 neg_lo:[0,1] neg_hi:[0,1]
	v_pk_add_f16 v73, v117, v157 neg_lo:[0,1] neg_hi:[0,1]
	v_exp_f16_sdwa v82, v70 dst_sel:WORD_0 dst_unused:UNUSED_PAD src0_sel:WORD_0
	v_exp_f16_sdwa v83, v71 dst_sel:WORD_0 dst_unused:UNUSED_PAD src0_sel:WORD_0
	v_exp_f16_sdwa v84, v72 dst_sel:WORD_0 dst_unused:UNUSED_PAD src0_sel:WORD_0
	v_exp_f16_sdwa v85, v73 dst_sel:WORD_0 dst_unused:UNUSED_PAD src0_sel:WORD_0
	v_exp_f16_sdwa v82, v70 dst_sel:WORD_1 dst_unused:UNUSED_PRESERVE src0_sel:WORD_1
	v_exp_f16_sdwa v83, v71 dst_sel:WORD_1 dst_unused:UNUSED_PRESERVE src0_sel:WORD_1
	v_exp_f16_sdwa v84, v72 dst_sel:WORD_1 dst_unused:UNUSED_PRESERVE src0_sel:WORD_1
	v_exp_f16_sdwa v85, v73 dst_sel:WORD_1 dst_unused:UNUSED_PRESERVE src0_sel:WORD_1
	v_pk_add_f16 v65, v65, v82
	v_pk_add_f16 v64, v64, v83
	v_rcp_f16_e32 v70, v65
	v_rcp_f16_sdwa v65, v65 dst_sel:DWORD dst_unused:UNUSED_PAD src0_sel:WORD_1
	v_pk_add_f16 v63, v63, v84
	v_rcp_f16_e32 v71, v64
	v_rcp_f16_sdwa v64, v64 dst_sel:DWORD dst_unused:UNUSED_PAD src0_sel:WORD_1
	v_pk_add_f16 v62, v62, v85
	v_rcp_f16_e32 v72, v63
	v_rcp_f16_sdwa v73, v63 dst_sel:DWORD dst_unused:UNUSED_PAD src0_sel:WORD_1
	v_pk_fma_f16 v43, v15, v83, v43
	v_pk_fma_f16 v42, v14, v82, v42
	v_rcp_f16_e32 v82, v62
	v_rcp_f16_sdwa v83, v62 dst_sel:DWORD dst_unused:UNUSED_PAD src0_sel:WORD_1
	v_pack_b32_f16 v62, v70, v65
	v_pk_mul_f16 v62, v42, v62
	v_pack_b32_f16 v42, v71, v64
	v_pk_fma_f16 v44, v16, v84, v44
	v_pk_mul_f16 v63, v43, v42
	v_pack_b32_f16 v42, v72, v73
	v_pk_fma_f16 v45, v17, v85, v45
	v_pk_mul_f16 v64, v44, v42
	v_pack_b32_f16 v42, v82, v83
	v_pk_mul_f16 v65, v45, v42
	s_waitcnt vmcnt(6)
	v_pk_mul_f16 v42, v185, v150 op_sel_hi:[0,1]
	v_pk_mul_f16 v70, v183, v150 op_sel_hi:[0,1]
	v_pk_mul_f16 v82, v184, v150 op_sel_hi:[0,1]
	v_pk_mul_f16 v43, v185, v151 op_sel_hi:[0,1]
	v_pk_mul_f16 v44, v185, v152 op_sel_hi:[0,1]
	v_pk_mul_f16 v45, v185, v153 op_sel_hi:[0,1]
	v_pk_mul_f16 v71, v183, v151 op_sel_hi:[0,1]
	v_pk_mul_f16 v72, v183, v152 op_sel_hi:[0,1]
	v_pk_mul_f16 v73, v183, v153 op_sel_hi:[0,1]
	v_pk_mul_f16 v83, v184, v151 op_sel_hi:[0,1]
	v_pk_mul_f16 v84, v184, v152 op_sel_hi:[0,1]
	v_pk_mul_f16 v85, v184, v153 op_sel_hi:[0,1]
	v_pk_fma_f16 v50, v50, v150, v42
	v_pk_fma_f16 v66, v66, v150, v70
	v_pk_fma_f16 v89, v94, v150, v82
	v_pk_fma_f16 v53, v53, v153, v45
	v_pk_maximum3_f16 v114, v50, v66, v89
	v_pk_fma_f16 v52, v52, v152, v44
	v_pk_fma_f16 v51, v51, v151, v43
	v_pk_fma_f16 v69, v69, v153, v73
	v_pk_fma_f16 v68, v68, v152, v72
	v_pk_fma_f16 v67, v67, v151, v71
	v_pk_fma_f16 v86, v97, v153, v85
	v_pk_fma_f16 v87, v96, v152, v84
	v_pk_fma_f16 v88, v95, v151, v83
	v_pk_fma_f16 v97, v18, v150, v42
	v_pk_fma_f16 v101, v34, v150, v70
	v_pk_fma_f16 v109, v54, v150, v82
	v_pk_fma_f16 v42, v74, v150, v42
	v_pk_fma_f16 v70, v102, v150, v70
	v_pk_fma_f16 v82, v118, v150, v82
	v_pk_maximum3_f16 v115, v51, v67, v88
	v_pk_maximum3_f16 v116, v52, v68, v87
	v_pk_maximum3_f16 v117, v53, v69, v86
	v_pk_maximum3_f16 v122, v97, v101, v109
	v_pk_fma_f16 v94, v21, v153, v45
	v_pk_maximum3_f16 v126, v42, v70, v82
	v_pk_fma_f16 v95, v20, v152, v44
	v_pk_maximum3_f16 v114, v114, v122, v126
	v_pk_fma_f16 v96, v19, v151, v43
	v_pk_fma_f16 v98, v37, v153, v73
	v_pk_fma_f16 v99, v36, v152, v72
	v_pk_fma_f16 v100, v35, v151, v71
	v_pk_fma_f16 v106, v57, v153, v85
	v_pk_fma_f16 v107, v56, v152, v84
	v_pk_fma_f16 v108, v55, v151, v83
	v_pk_fma_f16 v45, v77, v153, v45
	v_pk_fma_f16 v44, v76, v152, v44
	v_pk_fma_f16 v43, v75, v151, v43
	v_pk_fma_f16 v73, v105, v153, v73
	v_pk_fma_f16 v72, v104, v152, v72
	v_pk_fma_f16 v71, v103, v151, v71
	v_pk_fma_f16 v85, v121, v153, v85
	v_pk_fma_f16 v84, v120, v152, v84
	v_pk_fma_f16 v83, v119, v151, v83
	v_pk_maximum3_f16 v123, v96, v100, v108
	v_pk_maximum3_f16 v124, v95, v99, v107
	v_pk_maximum3_f16 v125, v94, v98, v106
	v_pk_maximum3_f16 v128, v44, v72, v84
	v_pk_maximum3_f16 v129, v45, v73, v85
	v_pk_maximum3_f16 v127, v43, v71, v83
	v_pk_maximum3_f16 v115, v115, v123, v127
	v_pk_maximum3_f16 v116, v116, v124, v128
	v_pk_maximum3_f16 v117, v117, v125, v129
	v_pk_add_f16 v50, v50, v114 neg_lo:[0,1] neg_hi:[0,1]
	v_pk_add_f16 v51, v51, v115 neg_lo:[0,1] neg_hi:[0,1]
	v_pk_add_f16 v52, v52, v116 neg_lo:[0,1] neg_hi:[0,1]
	v_pk_add_f16 v53, v53, v117 neg_lo:[0,1] neg_hi:[0,1]
	v_pk_add_f16 v66, v66, v114 neg_lo:[0,1] neg_hi:[0,1]
	v_exp_f16_sdwa v122, v50 dst_sel:WORD_0 dst_unused:UNUSED_PAD src0_sel:WORD_0
	v_exp_f16_sdwa v123, v51 dst_sel:WORD_0 dst_unused:UNUSED_PAD src0_sel:WORD_0
	v_exp_f16_sdwa v124, v52 dst_sel:WORD_0 dst_unused:UNUSED_PAD src0_sel:WORD_0
	v_exp_f16_sdwa v125, v53 dst_sel:WORD_0 dst_unused:UNUSED_PAD src0_sel:WORD_0
	v_exp_f16_sdwa v122, v50 dst_sel:WORD_1 dst_unused:UNUSED_PRESERVE src0_sel:WORD_1
	v_exp_f16_sdwa v123, v51 dst_sel:WORD_1 dst_unused:UNUSED_PRESERVE src0_sel:WORD_1
	v_exp_f16_sdwa v124, v52 dst_sel:WORD_1 dst_unused:UNUSED_PRESERVE src0_sel:WORD_1
	v_exp_f16_sdwa v125, v53 dst_sel:WORD_1 dst_unused:UNUSED_PRESERVE src0_sel:WORD_1
	v_pk_add_f16 v67, v67, v115 neg_lo:[0,1] neg_hi:[0,1]
	v_pk_add_f16 v50, v125, 0
	v_pk_fma_f16 v22, v22, v122, 0
	v_pk_add_f16 v51, v124, 0
	v_pk_add_f16 v52, v123, 0
	v_pk_add_f16 v53, v122, 0
	v_pk_fma_f16 v23, v23, v123, 0
	v_pk_fma_f16 v24, v24, v124, 0
	v_pk_fma_f16 v25, v25, v125, 0
	v_pk_add_f16 v68, v68, v116 neg_lo:[0,1] neg_hi:[0,1]
	v_pk_add_f16 v69, v69, v117 neg_lo:[0,1] neg_hi:[0,1]
	v_pk_add_f16 v42, v42, v114 neg_lo:[0,1] neg_hi:[0,1]
	v_exp_f16_sdwa v122, v66 dst_sel:WORD_0 dst_unused:UNUSED_PAD src0_sel:WORD_0
	v_exp_f16_sdwa v123, v67 dst_sel:WORD_0 dst_unused:UNUSED_PAD src0_sel:WORD_0
	v_exp_f16_sdwa v124, v68 dst_sel:WORD_0 dst_unused:UNUSED_PAD src0_sel:WORD_0
	v_exp_f16_sdwa v125, v69 dst_sel:WORD_0 dst_unused:UNUSED_PAD src0_sel:WORD_0
	v_exp_f16_sdwa v122, v66 dst_sel:WORD_1 dst_unused:UNUSED_PRESERVE src0_sel:WORD_1
	v_exp_f16_sdwa v123, v67 dst_sel:WORD_1 dst_unused:UNUSED_PRESERVE src0_sel:WORD_1
	v_exp_f16_sdwa v124, v68 dst_sel:WORD_1 dst_unused:UNUSED_PRESERVE src0_sel:WORD_1
	v_exp_f16_sdwa v125, v69 dst_sel:WORD_1 dst_unused:UNUSED_PRESERVE src0_sel:WORD_1
	v_pk_add_f16 v43, v43, v115 neg_lo:[0,1] neg_hi:[0,1]
	v_pk_add_f16 v50, v50, v125
	v_pk_fma_f16 v22, v30, v122, v22
	v_pk_add_f16 v30, v89, v114 neg_lo:[0,1] neg_hi:[0,1]
	v_pk_add_f16 v53, v53, v122
	v_pk_add_f16 v52, v52, v123
	v_pk_add_f16 v51, v51, v124
	v_pk_fma_f16 v25, v33, v125, v25
	v_pk_fma_f16 v24, v32, v124, v24
	v_pk_fma_f16 v23, v31, v123, v23
	v_pk_add_f16 v31, v88, v115 neg_lo:[0,1] neg_hi:[0,1]
	v_pk_add_f16 v32, v87, v116 neg_lo:[0,1] neg_hi:[0,1]
	v_pk_add_f16 v33, v86, v117 neg_lo:[0,1] neg_hi:[0,1]
	v_pk_add_f16 v44, v44, v116 neg_lo:[0,1] neg_hi:[0,1]
	v_exp_f16_sdwa v66, v30 dst_sel:WORD_0 dst_unused:UNUSED_PAD src0_sel:WORD_0
	v_exp_f16_sdwa v67, v31 dst_sel:WORD_0 dst_unused:UNUSED_PAD src0_sel:WORD_0
	v_exp_f16_sdwa v68, v32 dst_sel:WORD_0 dst_unused:UNUSED_PAD src0_sel:WORD_0
	v_exp_f16_sdwa v69, v33 dst_sel:WORD_0 dst_unused:UNUSED_PAD src0_sel:WORD_0
	v_exp_f16_sdwa v66, v30 dst_sel:WORD_1 dst_unused:UNUSED_PRESERVE src0_sel:WORD_1
	v_exp_f16_sdwa v67, v31 dst_sel:WORD_1 dst_unused:UNUSED_PRESERVE src0_sel:WORD_1
	v_exp_f16_sdwa v68, v32 dst_sel:WORD_1 dst_unused:UNUSED_PRESERVE src0_sel:WORD_1
	v_exp_f16_sdwa v69, v33 dst_sel:WORD_1 dst_unused:UNUSED_PRESERVE src0_sel:WORD_1
	v_pk_add_f16 v45, v45, v117 neg_lo:[0,1] neg_hi:[0,1]
	v_pk_add_f16 v30, v50, v69
	v_pk_add_f16 v31, v51, v68
	v_pk_add_f16 v32, v52, v67
	v_pk_add_f16 v33, v53, v66
	v_pk_fma_f16 v22, v46, v66, v22
	v_pk_fma_f16 v23, v47, v67, v23
	v_pk_fma_f16 v24, v48, v68, v24
	v_pk_fma_f16 v25, v49, v69, v25
	v_pk_add_f16 v46, v97, v114 neg_lo:[0,1] neg_hi:[0,1]
	v_pk_add_f16 v47, v96, v115 neg_lo:[0,1] neg_hi:[0,1]
	v_pk_add_f16 v48, v95, v116 neg_lo:[0,1] neg_hi:[0,1]
	v_pk_add_f16 v49, v94, v117 neg_lo:[0,1] neg_hi:[0,1]
	v_exp_f16_sdwa v50, v46 dst_sel:WORD_0 dst_unused:UNUSED_PAD src0_sel:WORD_0
	v_exp_f16_sdwa v51, v47 dst_sel:WORD_0 dst_unused:UNUSED_PAD src0_sel:WORD_0
	v_exp_f16_sdwa v52, v48 dst_sel:WORD_0 dst_unused:UNUSED_PAD src0_sel:WORD_0
	v_exp_f16_sdwa v53, v49 dst_sel:WORD_0 dst_unused:UNUSED_PAD src0_sel:WORD_0
	v_exp_f16_sdwa v50, v46 dst_sel:WORD_1 dst_unused:UNUSED_PRESERVE src0_sel:WORD_1
	v_exp_f16_sdwa v51, v47 dst_sel:WORD_1 dst_unused:UNUSED_PRESERVE src0_sel:WORD_1
	v_exp_f16_sdwa v52, v48 dst_sel:WORD_1 dst_unused:UNUSED_PRESERVE src0_sel:WORD_1
	v_exp_f16_sdwa v53, v49 dst_sel:WORD_1 dst_unused:UNUSED_PRESERVE src0_sel:WORD_1
	v_pk_add_f16 v46, v101, v114 neg_lo:[0,1] neg_hi:[0,1]
	v_pk_add_f16 v30, v30, v53
	v_pk_add_f16 v33, v33, v50
	v_pk_add_f16 v32, v32, v51
	v_pk_add_f16 v31, v31, v52
	v_pk_fma_f16 v25, v9, v53, v25
	v_pk_fma_f16 v24, v8, v52, v24
	v_pk_fma_f16 v23, v7, v51, v23
	v_pk_fma_f16 v22, v6, v50, v22
	v_pk_add_f16 v47, v100, v115 neg_lo:[0,1] neg_hi:[0,1]
	v_pk_add_f16 v48, v99, v116 neg_lo:[0,1] neg_hi:[0,1]
	v_pk_add_f16 v49, v98, v117 neg_lo:[0,1] neg_hi:[0,1]
	v_exp_f16_sdwa v50, v46 dst_sel:WORD_0 dst_unused:UNUSED_PAD src0_sel:WORD_0
	v_exp_f16_sdwa v51, v47 dst_sel:WORD_0 dst_unused:UNUSED_PAD src0_sel:WORD_0
	v_exp_f16_sdwa v52, v48 dst_sel:WORD_0 dst_unused:UNUSED_PAD src0_sel:WORD_0
	v_exp_f16_sdwa v53, v49 dst_sel:WORD_0 dst_unused:UNUSED_PAD src0_sel:WORD_0
	v_exp_f16_sdwa v50, v46 dst_sel:WORD_1 dst_unused:UNUSED_PRESERVE src0_sel:WORD_1
	v_exp_f16_sdwa v51, v47 dst_sel:WORD_1 dst_unused:UNUSED_PRESERVE src0_sel:WORD_1
	v_exp_f16_sdwa v52, v48 dst_sel:WORD_1 dst_unused:UNUSED_PRESERVE src0_sel:WORD_1
	v_exp_f16_sdwa v53, v49 dst_sel:WORD_1 dst_unused:UNUSED_PRESERVE src0_sel:WORD_1
	v_pk_add_f16 v46, v109, v114 neg_lo:[0,1] neg_hi:[0,1]
	v_pk_add_f16 v30, v30, v53
	v_pk_add_f16 v31, v31, v52
	v_pk_add_f16 v32, v32, v51
	v_pk_add_f16 v33, v33, v50
	v_pk_fma_f16 v22, v10, v50, v22
	v_pk_fma_f16 v23, v11, v51, v23
	v_pk_fma_f16 v24, v12, v52, v24
	v_pk_fma_f16 v25, v13, v53, v25
	v_pk_add_f16 v47, v108, v115 neg_lo:[0,1] neg_hi:[0,1]
	v_pk_add_f16 v48, v107, v116 neg_lo:[0,1] neg_hi:[0,1]
	v_pk_add_f16 v49, v106, v117 neg_lo:[0,1] neg_hi:[0,1]
	v_exp_f16_sdwa v50, v46 dst_sel:WORD_0 dst_unused:UNUSED_PAD src0_sel:WORD_0
	v_exp_f16_sdwa v51, v47 dst_sel:WORD_0 dst_unused:UNUSED_PAD src0_sel:WORD_0
	v_exp_f16_sdwa v52, v48 dst_sel:WORD_0 dst_unused:UNUSED_PAD src0_sel:WORD_0
	v_exp_f16_sdwa v53, v49 dst_sel:WORD_0 dst_unused:UNUSED_PAD src0_sel:WORD_0
	v_exp_f16_sdwa v50, v46 dst_sel:WORD_1 dst_unused:UNUSED_PRESERVE src0_sel:WORD_1
	v_exp_f16_sdwa v51, v47 dst_sel:WORD_1 dst_unused:UNUSED_PRESERVE src0_sel:WORD_1
	v_exp_f16_sdwa v52, v48 dst_sel:WORD_1 dst_unused:UNUSED_PRESERVE src0_sel:WORD_1
	v_exp_f16_sdwa v53, v49 dst_sel:WORD_1 dst_unused:UNUSED_PRESERVE src0_sel:WORD_1
	v_exp_f16_sdwa v46, v42 dst_sel:WORD_0 dst_unused:UNUSED_PAD src0_sel:WORD_0
	v_exp_f16_sdwa v47, v43 dst_sel:WORD_0 dst_unused:UNUSED_PAD src0_sel:WORD_0
	v_exp_f16_sdwa v48, v44 dst_sel:WORD_0 dst_unused:UNUSED_PAD src0_sel:WORD_0
	v_exp_f16_sdwa v49, v45 dst_sel:WORD_0 dst_unused:UNUSED_PAD src0_sel:WORD_0
	v_exp_f16_sdwa v46, v42 dst_sel:WORD_1 dst_unused:UNUSED_PRESERVE src0_sel:WORD_1
	v_exp_f16_sdwa v47, v43 dst_sel:WORD_1 dst_unused:UNUSED_PRESERVE src0_sel:WORD_1
	v_exp_f16_sdwa v48, v44 dst_sel:WORD_1 dst_unused:UNUSED_PRESERVE src0_sel:WORD_1
	v_exp_f16_sdwa v49, v45 dst_sel:WORD_1 dst_unused:UNUSED_PRESERVE src0_sel:WORD_1
	v_pk_add_f16 v42, v70, v114 neg_lo:[0,1] neg_hi:[0,1]
	v_pk_add_f16 v30, v30, v53
	v_pk_add_f16 v33, v33, v50
	v_pk_add_f16 v32, v32, v51
	v_pk_add_f16 v31, v31, v52
	v_pk_fma_f16 v25, v17, v53, v25
	v_pk_fma_f16 v24, v16, v52, v24
	v_pk_fma_f16 v23, v15, v51, v23
	v_pk_fma_f16 v22, v14, v50, v22
	v_pk_add_f16 v30, v30, v49
	v_pk_add_f16 v31, v31, v48
	v_pk_add_f16 v32, v32, v47
	v_pk_add_f16 v33, v33, v46
	v_pk_fma_f16 v22, v26, v46, v22
	v_pk_fma_f16 v23, v27, v47, v23
	v_pk_fma_f16 v24, v28, v48, v24
	v_pk_fma_f16 v25, v29, v49, v25
	v_pk_add_f16 v43, v71, v115 neg_lo:[0,1] neg_hi:[0,1]
	v_pk_add_f16 v44, v72, v116 neg_lo:[0,1] neg_hi:[0,1]
	v_pk_add_f16 v45, v73, v117 neg_lo:[0,1] neg_hi:[0,1]
	v_exp_f16_sdwa v46, v42 dst_sel:WORD_0 dst_unused:UNUSED_PAD src0_sel:WORD_0
	v_exp_f16_sdwa v47, v43 dst_sel:WORD_0 dst_unused:UNUSED_PAD src0_sel:WORD_0
	v_exp_f16_sdwa v48, v44 dst_sel:WORD_0 dst_unused:UNUSED_PAD src0_sel:WORD_0
	v_exp_f16_sdwa v49, v45 dst_sel:WORD_0 dst_unused:UNUSED_PAD src0_sel:WORD_0
	v_exp_f16_sdwa v46, v42 dst_sel:WORD_1 dst_unused:UNUSED_PRESERVE src0_sel:WORD_1
	v_exp_f16_sdwa v47, v43 dst_sel:WORD_1 dst_unused:UNUSED_PRESERVE src0_sel:WORD_1
	v_exp_f16_sdwa v48, v44 dst_sel:WORD_1 dst_unused:UNUSED_PRESERVE src0_sel:WORD_1
	v_exp_f16_sdwa v49, v45 dst_sel:WORD_1 dst_unused:UNUSED_PRESERVE src0_sel:WORD_1
	v_pk_add_f16 v42, v82, v114 neg_lo:[0,1] neg_hi:[0,1]
	v_pk_add_f16 v30, v30, v49
	v_pk_add_f16 v33, v33, v46
	v_pk_add_f16 v32, v32, v47
	v_pk_add_f16 v31, v31, v48
	v_pk_fma_f16 v25, v41, v49, v25
	v_pk_fma_f16 v24, v40, v48, v24
	v_pk_fma_f16 v23, v39, v47, v23
	v_pk_fma_f16 v22, v38, v46, v22
	v_pk_add_f16 v43, v83, v115 neg_lo:[0,1] neg_hi:[0,1]
	v_pk_add_f16 v44, v84, v116 neg_lo:[0,1] neg_hi:[0,1]
	v_pk_add_f16 v45, v85, v117 neg_lo:[0,1] neg_hi:[0,1]
	v_exp_f16_sdwa v46, v42 dst_sel:WORD_0 dst_unused:UNUSED_PAD src0_sel:WORD_0
	v_exp_f16_sdwa v47, v43 dst_sel:WORD_0 dst_unused:UNUSED_PAD src0_sel:WORD_0
	v_exp_f16_sdwa v48, v44 dst_sel:WORD_0 dst_unused:UNUSED_PAD src0_sel:WORD_0
	v_exp_f16_sdwa v49, v45 dst_sel:WORD_0 dst_unused:UNUSED_PAD src0_sel:WORD_0
	v_exp_f16_sdwa v46, v42 dst_sel:WORD_1 dst_unused:UNUSED_PRESERVE src0_sel:WORD_1
	v_exp_f16_sdwa v47, v43 dst_sel:WORD_1 dst_unused:UNUSED_PRESERVE src0_sel:WORD_1
	v_exp_f16_sdwa v48, v44 dst_sel:WORD_1 dst_unused:UNUSED_PRESERVE src0_sel:WORD_1
	v_exp_f16_sdwa v49, v45 dst_sel:WORD_1 dst_unused:UNUSED_PRESERVE src0_sel:WORD_1
	s_nop 0
	v_pk_add_f16 v30, v30, v49
	v_pk_add_f16 v31, v31, v48
	v_rcp_f16_e32 v44, v30
	v_rcp_f16_sdwa v30, v30 dst_sel:DWORD dst_unused:UNUSED_PAD src0_sel:WORD_1
	v_pk_add_f16 v32, v32, v47
	v_rcp_f16_e32 v45, v31
	v_rcp_f16_sdwa v31, v31 dst_sel:DWORD dst_unused:UNUSED_PAD src0_sel:WORD_1
	v_pk_add_f16 v33, v33, v46
	v_rcp_f16_e32 v43, v32
	v_rcp_f16_sdwa v32, v32 dst_sel:DWORD dst_unused:UNUSED_PAD src0_sel:WORD_1
	v_rcp_f16_e32 v42, v33
	v_rcp_f16_sdwa v33, v33 dst_sel:DWORD dst_unused:UNUSED_PAD src0_sel:WORD_1
	v_pk_fma_f16 v25, v61, v49, v25
	v_pack_b32_f16 v30, v44, v30
	v_pk_fma_f16 v24, v60, v48, v24
	v_pk_mul_f16 v25, v25, v30
	v_pack_b32_f16 v30, v45, v31
	v_pk_fma_f16 v23, v59, v47, v23
	v_pk_mul_f16 v24, v24, v30
	v_pack_b32_f16 v30, v43, v32
	v_pk_fma_f16 v22, v58, v46, v22
	v_pk_mul_f16 v23, v23, v30
	v_pack_b32_f16 v30, v42, v33
	v_pk_mul_f16 v22, v22, v30
	s_waitcnt vmcnt(0)
	s_cmp_eq_u32 s10, 1
	s_cbranch_scc1 .Lmydt3_0
	v_add_u32_e32 v250, 0x1b400, v171
	v_add_u32_e32 v251, 0x0, v250
	buffer_load_dwordx4 v[252:255], v251, s[16:19], 0 offen
	v_add_u32_e32 v251, 0xfffe7c00, v250
	buffer_load_dwordx4 v[252:255], v251, s[16:19], 0 offen
	v_add_u32_e32 v251, 0xfffe7e00, v250
	buffer_load_dwordx4 v[252:255], v251, s[16:19], 0 offen
	v_add_u32_e32 v251, 0xfffe8200, v250
	buffer_load_dwordx4 v[252:255], v251, s[16:19], 0 offen
	v_add_u32_e32 v251, 0xfffe8400, v250
	buffer_load_dwordx4 v[252:255], v251, s[16:19], 0 offen
	v_add_u32_e32 v251, 0xfffe8800, v250
	buffer_load_dwordx4 v[252:255], v251, s[16:19], 0 offen
	v_add_u32_e32 v251, 0xfffe8a00, v250
	buffer_load_dwordx4 v[252:255], v251, s[16:19], 0 offen
	v_add_u32_e32 v251, 0xfffffc00, v250
	buffer_load_dwordx4 v[252:255], v251, s[16:19], 0 offen
	v_add_u32_e32 v251, 0xfffffe00, v250
	buffer_load_dwordx4 v[252:255], v251, s[16:19], 0 offen
	v_add_u32_e32 v251, 0x200, v250
	buffer_load_dwordx4 v[252:255], v251, s[16:19], 0 offen
	v_add_u32_e32 v251, 0x400, v250
	buffer_load_dwordx4 v[252:255], v251, s[16:19], 0 offen
	v_add_u32_e32 v251, 0x800, v250
	buffer_load_dwordx4 v[252:255], v251, s[16:19], 0 offen
	v_add_u32_e32 v251, 0xa00, v250
	buffer_load_dwordx4 v[252:255], v251, s[16:19], 0 offen
	v_add_u32_e32 v251, 0x17c00, v250
	buffer_load_dwordx4 v[252:255], v251, s[16:19], 0 offen
	v_add_u32_e32 v251, 0x17e00, v250
	buffer_load_dwordx4 v[252:255], v251, s[16:19], 0 offen
	v_add_u32_e32 v251, 0x18200, v250
	buffer_load_dwordx4 v[252:255], v251, s[16:19], 0 offen
	v_add_u32_e32 v251, 0x18400, v250
	buffer_load_dwordx4 v[252:255], v251, s[16:19], 0 offen
	v_add_u32_e32 v251, 0x18800, v250
	buffer_load_dwordx4 v[252:255], v251, s[16:19], 0 offen
	v_add_u32_e32 v251, 0x18a00, v250
	buffer_load_dwordx4 v[252:255], v251, s[16:19], 0 offen
	v_add_u32_e32 v251, 0x18000, v250
	buffer_load_dwordx4 v[252:255], v251, s[16:19], 0 offen
	v_add_u32_e32 v251, 0x30000, v250
	buffer_load_dwordx4 v[252:255], v251, s[16:19], 0 offen
	v_add_u32_e32 v251, 0x48000, v250
	buffer_load_dwordx4 v[252:255], v251, s[16:19], 0 offen

.Lmyf_C1_7:
	s_mov_b64 exec, -1
	s_waitcnt vmcnt(21)
	v_cvt_f16_f32_e32 v202, v155
	v_cvt_f16_f32_e32 v204, v154
	v_cvt_f16_f32_e32 v203, v156
	v_add_u32_e32 v251, 0x48000, v200
	buffer_load_dwordx4 v[154:157], v251, s[36:39], 0 offen
	v_mov_b32_e32 v251, v200
	s_mov_b64 s[4:5], 0
	s_waitcnt vmcnt(3)
	v_pk_mul_f16 v212, v204, v209 op_sel_hi:[0,1]
	v_pk_mul_f16 v216, v202, v209 op_sel_hi:[0,1]
	v_pk_mul_f16 v220, v203, v209 op_sel_hi:[0,1]
	v_pk_mul_f16 v205, v204, v206 op_sel_hi:[0,1]
	v_pk_mul_f16 v210, v204, v207 op_sel_hi:[0,1]
	v_pk_mul_f16 v211, v204, v208 op_sel_hi:[0,1]
	v_pk_mul_f16 v213, v202, v206 op_sel_hi:[0,1]
	s_mov_b64 exec, s[64:65]
	buffer_load_dwordx4 v[34:37], v245, s[36:39], 0 offen
	buffer_load_dwordx4 v[18:21], v245, s[36:39], 0 offen offset:512
	s_mov_b64 exec, -1
	v_pk_mul_f16 v214, v202, v207 op_sel_hi:[0,1]
	v_pk_mul_f16 v215, v202, v208 op_sel_hi:[0,1]
	v_pk_mul_f16 v217, v203, v206 op_sel_hi:[0,1]
	v_pk_mul_f16 v218, v203, v207 op_sel_hi:[0,1]
	v_pk_mul_f16 v219, v203, v208 op_sel_hi:[0,1]
	v_pk_fma_f16 v125, v125, v209, v212
	v_pk_fma_f16 v141, v141, v209, v216
	v_pk_fma_f16 v149, v149, v209, v220
	v_pk_fma_f16 v221, v97, v209, v212
	v_pk_fma_f16 v225, v121, v209, v216
	v_pk_fma_f16 v229, v137, v209, v220
	v_pk_fma_f16 v212, v65, v209, v212
	v_pk_fma_f16 v216, v81, v209, v216
	buffer_load_dwordx4 v[46:49], v246, s[36:39], 0 offen offset:512
	buffer_load_dwordx4 v[22:25], v246, s[36:39], 0 offen offset:1024
	v_pk_fma_f16 v209, v105, v209, v220
	v_pk_maximum3_f16 v220, v125, v141, v149
	v_pk_fma_f16 v124, v124, v208, v211
	v_pk_fma_f16 v123, v123, v207, v210
	v_pk_fma_f16 v122, v122, v206, v205
	v_pk_fma_f16 v140, v140, v208, v215
	v_pk_fma_f16 v139, v139, v207, v214
	v_pk_fma_f16 v138, v138, v206, v213
	v_pk_fma_f16 v148, v148, v208, v219
	v_pk_fma_f16 v147, v147, v207, v218
	v_pk_fma_f16 v146, v146, v206, v217
	v_pk_fma_f16 v222, v96, v208, v211
	v_pk_fma_f16 v223, v95, v207, v210
	v_pk_fma_f16 v224, v94, v206, v205
	v_pk_fma_f16 v226, v120, v208, v215
	v_pk_fma_f16 v227, v119, v207, v214
	s_mov_b64 exec, s[66:67]
	buffer_load_dwordx4 v[66:69], v246, s[36:39], 0 offen offset:2048
	buffer_load_dwordx4 v[26:29], v246, s[36:39], 0 offen offset:2560
	s_mov_b64 exec, -1
	v_pk_fma_f16 v228, v118, v206, v213
	v_pk_fma_f16 v230, v136, v208, v219
	v_pk_fma_f16 v231, v135, v207, v218
	v_pk_fma_f16 v232, v134, v206, v217
	v_pk_fma_f16 v211, v64, v208, v211
	v_pk_fma_f16 v210, v63, v207, v210
	v_pk_fma_f16 v205, v62, v206, v205
	v_pk_fma_f16 v215, v80, v208, v215
	v_pk_fma_f16 v214, v79, v207, v214
	v_pk_fma_f16 v213, v78, v206, v213
	v_pk_fma_f16 v208, v104, v208, v219
	v_pk_fma_f16 v207, v103, v207, v218
	v_pk_fma_f16 v206, v102, v206, v217
	v_pk_maximum3_f16 v217, v122, v138, v146
	v_pk_maximum3_f16 v218, v123, v139, v147
	v_pk_maximum3_f16 v219, v124, v140, v148
	v_pk_maximum3_f16 v236, v221, v225, v229
	v_pk_maximum3_f16 v240, v212, v216, v209
	v_pk_maximum3_f16 v233, v224, v228, v232
	v_pk_maximum3_f16 v234, v223, v227, v231
	v_pk_maximum3_f16 v235, v222, v226, v230
	v_pk_maximum3_f16 v237, v205, v213, v206
	v_pk_maximum3_f16 v238, v210, v214, v207
	v_pk_maximum3_f16 v220, v220, v236, v240
	v_pk_maximum3_f16 v239, v211, v215, v208
	v_pk_maximum3_f16 v217, v217, v233, v237
	v_pk_maximum3_f16 v218, v218, v234, v238
	v_pk_maximum3_f16 v219, v219, v235, v239
	v_pk_add_f16 v125, v125, v220 neg_lo:[0,1] neg_hi:[0,1]
	s_mov_b64 exec, s[64:65]
	buffer_load_dwordx4 v[86:89], v247, s[36:39], 0 offen
	buffer_load_dwordx4 v[38:41], v247, s[36:39], 0 offen offset:512
	s_mov_b64 exec, -1
	v_pk_add_f16 v122, v122, v217 neg_lo:[0,1] neg_hi:[0,1]
	v_pk_add_f16 v123, v123, v218 neg_lo:[0,1] neg_hi:[0,1]
	v_pk_add_f16 v124, v124, v219 neg_lo:[0,1] neg_hi:[0,1]
	v_pk_add_f16 v138, v138, v217 neg_lo:[0,1] neg_hi:[0,1]
	v_exp_f16_sdwa v233, v122 dst_sel:WORD_0 dst_unused:UNUSED_PAD src0_sel:WORD_0
	v_exp_f16_sdwa v234, v123 dst_sel:WORD_0 dst_unused:UNUSED_PAD src0_sel:WORD_0
	v_exp_f16_sdwa v235, v124 dst_sel:WORD_0 dst_unused:UNUSED_PAD src0_sel:WORD_0
	v_exp_f16_sdwa v236, v125 dst_sel:WORD_0 dst_unused:UNUSED_PAD src0_sel:WORD_0
	v_exp_f16_sdwa v233, v122 dst_sel:WORD_1 dst_unused:UNUSED_PRESERVE src0_sel:WORD_1
	v_exp_f16_sdwa v234, v123 dst_sel:WORD_1 dst_unused:UNUSED_PRESERVE src0_sel:WORD_1
	v_exp_f16_sdwa v235, v124 dst_sel:WORD_1 dst_unused:UNUSED_PRESERVE src0_sel:WORD_1
	v_exp_f16_sdwa v236, v125 dst_sel:WORD_1 dst_unused:UNUSED_PRESERVE src0_sel:WORD_1
	v_pk_add_f16 v139, v139, v218 neg_lo:[0,1] neg_hi:[0,1]
	v_pk_add_f16 v125, v233, 0
	v_pk_fma_f16 v85, v85, v236, 0
	v_pk_add_f16 v122, v236, 0
	v_pk_add_f16 v123, v235, 0
	v_pk_add_f16 v124, v234, 0
	v_pk_fma_f16 v84, v84, v235, 0
	v_pk_fma_f16 v83, v83, v234, 0
	v_pk_fma_f16 v82, v82, v233, 0
	v_pk_add_f16 v140, v140, v219 neg_lo:[0,1] neg_hi:[0,1]
	buffer_load_dwordx4 v[114:117], v248, s[36:39], 0 offen offset:512
	buffer_load_dwordx4 v[50:53], v248, s[36:39], 0 offen offset:1024
	v_pk_add_f16 v141, v141, v220 neg_lo:[0,1] neg_hi:[0,1]
	v_exp_f16_sdwa v233, v138 dst_sel:WORD_0 dst_unused:UNUSED_PAD src0_sel:WORD_0
	v_exp_f16_sdwa v234, v139 dst_sel:WORD_0 dst_unused:UNUSED_PAD src0_sel:WORD_0
	v_exp_f16_sdwa v235, v140 dst_sel:WORD_0 dst_unused:UNUSED_PAD src0_sel:WORD_0
	v_exp_f16_sdwa v236, v141 dst_sel:WORD_0 dst_unused:UNUSED_PAD src0_sel:WORD_0
	v_exp_f16_sdwa v233, v138 dst_sel:WORD_1 dst_unused:UNUSED_PRESERVE src0_sel:WORD_1
	v_exp_f16_sdwa v234, v139 dst_sel:WORD_1 dst_unused:UNUSED_PRESERVE src0_sel:WORD_1
	v_exp_f16_sdwa v235, v140 dst_sel:WORD_1 dst_unused:UNUSED_PRESERVE src0_sel:WORD_1
	v_exp_f16_sdwa v236, v141 dst_sel:WORD_1 dst_unused:UNUSED_PRESERVE src0_sel:WORD_1
	v_pk_add_f16 v125, v125, v233
	v_pk_fma_f16 v85, v109, v236, v85
	v_pk_add_f16 v109, v149, v220 neg_lo:[0,1] neg_hi:[0,1]
	v_pk_add_f16 v124, v124, v234
	v_pk_add_f16 v123, v123, v235
	v_pk_add_f16 v122, v122, v236
	v_pk_fma_f16 v82, v106, v233, v82
	v_pk_fma_f16 v83, v107, v234, v83
	v_pk_fma_f16 v84, v108, v235, v84
	v_pk_add_f16 v106, v146, v217 neg_lo:[0,1] neg_hi:[0,1]
	v_pk_add_f16 v107, v147, v218 neg_lo:[0,1] neg_hi:[0,1]
	v_pk_add_f16 v108, v148, v219 neg_lo:[0,1] neg_hi:[0,1]
	v_exp_f16_sdwa v138, v106 dst_sel:WORD_0 dst_unused:UNUSED_PAD src0_sel:WORD_0
	v_exp_f16_sdwa v139, v107 dst_sel:WORD_0 dst_unused:UNUSED_PAD src0_sel:WORD_0
	v_exp_f16_sdwa v140, v108 dst_sel:WORD_0 dst_unused:UNUSED_PAD src0_sel:WORD_0
	v_exp_f16_sdwa v141, v109 dst_sel:WORD_0 dst_unused:UNUSED_PAD src0_sel:WORD_0
	v_exp_f16_sdwa v138, v106 dst_sel:WORD_1 dst_unused:UNUSED_PRESERVE src0_sel:WORD_1
	v_exp_f16_sdwa v139, v107 dst_sel:WORD_1 dst_unused:UNUSED_PRESERVE src0_sel:WORD_1
	v_exp_f16_sdwa v140, v108 dst_sel:WORD_1 dst_unused:UNUSED_PRESERVE src0_sel:WORD_1
	v_exp_f16_sdwa v141, v109 dst_sel:WORD_1 dst_unused:UNUSED_PRESERVE src0_sel:WORD_1
	v_pk_add_f16 v109, v125, v138
	v_pk_add_f16 v106, v122, v141
	s_mov_b64 exec, s[66:67]
	buffer_load_dwordx4 v[130:133], v248, s[36:39], 0 offen offset:2048
	buffer_load_dwordx4 v[70:73], v248, s[36:39], 0 offen offset:2560
	s_mov_b64 exec, -1
	v_pk_add_f16 v107, v123, v140
	v_pk_add_f16 v108, v124, v139
	v_pk_fma_f16 v85, v129, v141, v85
	v_pk_fma_f16 v84, v128, v140, v84
	v_pk_fma_f16 v83, v127, v139, v83
	v_pk_fma_f16 v82, v126, v138, v82
	v_pk_add_f16 v122, v224, v217 neg_lo:[0,1] neg_hi:[0,1]
	v_pk_add_f16 v123, v223, v218 neg_lo:[0,1] neg_hi:[0,1]
	v_pk_add_f16 v124, v222, v219 neg_lo:[0,1] neg_hi:[0,1]
	v_pk_add_f16 v125, v221, v220 neg_lo:[0,1] neg_hi:[0,1]
	v_exp_f16_sdwa v126, v122 dst_sel:WORD_0 dst_unused:UNUSED_PAD src0_sel:WORD_0
	v_exp_f16_sdwa v127, v123 dst_sel:WORD_0 dst_unused:UNUSED_PAD src0_sel:WORD_0
	v_exp_f16_sdwa v128, v124 dst_sel:WORD_0 dst_unused:UNUSED_PAD src0_sel:WORD_0
	v_exp_f16_sdwa v129, v125 dst_sel:WORD_0 dst_unused:UNUSED_PAD src0_sel:WORD_0
	v_exp_f16_sdwa v126, v122 dst_sel:WORD_1 dst_unused:UNUSED_PRESERVE src0_sel:WORD_1
	v_exp_f16_sdwa v127, v123 dst_sel:WORD_1 dst_unused:UNUSED_PRESERVE src0_sel:WORD_1
	v_exp_f16_sdwa v128, v124 dst_sel:WORD_1 dst_unused:UNUSED_PRESERVE src0_sel:WORD_1
	v_exp_f16_sdwa v129, v125 dst_sel:WORD_1 dst_unused:UNUSED_PRESERVE src0_sel:WORD_1
	v_pk_add_f16 v122, v228, v217 neg_lo:[0,1] neg_hi:[0,1]
	v_pk_add_f16 v109, v109, v126
	v_pk_add_f16 v108, v108, v127
	v_pk_add_f16 v107, v107, v128
	s_mov_b64 exec, s[76:77]
	buffer_load_dwordx4 v[142:145], v249, s[36:39], 0 offen
	buffer_load_dwordx4 v[90:93], v249, s[36:39], 0 offen offset:512
	s_mov_b64 exec, -1
	v_pk_add_f16 v106, v106, v129
	v_pk_fma_f16 v82, v54, v126, v82
	v_pk_fma_f16 v83, v55, v127, v83
	v_pk_fma_f16 v84, v56, v128, v84
	v_pk_fma_f16 v85, v57, v129, v85
	v_pk_add_f16 v123, v227, v218 neg_lo:[0,1] neg_hi:[0,1]
	v_pk_add_f16 v124, v226, v219 neg_lo:[0,1] neg_hi:[0,1]
	v_pk_add_f16 v125, v225, v220 neg_lo:[0,1] neg_hi:[0,1]
	v_exp_f16_sdwa v126, v122 dst_sel:WORD_0 dst_unused:UNUSED_PAD src0_sel:WORD_0
	v_exp_f16_sdwa v127, v123 dst_sel:WORD_0 dst_unused:UNUSED_PAD src0_sel:WORD_0
	v_exp_f16_sdwa v128, v124 dst_sel:WORD_0 dst_unused:UNUSED_PAD src0_sel:WORD_0
	v_exp_f16_sdwa v129, v125 dst_sel:WORD_0 dst_unused:UNUSED_PAD src0_sel:WORD_0
	v_exp_f16_sdwa v126, v122 dst_sel:WORD_1 dst_unused:UNUSED_PRESERVE src0_sel:WORD_1
	v_exp_f16_sdwa v127, v123 dst_sel:WORD_1 dst_unused:UNUSED_PRESERVE src0_sel:WORD_1
	v_exp_f16_sdwa v128, v124 dst_sel:WORD_1 dst_unused:UNUSED_PRESERVE src0_sel:WORD_1
	v_exp_f16_sdwa v129, v125 dst_sel:WORD_1 dst_unused:UNUSED_PRESERVE src0_sel:WORD_1
	v_pk_add_f16 v122, v232, v217 neg_lo:[0,1] neg_hi:[0,1]
	v_pk_add_f16 v109, v109, v126
	v_pk_add_f16 v106, v106, v129
	v_pk_add_f16 v107, v107, v128
	v_pk_add_f16 v108, v108, v127
	v_pk_fma_f16 v85, v77, v129, v85
	v_pk_fma_f16 v84, v76, v128, v84
	s_mov_b64 exec, s[70:71]
	buffer_load_dwordx4 v[150:153], v250, s[36:39], 0 offen offset:512
	buffer_load_dwordx4 v[110:113], v250, s[36:39], 0 offen offset:1024
	s_mov_b64 exec, -1
	v_pk_fma_f16 v83, v75, v127, v83
	v_pk_fma_f16 v82, v74, v126, v82
	v_pk_add_f16 v123, v231, v218 neg_lo:[0,1] neg_hi:[0,1]
	v_pk_add_f16 v124, v230, v219 neg_lo:[0,1] neg_hi:[0,1]
	v_pk_add_f16 v125, v229, v220 neg_lo:[0,1] neg_hi:[0,1]
	v_exp_f16_sdwa v126, v122 dst_sel:WORD_0 dst_unused:UNUSED_PAD src0_sel:WORD_0
	v_exp_f16_sdwa v127, v123 dst_sel:WORD_0 dst_unused:UNUSED_PAD src0_sel:WORD_0
	v_exp_f16_sdwa v128, v124 dst_sel:WORD_0 dst_unused:UNUSED_PAD src0_sel:WORD_0
	v_exp_f16_sdwa v129, v125 dst_sel:WORD_0 dst_unused:UNUSED_PAD src0_sel:WORD_0
	v_exp_f16_sdwa v126, v122 dst_sel:WORD_1 dst_unused:UNUSED_PRESERVE src0_sel:WORD_1
	v_exp_f16_sdwa v127, v123 dst_sel:WORD_1 dst_unused:UNUSED_PRESERVE src0_sel:WORD_1
	v_exp_f16_sdwa v128, v124 dst_sel:WORD_1 dst_unused:UNUSED_PRESERVE src0_sel:WORD_1
	v_exp_f16_sdwa v129, v125 dst_sel:WORD_1 dst_unused:UNUSED_PRESERVE src0_sel:WORD_1
	v_pk_add_f16 v122, v205, v217 neg_lo:[0,1] neg_hi:[0,1]
	v_pk_add_f16 v109, v109, v126
	v_pk_add_f16 v108, v108, v127
	v_pk_add_f16 v107, v107, v128
	v_pk_add_f16 v106, v106, v129
	v_pk_fma_f16 v82, v98, v126, v82
	v_pk_fma_f16 v83, v99, v127, v83
	v_pk_fma_f16 v84, v100, v128, v84
	v_pk_fma_f16 v85, v101, v129, v85
	s_mov_b64 exec, s[78:79]
	buffer_load_dwordx4 v[14:17], v250, s[36:39], 0 offen offset:2048
	buffer_load_dwordx4 v[10:13], v250, s[36:39], 0 offen offset:2560
	s_mov_b64 exec, -1
	v_pk_add_f16 v123, v210, v218 neg_lo:[0,1] neg_hi:[0,1]
	v_pk_add_f16 v124, v211, v219 neg_lo:[0,1] neg_hi:[0,1]
	v_pk_add_f16 v125, v212, v220 neg_lo:[0,1] neg_hi:[0,1]
	v_exp_f16_sdwa v126, v122 dst_sel:WORD_0 dst_unused:UNUSED_PAD src0_sel:WORD_0
	v_exp_f16_sdwa v127, v123 dst_sel:WORD_0 dst_unused:UNUSED_PAD src0_sel:WORD_0
	v_exp_f16_sdwa v128, v124 dst_sel:WORD_0 dst_unused:UNUSED_PAD src0_sel:WORD_0
	v_exp_f16_sdwa v129, v125 dst_sel:WORD_0 dst_unused:UNUSED_PAD src0_sel:WORD_0
	v_exp_f16_sdwa v126, v122 dst_sel:WORD_1 dst_unused:UNUSED_PRESERVE src0_sel:WORD_1
	v_exp_f16_sdwa v127, v123 dst_sel:WORD_1 dst_unused:UNUSED_PRESERVE src0_sel:WORD_1
	v_exp_f16_sdwa v128, v124 dst_sel:WORD_1 dst_unused:UNUSED_PRESERVE src0_sel:WORD_1
	v_exp_f16_sdwa v129, v125 dst_sel:WORD_1 dst_unused:UNUSED_PRESERVE src0_sel:WORD_1
	v_pk_add_f16 v122, v213, v217 neg_lo:[0,1] neg_hi:[0,1]
	v_pk_add_f16 v109, v109, v126
	v_pk_add_f16 v106, v106, v129
	v_pk_add_f16 v107, v107, v128
	v_pk_add_f16 v108, v108, v127
	v_pk_fma_f16 v85, v33, v129, v85
	v_pk_fma_f16 v84, v32, v128, v84
	v_pk_fma_f16 v83, v31, v127, v83
	v_pk_fma_f16 v82, v30, v126, v82
	v_pk_add_f16 v123, v214, v218 neg_lo:[0,1] neg_hi:[0,1]
	v_pk_add_f16 v124, v215, v219 neg_lo:[0,1] neg_hi:[0,1]
	v_pk_add_f16 v125, v216, v220 neg_lo:[0,1] neg_hi:[0,1]
	v_exp_f16_sdwa v126, v122 dst_sel:WORD_0 dst_unused:UNUSED_PAD src0_sel:WORD_0
	v_exp_f16_sdwa v127, v123 dst_sel:WORD_0 dst_unused:UNUSED_PAD src0_sel:WORD_0
	v_exp_f16_sdwa v128, v124 dst_sel:WORD_0 dst_unused:UNUSED_PAD src0_sel:WORD_0
	v_exp_f16_sdwa v129, v125 dst_sel:WORD_0 dst_unused:UNUSED_PAD src0_sel:WORD_0
	v_exp_f16_sdwa v126, v122 dst_sel:WORD_1 dst_unused:UNUSED_PRESERVE src0_sel:WORD_1
	v_exp_f16_sdwa v127, v123 dst_sel:WORD_1 dst_unused:UNUSED_PRESERVE src0_sel:WORD_1
	v_exp_f16_sdwa v128, v124 dst_sel:WORD_1 dst_unused:UNUSED_PRESERVE src0_sel:WORD_1
	v_exp_f16_sdwa v129, v125 dst_sel:WORD_1 dst_unused:UNUSED_PRESERVE src0_sel:WORD_1
	v_pk_add_f16 v122, v206, v217 neg_lo:[0,1] neg_hi:[0,1]
	v_pk_add_f16 v109, v109, v126
	v_pk_add_f16 v108, v108, v127
	v_pk_add_f16 v107, v107, v128
	v_pk_add_f16 v106, v106, v129
	v_pk_fma_f16 v82, v42, v126, v82
	v_pk_fma_f16 v83, v43, v127, v83
	v_pk_fma_f16 v84, v44, v128, v84
	v_pk_fma_f16 v85, v45, v129, v85
	v_pk_add_f16 v123, v207, v218 neg_lo:[0,1] neg_hi:[0,1]
	v_pk_add_f16 v124, v208, v219 neg_lo:[0,1] neg_hi:[0,1]
	v_pk_add_f16 v125, v209, v220 neg_lo:[0,1] neg_hi:[0,1]
	v_exp_f16_sdwa v126, v122 dst_sel:WORD_0 dst_unused:UNUSED_PAD src0_sel:WORD_0
	v_exp_f16_sdwa v127, v123 dst_sel:WORD_0 dst_unused:UNUSED_PAD src0_sel:WORD_0
	v_exp_f16_sdwa v128, v124 dst_sel:WORD_0 dst_unused:UNUSED_PAD src0_sel:WORD_0
	v_exp_f16_sdwa v129, v125 dst_sel:WORD_0 dst_unused:UNUSED_PAD src0_sel:WORD_0
	v_exp_f16_sdwa v126, v122 dst_sel:WORD_1 dst_unused:UNUSED_PRESERVE src0_sel:WORD_1
	v_exp_f16_sdwa v127, v123 dst_sel:WORD_1 dst_unused:UNUSED_PRESERVE src0_sel:WORD_1
	v_exp_f16_sdwa v128, v124 dst_sel:WORD_1 dst_unused:UNUSED_PRESERVE src0_sel:WORD_1
	v_exp_f16_sdwa v129, v125 dst_sel:WORD_1 dst_unused:UNUSED_PRESERVE src0_sel:WORD_1
	v_pk_add_f16 v109, v109, v126
	v_pk_add_f16 v108, v108, v127
	v_rcp_f16_e32 v122, v109
	v_rcp_f16_sdwa v109, v109 dst_sel:DWORD dst_unused:UNUSED_PAD src0_sel:WORD_1
	v_pk_add_f16 v107, v107, v128
	v_rcp_f16_e32 v123, v108
	v_rcp_f16_sdwa v108, v108 dst_sel:DWORD dst_unused:UNUSED_PAD src0_sel:WORD_1
	v_pk_add_f16 v106, v106, v129
	v_rcp_f16_e32 v124, v107
	v_rcp_f16_sdwa v107, v107 dst_sel:DWORD dst_unused:UNUSED_PAD src0_sel:WORD_1
	v_rcp_f16_e32 v125, v106
	v_rcp_f16_sdwa v106, v106 dst_sel:DWORD dst_unused:UNUSED_PAD src0_sel:WORD_1
	v_pk_fma_f16 v82, v58, v126, v82
	v_pack_b32_f16 v109, v122, v109
	v_pk_fma_f16 v83, v59, v127, v83
	v_pk_mul_f16 v138, v82, v109
	v_pack_b32_f16 v82, v123, v108
	v_pk_fma_f16 v84, v60, v128, v84
	v_pk_mul_f16 v139, v83, v82
	v_pack_b32_f16 v82, v124, v107
	v_pk_fma_f16 v85, v61, v129, v85
	v_pk_mul_f16 v140, v84, v82
	v_pack_b32_f16 v82, v125, v106
	v_pk_mul_f16 v141, v85, v82
	s_waitcnt vmcnt(12)
	v_pk_mul_f16 v85, v204, v165 op_sel_hi:[0,1]
	v_pk_mul_f16 v109, v202, v165 op_sel_hi:[0,1]
	v_pk_mul_f16 v122, v203, v162 op_sel_hi:[0,1]
	v_pk_mul_f16 v125, v203, v165 op_sel_hi:[0,1]
	v_pk_mul_f16 v82, v204, v162 op_sel_hi:[0,1]
	v_pk_mul_f16 v83, v204, v163 op_sel_hi:[0,1]
	v_pk_mul_f16 v84, v204, v164 op_sel_hi:[0,1]
	v_pk_mul_f16 v106, v202, v162 op_sel_hi:[0,1]
	v_pk_mul_f16 v107, v202, v163 op_sel_hi:[0,1]
	v_pk_mul_f16 v108, v202, v164 op_sel_hi:[0,1]
	v_pk_mul_f16 v123, v203, v163 op_sel_hi:[0,1]
	v_pk_mul_f16 v124, v203, v164 op_sel_hi:[0,1]
	v_pk_fma_f16 v97, v97, v165, v85
	v_pk_fma_f16 v121, v121, v165, v109
	v_pk_fma_f16 v126, v137, v165, v125
	v_pk_fma_f16 v129, v134, v162, v122
	v_pk_fma_f16 v134, v65, v165, v85
	v_pk_fma_f16 v146, v81, v165, v109
	v_pk_fma_f16 v205, v105, v165, v125
	v_pk_fma_f16 v85, v37, v165, v85
	v_pk_fma_f16 v109, v49, v165, v109
	v_pk_fma_f16 v125, v69, v165, v125
	v_pk_maximum3_f16 v165, v97, v121, v126
	v_pk_fma_f16 v96, v96, v164, v84
	v_pk_fma_f16 v95, v95, v163, v83
	v_pk_fma_f16 v94, v94, v162, v82
	v_pk_fma_f16 v120, v120, v164, v108
	v_pk_fma_f16 v119, v119, v163, v107
	v_pk_fma_f16 v118, v118, v162, v106
	v_pk_fma_f16 v127, v136, v164, v124
	v_pk_fma_f16 v128, v135, v163, v123
	v_pk_fma_f16 v135, v64, v164, v84
	v_pk_fma_f16 v136, v63, v163, v83
	v_pk_fma_f16 v137, v62, v162, v82
	v_pk_fma_f16 v147, v80, v164, v108
	v_pk_fma_f16 v148, v79, v163, v107
	v_pk_fma_f16 v149, v78, v162, v106
	v_pk_fma_f16 v206, v104, v164, v124
	v_pk_fma_f16 v207, v103, v163, v123
	v_pk_fma_f16 v208, v102, v162, v122
	v_pk_fma_f16 v84, v36, v164, v84
	v_pk_fma_f16 v83, v35, v163, v83
	v_pk_fma_f16 v82, v34, v162, v82
	v_pk_fma_f16 v108, v48, v164, v108
	v_pk_fma_f16 v107, v47, v163, v107
	v_pk_fma_f16 v106, v46, v162, v106
	v_pk_fma_f16 v124, v68, v164, v124
	v_pk_fma_f16 v123, v67, v163, v123
	v_pk_fma_f16 v122, v66, v162, v122
	v_pk_maximum3_f16 v162, v94, v118, v129
	v_pk_maximum3_f16 v163, v95, v119, v128
	v_pk_maximum3_f16 v164, v96, v120, v127
	v_pk_maximum3_f16 v212, v134, v146, v205
	v_pk_maximum3_f16 v216, v85, v109, v125
	v_pk_maximum3_f16 v209, v137, v149, v208
	v_pk_maximum3_f16 v210, v136, v148, v207
	v_pk_maximum3_f16 v211, v135, v147, v206
	v_pk_maximum3_f16 v213, v82, v106, v122
	v_pk_maximum3_f16 v214, v83, v107, v123
	v_pk_maximum3_f16 v165, v165, v212, v216
	v_pk_maximum3_f16 v215, v84, v108, v124
	v_pk_maximum3_f16 v162, v162, v209, v213
	v_pk_maximum3_f16 v163, v163, v210, v214
	v_pk_maximum3_f16 v164, v164, v211, v215
	v_pk_add_f16 v97, v97, v165 neg_lo:[0,1] neg_hi:[0,1]
	v_pk_add_f16 v94, v94, v162 neg_lo:[0,1] neg_hi:[0,1]
	v_pk_add_f16 v95, v95, v163 neg_lo:[0,1] neg_hi:[0,1]
	v_pk_add_f16 v96, v96, v164 neg_lo:[0,1] neg_hi:[0,1]
	v_pk_add_f16 v118, v118, v162 neg_lo:[0,1] neg_hi:[0,1]
	v_exp_f16_sdwa v209, v94 dst_sel:WORD_0 dst_unused:UNUSED_PAD src0_sel:WORD_0
	v_exp_f16_sdwa v210, v95 dst_sel:WORD_0 dst_unused:UNUSED_PAD src0_sel:WORD_0
	v_exp_f16_sdwa v211, v96 dst_sel:WORD_0 dst_unused:UNUSED_PAD src0_sel:WORD_0
	v_exp_f16_sdwa v212, v97 dst_sel:WORD_0 dst_unused:UNUSED_PAD src0_sel:WORD_0
	v_exp_f16_sdwa v209, v94 dst_sel:WORD_1 dst_unused:UNUSED_PRESERVE src0_sel:WORD_1
	v_exp_f16_sdwa v210, v95 dst_sel:WORD_1 dst_unused:UNUSED_PRESERVE src0_sel:WORD_1
	v_exp_f16_sdwa v211, v96 dst_sel:WORD_1 dst_unused:UNUSED_PRESERVE src0_sel:WORD_1
	v_exp_f16_sdwa v212, v97 dst_sel:WORD_1 dst_unused:UNUSED_PRESERVE src0_sel:WORD_1
	v_pk_add_f16 v119, v119, v163 neg_lo:[0,1] neg_hi:[0,1]
	v_pk_add_f16 v97, v209, 0
	v_pk_fma_f16 v57, v57, v212, 0
	v_pk_add_f16 v94, v212, 0
	v_pk_add_f16 v95, v211, 0
	v_pk_add_f16 v96, v210, 0
	v_pk_fma_f16 v56, v56, v211, 0
	v_pk_fma_f16 v55, v55, v210, 0
	v_pk_fma_f16 v54, v54, v209, 0
	v_pk_add_f16 v120, v120, v164 neg_lo:[0,1] neg_hi:[0,1]
	v_pk_add_f16 v121, v121, v165 neg_lo:[0,1] neg_hi:[0,1]
	v_pk_add_f16 v82, v82, v162 neg_lo:[0,1] neg_hi:[0,1]
	v_exp_f16_sdwa v209, v118 dst_sel:WORD_0 dst_unused:UNUSED_PAD src0_sel:WORD_0
	v_exp_f16_sdwa v210, v119 dst_sel:WORD_0 dst_unused:UNUSED_PAD src0_sel:WORD_0
	v_exp_f16_sdwa v211, v120 dst_sel:WORD_0 dst_unused:UNUSED_PAD src0_sel:WORD_0
	v_exp_f16_sdwa v212, v121 dst_sel:WORD_0 dst_unused:UNUSED_PAD src0_sel:WORD_0
	v_exp_f16_sdwa v209, v118 dst_sel:WORD_1 dst_unused:UNUSED_PRESERVE src0_sel:WORD_1
	v_exp_f16_sdwa v210, v119 dst_sel:WORD_1 dst_unused:UNUSED_PRESERVE src0_sel:WORD_1
	v_exp_f16_sdwa v211, v120 dst_sel:WORD_1 dst_unused:UNUSED_PRESERVE src0_sel:WORD_1
	v_exp_f16_sdwa v212, v121 dst_sel:WORD_1 dst_unused:UNUSED_PRESERVE src0_sel:WORD_1
	v_pk_add_f16 v83, v83, v163 neg_lo:[0,1] neg_hi:[0,1]
	v_pk_add_f16 v97, v97, v209
	v_pk_fma_f16 v57, v77, v212, v57
	v_pk_add_f16 v77, v126, v165 neg_lo:[0,1] neg_hi:[0,1]
	v_pk_add_f16 v96, v96, v210
	v_pk_add_f16 v95, v95, v211
	v_pk_add_f16 v94, v94, v212
	v_pk_fma_f16 v54, v74, v209, v54
	v_pk_fma_f16 v55, v75, v210, v55
	v_pk_fma_f16 v56, v76, v211, v56
	v_pk_add_f16 v74, v129, v162 neg_lo:[0,1] neg_hi:[0,1]
	v_pk_add_f16 v75, v128, v163 neg_lo:[0,1] neg_hi:[0,1]
	v_pk_add_f16 v76, v127, v164 neg_lo:[0,1] neg_hi:[0,1]
	v_pk_add_f16 v84, v84, v164 neg_lo:[0,1] neg_hi:[0,1]
	v_exp_f16_sdwa v118, v74 dst_sel:WORD_0 dst_unused:UNUSED_PAD src0_sel:WORD_0
	v_exp_f16_sdwa v119, v75 dst_sel:WORD_0 dst_unused:UNUSED_PAD src0_sel:WORD_0
	v_exp_f16_sdwa v120, v76 dst_sel:WORD_0 dst_unused:UNUSED_PAD src0_sel:WORD_0
	v_exp_f16_sdwa v121, v77 dst_sel:WORD_0 dst_unused:UNUSED_PAD src0_sel:WORD_0
	v_exp_f16_sdwa v118, v74 dst_sel:WORD_1 dst_unused:UNUSED_PRESERVE src0_sel:WORD_1
	v_exp_f16_sdwa v119, v75 dst_sel:WORD_1 dst_unused:UNUSED_PRESERVE src0_sel:WORD_1
	v_exp_f16_sdwa v120, v76 dst_sel:WORD_1 dst_unused:UNUSED_PRESERVE src0_sel:WORD_1
	v_exp_f16_sdwa v121, v77 dst_sel:WORD_1 dst_unused:UNUSED_PRESERVE src0_sel:WORD_1
	v_pk_add_f16 v85, v85, v165 neg_lo:[0,1] neg_hi:[0,1]
	v_pk_add_f16 v77, v97, v118
	v_pk_add_f16 v74, v94, v121
	v_pk_add_f16 v75, v95, v120
	v_pk_add_f16 v76, v96, v119
	v_pk_fma_f16 v57, v101, v121, v57
	v_pk_fma_f16 v56, v100, v120, v56
	v_pk_fma_f16 v55, v99, v119, v55
	v_pk_fma_f16 v54, v98, v118, v54
	v_pk_add_f16 v94, v137, v162 neg_lo:[0,1] neg_hi:[0,1]
	v_pk_add_f16 v95, v136, v163 neg_lo:[0,1] neg_hi:[0,1]
	v_pk_add_f16 v96, v135, v164 neg_lo:[0,1] neg_hi:[0,1]
	v_pk_add_f16 v97, v134, v165 neg_lo:[0,1] neg_hi:[0,1]
	v_exp_f16_sdwa v98, v94 dst_sel:WORD_0 dst_unused:UNUSED_PAD src0_sel:WORD_0
	v_exp_f16_sdwa v99, v95 dst_sel:WORD_0 dst_unused:UNUSED_PAD src0_sel:WORD_0
	v_exp_f16_sdwa v100, v96 dst_sel:WORD_0 dst_unused:UNUSED_PAD src0_sel:WORD_0
	v_exp_f16_sdwa v101, v97 dst_sel:WORD_0 dst_unused:UNUSED_PAD src0_sel:WORD_0
	v_exp_f16_sdwa v98, v94 dst_sel:WORD_1 dst_unused:UNUSED_PRESERVE src0_sel:WORD_1
	v_exp_f16_sdwa v99, v95 dst_sel:WORD_1 dst_unused:UNUSED_PRESERVE src0_sel:WORD_1
	v_exp_f16_sdwa v100, v96 dst_sel:WORD_1 dst_unused:UNUSED_PRESERVE src0_sel:WORD_1
	v_exp_f16_sdwa v101, v97 dst_sel:WORD_1 dst_unused:UNUSED_PRESERVE src0_sel:WORD_1
	v_pk_add_f16 v94, v149, v162 neg_lo:[0,1] neg_hi:[0,1]
	v_pk_add_f16 v77, v77, v98
	v_pk_add_f16 v76, v76, v99
	v_pk_add_f16 v75, v75, v100
	v_pk_add_f16 v74, v74, v101
	v_pk_fma_f16 v54, v30, v98, v54
	v_pk_fma_f16 v55, v31, v99, v55
	v_pk_fma_f16 v56, v32, v100, v56
	v_pk_fma_f16 v57, v33, v101, v57
	v_pk_add_f16 v95, v148, v163 neg_lo:[0,1] neg_hi:[0,1]
	v_pk_add_f16 v96, v147, v164 neg_lo:[0,1] neg_hi:[0,1]
	v_pk_add_f16 v97, v146, v165 neg_lo:[0,1] neg_hi:[0,1]
	v_exp_f16_sdwa v98, v94 dst_sel:WORD_0 dst_unused:UNUSED_PAD src0_sel:WORD_0
	v_exp_f16_sdwa v99, v95 dst_sel:WORD_0 dst_unused:UNUSED_PAD src0_sel:WORD_0
	v_exp_f16_sdwa v100, v96 dst_sel:WORD_0 dst_unused:UNUSED_PAD src0_sel:WORD_0
	v_exp_f16_sdwa v101, v97 dst_sel:WORD_0 dst_unused:UNUSED_PAD src0_sel:WORD_0
	v_exp_f16_sdwa v98, v94 dst_sel:WORD_1 dst_unused:UNUSED_PRESERVE src0_sel:WORD_1
	v_exp_f16_sdwa v99, v95 dst_sel:WORD_1 dst_unused:UNUSED_PRESERVE src0_sel:WORD_1
	v_exp_f16_sdwa v100, v96 dst_sel:WORD_1 dst_unused:UNUSED_PRESERVE src0_sel:WORD_1
	v_exp_f16_sdwa v101, v97 dst_sel:WORD_1 dst_unused:UNUSED_PRESERVE src0_sel:WORD_1
	v_pk_add_f16 v94, v208, v162 neg_lo:[0,1] neg_hi:[0,1]
	v_pk_add_f16 v77, v77, v98
	v_pk_add_f16 v74, v74, v101
	v_pk_add_f16 v75, v75, v100
	v_pk_add_f16 v76, v76, v99
	v_pk_fma_f16 v57, v45, v101, v57
	v_pk_fma_f16 v56, v44, v100, v56
	v_pk_fma_f16 v55, v43, v99, v55
	v_pk_fma_f16 v54, v42, v98, v54
	v_pk_add_f16 v95, v207, v163 neg_lo:[0,1] neg_hi:[0,1]
	v_pk_add_f16 v96, v206, v164 neg_lo:[0,1] neg_hi:[0,1]
	v_pk_add_f16 v97, v205, v165 neg_lo:[0,1] neg_hi:[0,1]
	v_exp_f16_sdwa v98, v94 dst_sel:WORD_0 dst_unused:UNUSED_PAD src0_sel:WORD_0
	v_exp_f16_sdwa v99, v95 dst_sel:WORD_0 dst_unused:UNUSED_PAD src0_sel:WORD_0
	v_exp_f16_sdwa v100, v96 dst_sel:WORD_0 dst_unused:UNUSED_PAD src0_sel:WORD_0
	v_exp_f16_sdwa v101, v97 dst_sel:WORD_0 dst_unused:UNUSED_PAD src0_sel:WORD_0
	v_exp_f16_sdwa v98, v94 dst_sel:WORD_1 dst_unused:UNUSED_PRESERVE src0_sel:WORD_1
	v_exp_f16_sdwa v99, v95 dst_sel:WORD_1 dst_unused:UNUSED_PRESERVE src0_sel:WORD_1
	v_exp_f16_sdwa v100, v96 dst_sel:WORD_1 dst_unused:UNUSED_PRESERVE src0_sel:WORD_1
	v_exp_f16_sdwa v101, v97 dst_sel:WORD_1 dst_unused:UNUSED_PRESERVE src0_sel:WORD_1
	v_exp_f16_sdwa v94, v82 dst_sel:WORD_0 dst_unused:UNUSED_PAD src0_sel:WORD_0
	v_exp_f16_sdwa v95, v83 dst_sel:WORD_0 dst_unused:UNUSED_PAD src0_sel:WORD_0
	v_exp_f16_sdwa v96, v84 dst_sel:WORD_0 dst_unused:UNUSED_PAD src0_sel:WORD_0
	v_exp_f16_sdwa v97, v85 dst_sel:WORD_0 dst_unused:UNUSED_PAD src0_sel:WORD_0
	v_exp_f16_sdwa v94, v82 dst_sel:WORD_1 dst_unused:UNUSED_PRESERVE src0_sel:WORD_1
	v_exp_f16_sdwa v95, v83 dst_sel:WORD_1 dst_unused:UNUSED_PRESERVE src0_sel:WORD_1
	v_exp_f16_sdwa v96, v84 dst_sel:WORD_1 dst_unused:UNUSED_PRESERVE src0_sel:WORD_1
	v_exp_f16_sdwa v97, v85 dst_sel:WORD_1 dst_unused:UNUSED_PRESERVE src0_sel:WORD_1
	v_pk_add_f16 v82, v106, v162 neg_lo:[0,1] neg_hi:[0,1]
	v_pk_add_f16 v77, v77, v98
	v_pk_add_f16 v76, v76, v99
	v_pk_add_f16 v75, v75, v100
	v_pk_add_f16 v74, v74, v101
	v_pk_fma_f16 v54, v58, v98, v54
	v_pk_fma_f16 v55, v59, v99, v55
	v_pk_fma_f16 v56, v60, v100, v56
	v_pk_fma_f16 v57, v61, v101, v57
	v_pk_add_f16 v77, v77, v94
	v_pk_add_f16 v74, v74, v97
	v_pk_add_f16 v75, v75, v96
	v_pk_add_f16 v76, v76, v95
	v_pk_fma_f16 v57, v21, v97, v57
	v_pk_fma_f16 v56, v20, v96, v56
	v_pk_fma_f16 v55, v19, v95, v55
	v_pk_fma_f16 v54, v18, v94, v54
	v_pk_add_f16 v83, v107, v163 neg_lo:[0,1] neg_hi:[0,1]
	v_pk_add_f16 v84, v108, v164 neg_lo:[0,1] neg_hi:[0,1]
	v_pk_add_f16 v85, v109, v165 neg_lo:[0,1] neg_hi:[0,1]
	v_exp_f16_sdwa v94, v82 dst_sel:WORD_0 dst_unused:UNUSED_PAD src0_sel:WORD_0
	v_exp_f16_sdwa v95, v83 dst_sel:WORD_0 dst_unused:UNUSED_PAD src0_sel:WORD_0
	v_exp_f16_sdwa v96, v84 dst_sel:WORD_0 dst_unused:UNUSED_PAD src0_sel:WORD_0
	v_exp_f16_sdwa v97, v85 dst_sel:WORD_0 dst_unused:UNUSED_PAD src0_sel:WORD_0
	v_exp_f16_sdwa v94, v82 dst_sel:WORD_1 dst_unused:UNUSED_PRESERVE src0_sel:WORD_1
	v_exp_f16_sdwa v95, v83 dst_sel:WORD_1 dst_unused:UNUSED_PRESERVE src0_sel:WORD_1
	v_exp_f16_sdwa v96, v84 dst_sel:WORD_1 dst_unused:UNUSED_PRESERVE src0_sel:WORD_1
	v_exp_f16_sdwa v97, v85 dst_sel:WORD_1 dst_unused:UNUSED_PRESERVE src0_sel:WORD_1
	v_pk_add_f16 v82, v122, v162 neg_lo:[0,1] neg_hi:[0,1]
	v_pk_add_f16 v77, v77, v94
	v_pk_add_f16 v76, v76, v95
	v_pk_add_f16 v75, v75, v96
	v_pk_add_f16 v74, v74, v97
	v_pk_fma_f16 v54, v22, v94, v54
	v_pk_fma_f16 v55, v23, v95, v55
	v_pk_fma_f16 v56, v24, v96, v56
	v_pk_fma_f16 v57, v25, v97, v57
	v_pk_add_f16 v83, v123, v163 neg_lo:[0,1] neg_hi:[0,1]
	v_pk_add_f16 v84, v124, v164 neg_lo:[0,1] neg_hi:[0,1]
	v_pk_add_f16 v85, v125, v165 neg_lo:[0,1] neg_hi:[0,1]
	v_exp_f16_sdwa v94, v82 dst_sel:WORD_0 dst_unused:UNUSED_PAD src0_sel:WORD_0
	v_exp_f16_sdwa v95, v83 dst_sel:WORD_0 dst_unused:UNUSED_PAD src0_sel:WORD_0
	v_exp_f16_sdwa v96, v84 dst_sel:WORD_0 dst_unused:UNUSED_PAD src0_sel:WORD_0
	v_exp_f16_sdwa v97, v85 dst_sel:WORD_0 dst_unused:UNUSED_PAD src0_sel:WORD_0
	v_exp_f16_sdwa v94, v82 dst_sel:WORD_1 dst_unused:UNUSED_PRESERVE src0_sel:WORD_1
	v_exp_f16_sdwa v95, v83 dst_sel:WORD_1 dst_unused:UNUSED_PRESERVE src0_sel:WORD_1
	v_exp_f16_sdwa v96, v84 dst_sel:WORD_1 dst_unused:UNUSED_PRESERVE src0_sel:WORD_1
	v_exp_f16_sdwa v97, v85 dst_sel:WORD_1 dst_unused:UNUSED_PRESERVE src0_sel:WORD_1
	v_pk_add_f16 v77, v77, v94
	v_pk_add_f16 v76, v76, v95
	v_rcp_f16_e32 v82, v77
	v_rcp_f16_sdwa v77, v77 dst_sel:DWORD dst_unused:UNUSED_PAD src0_sel:WORD_1
	v_pk_add_f16 v75, v75, v96
	v_rcp_f16_e32 v83, v76
	v_rcp_f16_sdwa v76, v76 dst_sel:DWORD dst_unused:UNUSED_PAD src0_sel:WORD_1
	v_pk_add_f16 v74, v74, v97
	v_rcp_f16_e32 v84, v75
	v_rcp_f16_sdwa v75, v75 dst_sel:DWORD dst_unused:UNUSED_PAD src0_sel:WORD_1
	v_rcp_f16_e32 v85, v74
	v_rcp_f16_sdwa v74, v74 dst_sel:DWORD dst_unused:UNUSED_PAD src0_sel:WORD_1
	v_pk_fma_f16 v54, v26, v94, v54
	v_pack_b32_f16 v77, v82, v77
	v_pk_fma_f16 v55, v27, v95, v55
	v_pk_mul_f16 v77, v54, v77
	v_pack_b32_f16 v54, v83, v76
	v_pk_fma_f16 v56, v28, v96, v56
	v_pk_mul_f16 v76, v55, v54
	v_pack_b32_f16 v54, v84, v75
	v_pk_fma_f16 v57, v29, v97, v57
	v_pk_mul_f16 v75, v56, v54
	v_pack_b32_f16 v54, v85, v74
	v_pk_mul_f16 v74, v57, v54
	s_waitcnt vmcnt(6)
	v_pk_mul_f16 v57, v204, v161 op_sel_hi:[0,1]
	v_pk_mul_f16 v85, v202, v161 op_sel_hi:[0,1]
	v_pk_mul_f16 v97, v203, v161 op_sel_hi:[0,1]
	v_pk_mul_f16 v54, v204, v158 op_sel_hi:[0,1]
	v_pk_mul_f16 v55, v204, v159 op_sel_hi:[0,1]
	v_pk_mul_f16 v56, v204, v160 op_sel_hi:[0,1]
	v_pk_mul_f16 v82, v202, v158 op_sel_hi:[0,1]
	v_pk_mul_f16 v83, v202, v159 op_sel_hi:[0,1]
	v_pk_mul_f16 v84, v202, v160 op_sel_hi:[0,1]
	v_pk_mul_f16 v94, v203, v158 op_sel_hi:[0,1]
	v_pk_mul_f16 v95, v203, v159 op_sel_hi:[0,1]
	v_pk_mul_f16 v96, v203, v160 op_sel_hi:[0,1]
	v_pk_fma_f16 v65, v65, v161, v57
	v_pk_fma_f16 v81, v81, v161, v85
	v_pk_fma_f16 v98, v105, v161, v97
	v_pk_fma_f16 v64, v64, v160, v56
	v_pk_maximum3_f16 v125, v65, v81, v98
	v_pk_fma_f16 v63, v63, v159, v55
	v_pk_fma_f16 v62, v62, v158, v54
	v_pk_fma_f16 v80, v80, v160, v84
	v_pk_fma_f16 v79, v79, v159, v83
	v_pk_fma_f16 v78, v78, v158, v82
	v_pk_fma_f16 v99, v104, v160, v96
	v_pk_fma_f16 v100, v103, v159, v95
	v_pk_fma_f16 v101, v102, v158, v94
	v_pk_fma_f16 v102, v37, v161, v57
	v_pk_fma_f16 v106, v49, v161, v85
	v_pk_fma_f16 v118, v69, v161, v97
	v_pk_fma_f16 v57, v89, v161, v57
	v_pk_fma_f16 v85, v117, v161, v85
	v_pk_fma_f16 v97, v133, v161, v97
	v_pk_maximum3_f16 v122, v62, v78, v101
	v_pk_maximum3_f16 v123, v63, v79, v100
	v_pk_maximum3_f16 v124, v64, v80, v99
	v_pk_maximum3_f16 v129, v102, v106, v118
	v_pk_fma_f16 v103, v36, v160, v56
	v_pk_maximum3_f16 v137, v57, v85, v97
	v_pk_fma_f16 v104, v35, v159, v55
	v_pk_maximum3_f16 v125, v125, v129, v137
	v_pk_fma_f16 v105, v34, v158, v54
	v_pk_fma_f16 v107, v48, v160, v84
	v_pk_fma_f16 v108, v47, v159, v83
	v_pk_fma_f16 v109, v46, v158, v82
	v_pk_fma_f16 v119, v68, v160, v96
	v_pk_fma_f16 v120, v67, v159, v95
	v_pk_fma_f16 v121, v66, v158, v94
	v_pk_fma_f16 v56, v88, v160, v56
	v_pk_fma_f16 v55, v87, v159, v55
	v_pk_fma_f16 v54, v86, v158, v54
	v_pk_fma_f16 v84, v116, v160, v84
	v_pk_fma_f16 v83, v115, v159, v83
	v_pk_fma_f16 v82, v114, v158, v82
	v_pk_fma_f16 v96, v132, v160, v96
	v_pk_fma_f16 v95, v131, v159, v95
	v_pk_fma_f16 v94, v130, v158, v94
	v_pk_maximum3_f16 v126, v105, v109, v121
	v_pk_maximum3_f16 v127, v104, v108, v120
	v_pk_maximum3_f16 v128, v103, v107, v119
	v_pk_maximum3_f16 v135, v55, v83, v95
	v_pk_maximum3_f16 v136, v56, v84, v96
	v_pk_maximum3_f16 v134, v54, v82, v94
	v_pk_maximum3_f16 v122, v122, v126, v134
	v_pk_maximum3_f16 v123, v123, v127, v135
	v_pk_maximum3_f16 v124, v124, v128, v136
	v_pk_add_f16 v65, v65, v125 neg_lo:[0,1] neg_hi:[0,1]
	v_pk_add_f16 v62, v62, v122 neg_lo:[0,1] neg_hi:[0,1]
	v_pk_add_f16 v63, v63, v123 neg_lo:[0,1] neg_hi:[0,1]
	v_pk_add_f16 v64, v64, v124 neg_lo:[0,1] neg_hi:[0,1]
	v_pk_add_f16 v78, v78, v122 neg_lo:[0,1] neg_hi:[0,1]
	v_exp_f16_sdwa v126, v62 dst_sel:WORD_0 dst_unused:UNUSED_PAD src0_sel:WORD_0
	v_exp_f16_sdwa v127, v63 dst_sel:WORD_0 dst_unused:UNUSED_PAD src0_sel:WORD_0
	v_exp_f16_sdwa v128, v64 dst_sel:WORD_0 dst_unused:UNUSED_PAD src0_sel:WORD_0
	v_exp_f16_sdwa v129, v65 dst_sel:WORD_0 dst_unused:UNUSED_PAD src0_sel:WORD_0
	v_exp_f16_sdwa v126, v62 dst_sel:WORD_1 dst_unused:UNUSED_PRESERVE src0_sel:WORD_1
	v_exp_f16_sdwa v127, v63 dst_sel:WORD_1 dst_unused:UNUSED_PRESERVE src0_sel:WORD_1
	v_exp_f16_sdwa v128, v64 dst_sel:WORD_1 dst_unused:UNUSED_PRESERVE src0_sel:WORD_1
	v_exp_f16_sdwa v129, v65 dst_sel:WORD_1 dst_unused:UNUSED_PRESERVE src0_sel:WORD_1
	v_pk_add_f16 v79, v79, v123 neg_lo:[0,1] neg_hi:[0,1]
	v_pk_add_f16 v65, v126, 0
	v_pk_fma_f16 v33, v33, v129, 0
	v_pk_add_f16 v62, v129, 0
	v_pk_add_f16 v63, v128, 0
	v_pk_add_f16 v64, v127, 0
	v_pk_fma_f16 v32, v32, v128, 0
	v_pk_fma_f16 v31, v31, v127, 0
	v_pk_fma_f16 v30, v30, v126, 0
	v_pk_add_f16 v80, v80, v124 neg_lo:[0,1] neg_hi:[0,1]
	v_pk_add_f16 v81, v81, v125 neg_lo:[0,1] neg_hi:[0,1]
	v_pk_add_f16 v54, v54, v122 neg_lo:[0,1] neg_hi:[0,1]
	v_exp_f16_sdwa v126, v78 dst_sel:WORD_0 dst_unused:UNUSED_PAD src0_sel:WORD_0
	v_exp_f16_sdwa v127, v79 dst_sel:WORD_0 dst_unused:UNUSED_PAD src0_sel:WORD_0
	v_exp_f16_sdwa v128, v80 dst_sel:WORD_0 dst_unused:UNUSED_PAD src0_sel:WORD_0
	v_exp_f16_sdwa v129, v81 dst_sel:WORD_0 dst_unused:UNUSED_PAD src0_sel:WORD_0
	v_exp_f16_sdwa v126, v78 dst_sel:WORD_1 dst_unused:UNUSED_PRESERVE src0_sel:WORD_1
	v_exp_f16_sdwa v127, v79 dst_sel:WORD_1 dst_unused:UNUSED_PRESERVE src0_sel:WORD_1
	v_exp_f16_sdwa v128, v80 dst_sel:WORD_1 dst_unused:UNUSED_PRESERVE src0_sel:WORD_1
	v_exp_f16_sdwa v129, v81 dst_sel:WORD_1 dst_unused:UNUSED_PRESERVE src0_sel:WORD_1
	v_pk_add_f16 v55, v55, v123 neg_lo:[0,1] neg_hi:[0,1]
	v_pk_add_f16 v65, v65, v126
	v_pk_fma_f16 v33, v45, v129, v33
	v_pk_add_f16 v45, v98, v125 neg_lo:[0,1] neg_hi:[0,1]
	v_pk_add_f16 v64, v64, v127
	v_pk_add_f16 v63, v63, v128
	v_pk_add_f16 v62, v62, v129
	v_pk_fma_f16 v30, v42, v126, v30
	v_pk_fma_f16 v31, v43, v127, v31
	v_pk_fma_f16 v32, v44, v128, v32
	v_pk_add_f16 v42, v101, v122 neg_lo:[0,1] neg_hi:[0,1]
	v_pk_add_f16 v43, v100, v123 neg_lo:[0,1] neg_hi:[0,1]
	v_pk_add_f16 v44, v99, v124 neg_lo:[0,1] neg_hi:[0,1]
	v_pk_add_f16 v56, v56, v124 neg_lo:[0,1] neg_hi:[0,1]
	v_exp_f16_sdwa v78, v42 dst_sel:WORD_0 dst_unused:UNUSED_PAD src0_sel:WORD_0
	v_exp_f16_sdwa v79, v43 dst_sel:WORD_0 dst_unused:UNUSED_PAD src0_sel:WORD_0
	v_exp_f16_sdwa v80, v44 dst_sel:WORD_0 dst_unused:UNUSED_PAD src0_sel:WORD_0
	v_exp_f16_sdwa v81, v45 dst_sel:WORD_0 dst_unused:UNUSED_PAD src0_sel:WORD_0
	v_exp_f16_sdwa v78, v42 dst_sel:WORD_1 dst_unused:UNUSED_PRESERVE src0_sel:WORD_1
	v_exp_f16_sdwa v79, v43 dst_sel:WORD_1 dst_unused:UNUSED_PRESERVE src0_sel:WORD_1
	v_exp_f16_sdwa v80, v44 dst_sel:WORD_1 dst_unused:UNUSED_PRESERVE src0_sel:WORD_1
	v_exp_f16_sdwa v81, v45 dst_sel:WORD_1 dst_unused:UNUSED_PRESERVE src0_sel:WORD_1
	v_pk_add_f16 v57, v57, v125 neg_lo:[0,1] neg_hi:[0,1]
	v_pk_add_f16 v45, v65, v78
	v_pk_add_f16 v42, v62, v81
	v_pk_add_f16 v43, v63, v80
	v_pk_add_f16 v44, v64, v79
	v_pk_fma_f16 v33, v61, v81, v33
	v_pk_fma_f16 v32, v60, v80, v32
	v_pk_fma_f16 v31, v59, v79, v31
	v_pk_fma_f16 v30, v58, v78, v30
	v_pk_add_f16 v58, v105, v122 neg_lo:[0,1] neg_hi:[0,1]
	v_pk_add_f16 v59, v104, v123 neg_lo:[0,1] neg_hi:[0,1]
	v_pk_add_f16 v60, v103, v124 neg_lo:[0,1] neg_hi:[0,1]
	v_pk_add_f16 v61, v102, v125 neg_lo:[0,1] neg_hi:[0,1]
	v_exp_f16_sdwa v62, v58 dst_sel:WORD_0 dst_unused:UNUSED_PAD src0_sel:WORD_0
	v_exp_f16_sdwa v63, v59 dst_sel:WORD_0 dst_unused:UNUSED_PAD src0_sel:WORD_0
	v_exp_f16_sdwa v64, v60 dst_sel:WORD_0 dst_unused:UNUSED_PAD src0_sel:WORD_0
	v_exp_f16_sdwa v65, v61 dst_sel:WORD_0 dst_unused:UNUSED_PAD src0_sel:WORD_0
	v_exp_f16_sdwa v62, v58 dst_sel:WORD_1 dst_unused:UNUSED_PRESERVE src0_sel:WORD_1
	v_exp_f16_sdwa v63, v59 dst_sel:WORD_1 dst_unused:UNUSED_PRESERVE src0_sel:WORD_1
	v_exp_f16_sdwa v64, v60 dst_sel:WORD_1 dst_unused:UNUSED_PRESERVE src0_sel:WORD_1
	v_exp_f16_sdwa v65, v61 dst_sel:WORD_1 dst_unused:UNUSED_PRESERVE src0_sel:WORD_1
	v_pk_add_f16 v58, v109, v122 neg_lo:[0,1] neg_hi:[0,1]
	v_pk_add_f16 v45, v45, v62
	v_pk_add_f16 v44, v44, v63
	v_pk_add_f16 v43, v43, v64
	v_pk_add_f16 v42, v42, v65
	v_pk_fma_f16 v30, v18, v62, v30
	v_pk_fma_f16 v31, v19, v63, v31
	v_pk_fma_f16 v32, v20, v64, v32
	v_pk_fma_f16 v33, v21, v65, v33
	v_pk_add_f16 v59, v108, v123 neg_lo:[0,1] neg_hi:[0,1]
	v_pk_add_f16 v60, v107, v124 neg_lo:[0,1] neg_hi:[0,1]
	v_pk_add_f16 v61, v106, v125 neg_lo:[0,1] neg_hi:[0,1]
	v_exp_f16_sdwa v62, v58 dst_sel:WORD_0 dst_unused:UNUSED_PAD src0_sel:WORD_0
	v_exp_f16_sdwa v63, v59 dst_sel:WORD_0 dst_unused:UNUSED_PAD src0_sel:WORD_0
	v_exp_f16_sdwa v64, v60 dst_sel:WORD_0 dst_unused:UNUSED_PAD src0_sel:WORD_0
	v_exp_f16_sdwa v65, v61 dst_sel:WORD_0 dst_unused:UNUSED_PAD src0_sel:WORD_0
	v_exp_f16_sdwa v62, v58 dst_sel:WORD_1 dst_unused:UNUSED_PRESERVE src0_sel:WORD_1
	v_exp_f16_sdwa v63, v59 dst_sel:WORD_1 dst_unused:UNUSED_PRESERVE src0_sel:WORD_1
	v_exp_f16_sdwa v64, v60 dst_sel:WORD_1 dst_unused:UNUSED_PRESERVE src0_sel:WORD_1
	v_exp_f16_sdwa v65, v61 dst_sel:WORD_1 dst_unused:UNUSED_PRESERVE src0_sel:WORD_1
	v_pk_add_f16 v58, v121, v122 neg_lo:[0,1] neg_hi:[0,1]
	v_pk_add_f16 v45, v45, v62
	v_pk_add_f16 v42, v42, v65
	v_pk_add_f16 v43, v43, v64
	v_pk_add_f16 v44, v44, v63
	v_pk_fma_f16 v33, v25, v65, v33
	v_pk_fma_f16 v32, v24, v64, v32
	v_pk_fma_f16 v31, v23, v63, v31
	v_pk_fma_f16 v30, v22, v62, v30
	v_pk_add_f16 v59, v120, v123 neg_lo:[0,1] neg_hi:[0,1]
	v_pk_add_f16 v60, v119, v124 neg_lo:[0,1] neg_hi:[0,1]
	v_pk_add_f16 v61, v118, v125 neg_lo:[0,1] neg_hi:[0,1]
	v_exp_f16_sdwa v62, v58 dst_sel:WORD_0 dst_unused:UNUSED_PAD src0_sel:WORD_0
	v_exp_f16_sdwa v63, v59 dst_sel:WORD_0 dst_unused:UNUSED_PAD src0_sel:WORD_0
	v_exp_f16_sdwa v64, v60 dst_sel:WORD_0 dst_unused:UNUSED_PAD src0_sel:WORD_0
	v_exp_f16_sdwa v65, v61 dst_sel:WORD_0 dst_unused:UNUSED_PAD src0_sel:WORD_0
	v_exp_f16_sdwa v62, v58 dst_sel:WORD_1 dst_unused:UNUSED_PRESERVE src0_sel:WORD_1
	v_exp_f16_sdwa v63, v59 dst_sel:WORD_1 dst_unused:UNUSED_PRESERVE src0_sel:WORD_1
	v_exp_f16_sdwa v64, v60 dst_sel:WORD_1 dst_unused:UNUSED_PRESERVE src0_sel:WORD_1
	v_exp_f16_sdwa v65, v61 dst_sel:WORD_1 dst_unused:UNUSED_PRESERVE src0_sel:WORD_1
	v_exp_f16_sdwa v58, v54 dst_sel:WORD_0 dst_unused:UNUSED_PAD src0_sel:WORD_0
	v_exp_f16_sdwa v59, v55 dst_sel:WORD_0 dst_unused:UNUSED_PAD src0_sel:WORD_0
	v_exp_f16_sdwa v60, v56 dst_sel:WORD_0 dst_unused:UNUSED_PAD src0_sel:WORD_0
	v_exp_f16_sdwa v61, v57 dst_sel:WORD_0 dst_unused:UNUSED_PAD src0_sel:WORD_0
	v_exp_f16_sdwa v58, v54 dst_sel:WORD_1 dst_unused:UNUSED_PRESERVE src0_sel:WORD_1
	v_exp_f16_sdwa v59, v55 dst_sel:WORD_1 dst_unused:UNUSED_PRESERVE src0_sel:WORD_1
	v_exp_f16_sdwa v60, v56 dst_sel:WORD_1 dst_unused:UNUSED_PRESERVE src0_sel:WORD_1
	v_exp_f16_sdwa v61, v57 dst_sel:WORD_1 dst_unused:UNUSED_PRESERVE src0_sel:WORD_1
	v_pk_add_f16 v54, v82, v122 neg_lo:[0,1] neg_hi:[0,1]
	v_pk_add_f16 v45, v45, v62
	v_pk_add_f16 v44, v44, v63
	v_pk_add_f16 v43, v43, v64
	v_pk_add_f16 v42, v42, v65
	v_pk_fma_f16 v30, v26, v62, v30
	v_pk_fma_f16 v31, v27, v63, v31
	v_pk_fma_f16 v32, v28, v64, v32
	v_pk_fma_f16 v33, v29, v65, v33
	v_pk_add_f16 v45, v45, v58
	v_pk_add_f16 v42, v42, v61
	v_pk_add_f16 v43, v43, v60
	v_pk_add_f16 v44, v44, v59
	v_pk_fma_f16 v33, v41, v61, v33
	v_pk_fma_f16 v32, v40, v60, v32
	v_pk_fma_f16 v31, v39, v59, v31
	v_pk_fma_f16 v30, v38, v58, v30
	v_pk_add_f16 v55, v83, v123 neg_lo:[0,1] neg_hi:[0,1]
	v_pk_add_f16 v56, v84, v124 neg_lo:[0,1] neg_hi:[0,1]
	v_pk_add_f16 v57, v85, v125 neg_lo:[0,1] neg_hi:[0,1]
	v_exp_f16_sdwa v58, v54 dst_sel:WORD_0 dst_unused:UNUSED_PAD src0_sel:WORD_0
	v_exp_f16_sdwa v59, v55 dst_sel:WORD_0 dst_unused:UNUSED_PAD src0_sel:WORD_0
	v_exp_f16_sdwa v60, v56 dst_sel:WORD_0 dst_unused:UNUSED_PAD src0_sel:WORD_0
	v_exp_f16_sdwa v61, v57 dst_sel:WORD_0 dst_unused:UNUSED_PAD src0_sel:WORD_0
	v_exp_f16_sdwa v58, v54 dst_sel:WORD_1 dst_unused:UNUSED_PRESERVE src0_sel:WORD_1
	v_exp_f16_sdwa v59, v55 dst_sel:WORD_1 dst_unused:UNUSED_PRESERVE src0_sel:WORD_1
	v_exp_f16_sdwa v60, v56 dst_sel:WORD_1 dst_unused:UNUSED_PRESERVE src0_sel:WORD_1
	v_exp_f16_sdwa v61, v57 dst_sel:WORD_1 dst_unused:UNUSED_PRESERVE src0_sel:WORD_1
	v_pk_add_f16 v54, v94, v122 neg_lo:[0,1] neg_hi:[0,1]
	v_pk_add_f16 v45, v45, v58
	v_pk_add_f16 v44, v44, v59
	v_pk_add_f16 v43, v43, v60
	v_pk_add_f16 v42, v42, v61
	v_pk_fma_f16 v30, v50, v58, v30
	v_pk_fma_f16 v31, v51, v59, v31
	v_pk_fma_f16 v32, v52, v60, v32
	v_pk_fma_f16 v33, v53, v61, v33
	v_pk_add_f16 v55, v95, v123 neg_lo:[0,1] neg_hi:[0,1]
	v_pk_add_f16 v56, v96, v124 neg_lo:[0,1] neg_hi:[0,1]
	v_pk_add_f16 v57, v97, v125 neg_lo:[0,1] neg_hi:[0,1]
	v_exp_f16_sdwa v58, v54 dst_sel:WORD_0 dst_unused:UNUSED_PAD src0_sel:WORD_0
	v_exp_f16_sdwa v59, v55 dst_sel:WORD_0 dst_unused:UNUSED_PAD src0_sel:WORD_0
	v_exp_f16_sdwa v60, v56 dst_sel:WORD_0 dst_unused:UNUSED_PAD src0_sel:WORD_0
	v_exp_f16_sdwa v61, v57 dst_sel:WORD_0 dst_unused:UNUSED_PAD src0_sel:WORD_0
	v_exp_f16_sdwa v58, v54 dst_sel:WORD_1 dst_unused:UNUSED_PRESERVE src0_sel:WORD_1
	v_exp_f16_sdwa v59, v55 dst_sel:WORD_1 dst_unused:UNUSED_PRESERVE src0_sel:WORD_1
	v_exp_f16_sdwa v60, v56 dst_sel:WORD_1 dst_unused:UNUSED_PRESERVE src0_sel:WORD_1
	v_exp_f16_sdwa v61, v57 dst_sel:WORD_1 dst_unused:UNUSED_PRESERVE src0_sel:WORD_1
	v_pk_add_f16 v45, v45, v58
	v_pk_add_f16 v44, v44, v59
	v_rcp_f16_e32 v54, v45
	v_rcp_f16_sdwa v45, v45 dst_sel:DWORD dst_unused:UNUSED_PAD src0_sel:WORD_1
	v_pk_add_f16 v43, v43, v60
	v_rcp_f16_e32 v55, v44
	v_rcp_f16_sdwa v44, v44 dst_sel:DWORD dst_unused:UNUSED_PAD src0_sel:WORD_1
	v_pk_add_f16 v42, v42, v61
	v_pk_fma_f16 v30, v70, v58, v30
	v_rcp_f16_e32 v58, v43
	v_rcp_f16_sdwa v43, v43 dst_sel:DWORD dst_unused:UNUSED_PAD src0_sel:WORD_1
	v_pk_fma_f16 v31, v71, v59, v31
	v_rcp_f16_e32 v59, v42
	v_rcp_f16_sdwa v42, v42 dst_sel:DWORD dst_unused:UNUSED_PAD src0_sel:WORD_1
	v_pack_b32_f16 v45, v54, v45
	v_pk_mul_f16 v57, v30, v45
	v_pack_b32_f16 v30, v55, v44
	v_pk_fma_f16 v32, v72, v60, v32
	v_pk_mul_f16 v56, v31, v30
	v_pack_b32_f16 v30, v58, v43
	v_pk_fma_f16 v33, v73, v61, v33
	v_pk_mul_f16 v55, v32, v30
	v_pack_b32_f16 v30, v59, v42
	v_pk_mul_f16 v54, v33, v30
	s_waitcnt vmcnt(0)
	s_mov_b32 s14, s38
	s_mov_b32 s15, s39
	v_add_u32_e32 v250, 0x0, v251
	buffer_load_dwordx4 v[252:255], v250, s[12:15], 0 offen
	v_add_u32_e32 v250, 0xfffe7c00, v251
	buffer_load_dwordx4 v[252:255], v250, s[12:15], 0 offen
	v_add_u32_e32 v250, 0xfffe7e00, v251
	buffer_load_dwordx4 v[252:255], v250, s[12:15], 0 offen
	v_add_u32_e32 v250, 0xfffe8200, v251
	buffer_load_dwordx4 v[252:255], v250, s[12:15], 0 offen
	v_add_u32_e32 v250, 0xfffe8400, v251
	buffer_load_dwordx4 v[252:255], v250, s[12:15], 0 offen
	v_add_u32_e32 v250, 0xfffe8800, v251
	buffer_load_dwordx4 v[252:255], v250, s[12:15], 0 offen
	v_add_u32_e32 v250, 0xfffe8a00, v251
	buffer_load_dwordx4 v[252:255], v250, s[12:15], 0 offen
	v_add_u32_e32 v250, 0xfffffc00, v251
	buffer_load_dwordx4 v[252:255], v250, s[12:15], 0 offen
	v_add_u32_e32 v250, 0xfffffe00, v251
	buffer_load_dwordx4 v[252:255], v250, s[12:15], 0 offen
	v_add_u32_e32 v250, 0x200, v251
	buffer_load_dwordx4 v[252:255], v250, s[12:15], 0 offen
	v_add_u32_e32 v250, 0x400, v251
	buffer_load_dwordx4 v[252:255], v250, s[12:15], 0 offen
	v_add_u32_e32 v250, 0x800, v251
	buffer_load_dwordx4 v[252:255], v250, s[12:15], 0 offen
	v_add_u32_e32 v250, 0xa00, v251
	buffer_load_dwordx4 v[252:255], v250, s[12:15], 0 offen
	v_add_u32_e32 v250, 0x17c00, v251
	buffer_load_dwordx4 v[252:255], v250, s[12:15], 0 offen
	v_add_u32_e32 v250, 0x17e00, v251
	buffer_load_dwordx4 v[252:255], v250, s[12:15], 0 offen
	v_add_u32_e32 v250, 0x18200, v251
	buffer_load_dwordx4 v[252:255], v250, s[12:15], 0 offen
	v_add_u32_e32 v250, 0x18400, v251
	buffer_load_dwordx4 v[252:255], v250, s[12:15], 0 offen
	v_add_u32_e32 v250, 0x18800, v251
	buffer_load_dwordx4 v[252:255], v250, s[12:15], 0 offen
	v_add_u32_e32 v250, 0x18a00, v251
	buffer_load_dwordx4 v[252:255], v250, s[12:15], 0 offen
	v_add_u32_e32 v250, 0x18000, v251
	buffer_load_dwordx4 v[252:255], v250, s[12:15], 0 offen
	v_add_u32_e32 v250, 0x30000, v251
	buffer_load_dwordx4 v[252:255], v250, s[12:15], 0 offen
	v_add_u32_e32 v250, 0x48000, v251
	buffer_load_dwordx4 v[252:255], v250, s[12:15], 0 offen
	v_pk_mul_f16 v30, v204, v154 op_sel_hi:[0,1]
	v_pk_mul_f16 v31, v204, v155 op_sel_hi:[0,1]
	v_pk_mul_f16 v32, v204, v156 op_sel_hi:[0,1]
	v_pk_mul_f16 v33, v204, v157 op_sel_hi:[0,1]
	v_pk_mul_f16 v42, v202, v154 op_sel_hi:[0,1]
	v_pk_mul_f16 v43, v202, v155 op_sel_hi:[0,1]
	v_pk_mul_f16 v44, v202, v156 op_sel_hi:[0,1]
	v_pk_mul_f16 v45, v202, v157 op_sel_hi:[0,1]
	v_pk_mul_f16 v58, v203, v154 op_sel_hi:[0,1]
	v_pk_mul_f16 v59, v203, v155 op_sel_hi:[0,1]
	v_pk_mul_f16 v60, v203, v156 op_sel_hi:[0,1]
	v_pk_mul_f16 v61, v203, v157 op_sel_hi:[0,1]
	v_pk_fma_f16 v37, v37, v157, v33
	v_pk_fma_f16 v36, v36, v156, v32
	v_pk_fma_f16 v35, v35, v155, v31
	v_pk_fma_f16 v34, v34, v154, v30
	v_pk_fma_f16 v49, v49, v157, v45
	v_pk_fma_f16 v48, v48, v156, v44
	v_pk_fma_f16 v47, v47, v155, v43
	v_pk_fma_f16 v46, v46, v154, v42
	v_pk_fma_f16 v62, v69, v157, v61
	v_pk_fma_f16 v63, v68, v156, v60
	v_pk_fma_f16 v64, v67, v155, v59
	v_pk_fma_f16 v65, v66, v154, v58
	v_pk_fma_f16 v66, v89, v157, v33
	v_pk_fma_f16 v67, v88, v156, v32
	v_pk_fma_f16 v68, v87, v155, v31
	v_pk_fma_f16 v69, v86, v154, v30
	v_pk_fma_f16 v78, v117, v157, v45
	v_pk_fma_f16 v79, v116, v156, v44
	v_pk_fma_f16 v80, v115, v155, v43
	v_pk_fma_f16 v81, v114, v154, v42
	v_pk_fma_f16 v82, v133, v157, v61
	v_pk_fma_f16 v83, v132, v156, v60
	v_pk_fma_f16 v84, v131, v155, v59
	v_pk_fma_f16 v85, v130, v154, v58
	v_pk_fma_f16 v61, v17, v157, v61
	v_pk_fma_f16 v60, v16, v156, v60
	v_pk_fma_f16 v59, v15, v155, v59
	v_pk_fma_f16 v58, v14, v154, v58
	v_pk_maximum3_f16 v14, v34, v46, v65
	v_pk_maximum3_f16 v15, v35, v47, v64
	v_pk_maximum3_f16 v16, v36, v48, v63
	v_pk_maximum3_f16 v17, v37, v49, v62
	v_pk_maximum3_f16 v86, v69, v81, v85
	v_pk_maximum3_f16 v87, v68, v80, v84
	v_pk_maximum3_f16 v88, v67, v79, v83
	v_pk_maximum3_f16 v89, v66, v78, v82
	v_pk_fma_f16 v33, v145, v157, v33
	v_pk_fma_f16 v32, v144, v156, v32
	v_pk_fma_f16 v31, v143, v155, v31
	v_pk_fma_f16 v30, v142, v154, v30
	v_pk_fma_f16 v45, v153, v157, v45
	v_pk_fma_f16 v44, v152, v156, v44
	v_pk_fma_f16 v43, v151, v155, v43
	v_pk_fma_f16 v42, v150, v154, v42
	v_pk_maximum3_f16 v95, v31, v43, v59
	v_pk_maximum3_f16 v96, v32, v44, v60
	v_pk_maximum3_f16 v97, v33, v45, v61
	v_pk_maximum3_f16 v94, v30, v42, v58
	v_pk_maximum3_f16 v15, v15, v87, v95
	v_pk_maximum3_f16 v16, v16, v88, v96
	v_pk_maximum3_f16 v17, v17, v89, v97
	v_pk_maximum3_f16 v14, v14, v86, v94
	v_xor_b32_e32 v86, 0x80008000, v17
	v_xor_b32_e32 v87, 0x80008000, v16
	v_xor_b32_e32 v88, 0x80008000, v15
	v_xor_b32_e32 v89, 0x80008000, v14
	v_pk_add_f16 v14, v34, v89
	v_pk_add_f16 v15, v35, v88
	v_pk_add_f16 v16, v36, v87
	v_pk_add_f16 v17, v37, v86
	v_exp_f16_sdwa v34, v14 dst_sel:WORD_0 dst_unused:UNUSED_PAD src0_sel:WORD_0
	v_exp_f16_sdwa v35, v15 dst_sel:WORD_0 dst_unused:UNUSED_PAD src0_sel:WORD_0
	v_exp_f16_sdwa v36, v16 dst_sel:WORD_0 dst_unused:UNUSED_PAD src0_sel:WORD_0
	v_exp_f16_sdwa v37, v17 dst_sel:WORD_0 dst_unused:UNUSED_PAD src0_sel:WORD_0
	v_exp_f16_sdwa v34, v14 dst_sel:WORD_1 dst_unused:UNUSED_PRESERVE src0_sel:WORD_1
	v_exp_f16_sdwa v35, v15 dst_sel:WORD_1 dst_unused:UNUSED_PRESERVE src0_sel:WORD_1
	v_exp_f16_sdwa v36, v16 dst_sel:WORD_1 dst_unused:UNUSED_PRESERVE src0_sel:WORD_1
	v_exp_f16_sdwa v37, v17 dst_sel:WORD_1 dst_unused:UNUSED_PRESERVE src0_sel:WORD_1
	v_pk_add_f16 v14, v34, 0
	v_pk_add_f16 v15, v35, 0
	v_pk_add_f16 v16, v36, 0
	v_pk_add_f16 v17, v37, 0
	v_pk_fma_f16 v18, v18, v34, 0
	v_pk_fma_f16 v19, v19, v35, 0
	v_pk_fma_f16 v20, v20, v36, 0
	v_pk_fma_f16 v21, v21, v37, 0
	v_pk_add_f16 v34, v46, v89
	v_pk_add_f16 v35, v47, v88
	v_pk_add_f16 v36, v48, v87
	v_pk_add_f16 v37, v49, v86
	v_exp_f16_sdwa v46, v34 dst_sel:WORD_0 dst_unused:UNUSED_PAD src0_sel:WORD_0
	v_exp_f16_sdwa v47, v35 dst_sel:WORD_0 dst_unused:UNUSED_PAD src0_sel:WORD_0
	v_exp_f16_sdwa v48, v36 dst_sel:WORD_0 dst_unused:UNUSED_PAD src0_sel:WORD_0
	v_exp_f16_sdwa v49, v37 dst_sel:WORD_0 dst_unused:UNUSED_PAD src0_sel:WORD_0
	v_exp_f16_sdwa v46, v34 dst_sel:WORD_1 dst_unused:UNUSED_PRESERVE src0_sel:WORD_1
	v_exp_f16_sdwa v47, v35 dst_sel:WORD_1 dst_unused:UNUSED_PRESERVE src0_sel:WORD_1
	v_exp_f16_sdwa v48, v36 dst_sel:WORD_1 dst_unused:UNUSED_PRESERVE src0_sel:WORD_1
	v_exp_f16_sdwa v49, v37 dst_sel:WORD_1 dst_unused:UNUSED_PRESERVE src0_sel:WORD_1
	s_nop 0
	v_pk_add_f16 v17, v17, v49
	v_pk_add_f16 v16, v16, v48
	v_pk_add_f16 v15, v15, v47
	v_pk_add_f16 v14, v14, v46
	v_pk_fma_f16 v21, v25, v49, v21
	v_pk_fma_f16 v20, v24, v48, v20
	v_pk_fma_f16 v19, v23, v47, v19
	v_pk_fma_f16 v18, v22, v46, v18
	v_pk_add_f16 v22, v65, v89
	v_pk_add_f16 v23, v64, v88
	v_pk_add_f16 v24, v63, v87
	v_pk_add_f16 v25, v62, v86
	v_exp_f16_sdwa v34, v22 dst_sel:WORD_0 dst_unused:UNUSED_PAD src0_sel:WORD_0
	v_exp_f16_sdwa v35, v23 dst_sel:WORD_0 dst_unused:UNUSED_PAD src0_sel:WORD_0
	v_exp_f16_sdwa v36, v24 dst_sel:WORD_0 dst_unused:UNUSED_PAD src0_sel:WORD_0
	v_exp_f16_sdwa v37, v25 dst_sel:WORD_0 dst_unused:UNUSED_PAD src0_sel:WORD_0
	v_exp_f16_sdwa v34, v22 dst_sel:WORD_1 dst_unused:UNUSED_PRESERVE src0_sel:WORD_1
	v_exp_f16_sdwa v35, v23 dst_sel:WORD_1 dst_unused:UNUSED_PRESERVE src0_sel:WORD_1
	v_exp_f16_sdwa v36, v24 dst_sel:WORD_1 dst_unused:UNUSED_PRESERVE src0_sel:WORD_1
	v_exp_f16_sdwa v37, v25 dst_sel:WORD_1 dst_unused:UNUSED_PRESERVE src0_sel:WORD_1
	v_pk_add_f16 v22, v69, v89
	v_pk_add_f16 v14, v14, v34
	v_pk_add_f16 v15, v15, v35
	v_pk_add_f16 v16, v16, v36
	v_pk_add_f16 v17, v17, v37
	v_pk_fma_f16 v18, v26, v34, v18
	v_pk_fma_f16 v19, v27, v35, v19
	v_pk_fma_f16 v20, v28, v36, v20
	v_pk_fma_f16 v21, v29, v37, v21
	v_pk_add_f16 v23, v68, v88
	v_pk_add_f16 v24, v67, v87
	v_pk_add_f16 v25, v66, v86
	v_exp_f16_sdwa v26, v22 dst_sel:WORD_0 dst_unused:UNUSED_PAD src0_sel:WORD_0
	v_exp_f16_sdwa v27, v23 dst_sel:WORD_0 dst_unused:UNUSED_PAD src0_sel:WORD_0
	v_exp_f16_sdwa v28, v24 dst_sel:WORD_0 dst_unused:UNUSED_PAD src0_sel:WORD_0
	v_exp_f16_sdwa v29, v25 dst_sel:WORD_0 dst_unused:UNUSED_PAD src0_sel:WORD_0
	v_exp_f16_sdwa v26, v22 dst_sel:WORD_1 dst_unused:UNUSED_PRESERVE src0_sel:WORD_1
	v_exp_f16_sdwa v27, v23 dst_sel:WORD_1 dst_unused:UNUSED_PRESERVE src0_sel:WORD_1
	v_exp_f16_sdwa v28, v24 dst_sel:WORD_1 dst_unused:UNUSED_PRESERVE src0_sel:WORD_1
	v_exp_f16_sdwa v29, v25 dst_sel:WORD_1 dst_unused:UNUSED_PRESERVE src0_sel:WORD_1
	v_pk_add_f16 v22, v81, v89
	v_pk_add_f16 v17, v17, v29
	v_pk_add_f16 v16, v16, v28
	v_pk_add_f16 v15, v15, v27
	v_pk_add_f16 v14, v14, v26
	v_pk_fma_f16 v21, v41, v29, v21
	v_pk_fma_f16 v20, v40, v28, v20
	v_pk_fma_f16 v19, v39, v27, v19
	v_pk_fma_f16 v18, v38, v26, v18
	v_pk_add_f16 v23, v80, v88
	v_pk_add_f16 v24, v79, v87
	v_pk_add_f16 v25, v78, v86
	v_exp_f16_sdwa v26, v22 dst_sel:WORD_0 dst_unused:UNUSED_PAD src0_sel:WORD_0
	v_exp_f16_sdwa v27, v23 dst_sel:WORD_0 dst_unused:UNUSED_PAD src0_sel:WORD_0
	v_exp_f16_sdwa v28, v24 dst_sel:WORD_0 dst_unused:UNUSED_PAD src0_sel:WORD_0
	v_exp_f16_sdwa v29, v25 dst_sel:WORD_0 dst_unused:UNUSED_PAD src0_sel:WORD_0
	v_exp_f16_sdwa v26, v22 dst_sel:WORD_1 dst_unused:UNUSED_PRESERVE src0_sel:WORD_1
	v_exp_f16_sdwa v27, v23 dst_sel:WORD_1 dst_unused:UNUSED_PRESERVE src0_sel:WORD_1
	v_exp_f16_sdwa v28, v24 dst_sel:WORD_1 dst_unused:UNUSED_PRESERVE src0_sel:WORD_1
	v_exp_f16_sdwa v29, v25 dst_sel:WORD_1 dst_unused:UNUSED_PRESERVE src0_sel:WORD_1
	v_pk_add_f16 v22, v85, v89
	v_pk_add_f16 v14, v14, v26
	v_pk_add_f16 v15, v15, v27
	v_pk_add_f16 v16, v16, v28
	v_pk_add_f16 v17, v17, v29
	v_pk_fma_f16 v18, v50, v26, v18
	v_pk_fma_f16 v19, v51, v27, v19
	v_pk_fma_f16 v20, v52, v28, v20
	v_pk_fma_f16 v21, v53, v29, v21
	v_pk_add_f16 v23, v84, v88
	v_pk_add_f16 v24, v83, v87
	v_pk_add_f16 v25, v82, v86
	v_exp_f16_sdwa v26, v22 dst_sel:WORD_0 dst_unused:UNUSED_PAD src0_sel:WORD_0
	v_exp_f16_sdwa v27, v23 dst_sel:WORD_0 dst_unused:UNUSED_PAD src0_sel:WORD_0
	v_exp_f16_sdwa v28, v24 dst_sel:WORD_0 dst_unused:UNUSED_PAD src0_sel:WORD_0
	v_exp_f16_sdwa v29, v25 dst_sel:WORD_0 dst_unused:UNUSED_PAD src0_sel:WORD_0
	v_exp_f16_sdwa v26, v22 dst_sel:WORD_1 dst_unused:UNUSED_PRESERVE src0_sel:WORD_1
	v_exp_f16_sdwa v27, v23 dst_sel:WORD_1 dst_unused:UNUSED_PRESERVE src0_sel:WORD_1
	v_exp_f16_sdwa v28, v24 dst_sel:WORD_1 dst_unused:UNUSED_PRESERVE src0_sel:WORD_1
	v_exp_f16_sdwa v29, v25 dst_sel:WORD_1 dst_unused:UNUSED_PRESERVE src0_sel:WORD_1
	v_pk_add_f16 v22, v30, v89
	v_pk_add_f16 v17, v17, v29
	v_pk_add_f16 v16, v16, v28
	v_pk_add_f16 v15, v15, v27
	v_pk_add_f16 v14, v14, v26
	v_pk_fma_f16 v21, v73, v29, v21
	v_pk_fma_f16 v20, v72, v28, v20
	v_pk_fma_f16 v19, v71, v27, v19
	v_pk_fma_f16 v18, v70, v26, v18
	v_pk_add_f16 v23, v31, v88
	v_pk_add_f16 v24, v32, v87
	v_pk_add_f16 v25, v33, v86
	v_exp_f16_sdwa v26, v22 dst_sel:WORD_0 dst_unused:UNUSED_PAD src0_sel:WORD_0
	v_exp_f16_sdwa v27, v23 dst_sel:WORD_0 dst_unused:UNUSED_PAD src0_sel:WORD_0
	v_exp_f16_sdwa v28, v24 dst_sel:WORD_0 dst_unused:UNUSED_PAD src0_sel:WORD_0
	v_exp_f16_sdwa v29, v25 dst_sel:WORD_0 dst_unused:UNUSED_PAD src0_sel:WORD_0
	v_exp_f16_sdwa v26, v22 dst_sel:WORD_1 dst_unused:UNUSED_PRESERVE src0_sel:WORD_1
	v_exp_f16_sdwa v27, v23 dst_sel:WORD_1 dst_unused:UNUSED_PRESERVE src0_sel:WORD_1
	v_exp_f16_sdwa v28, v24 dst_sel:WORD_1 dst_unused:UNUSED_PRESERVE src0_sel:WORD_1
	v_exp_f16_sdwa v29, v25 dst_sel:WORD_1 dst_unused:UNUSED_PRESERVE src0_sel:WORD_1
	v_pk_add_f16 v22, v42, v89
	v_pk_add_f16 v14, v14, v26
	v_pk_add_f16 v15, v15, v27
	v_pk_add_f16 v16, v16, v28
	v_pk_add_f16 v17, v17, v29
	v_pk_fma_f16 v18, v90, v26, v18
	v_pk_fma_f16 v19, v91, v27, v19
	v_pk_fma_f16 v20, v92, v28, v20
	v_pk_fma_f16 v21, v93, v29, v21
	v_pk_add_f16 v23, v43, v88
	v_pk_add_f16 v24, v44, v87
	v_pk_add_f16 v25, v45, v86
	v_exp_f16_sdwa v26, v22 dst_sel:WORD_0 dst_unused:UNUSED_PAD src0_sel:WORD_0
	v_exp_f16_sdwa v27, v23 dst_sel:WORD_0 dst_unused:UNUSED_PAD src0_sel:WORD_0
	v_exp_f16_sdwa v28, v24 dst_sel:WORD_0 dst_unused:UNUSED_PAD src0_sel:WORD_0
	v_exp_f16_sdwa v29, v25 dst_sel:WORD_0 dst_unused:UNUSED_PAD src0_sel:WORD_0
	v_exp_f16_sdwa v26, v22 dst_sel:WORD_1 dst_unused:UNUSED_PRESERVE src0_sel:WORD_1
	v_exp_f16_sdwa v27, v23 dst_sel:WORD_1 dst_unused:UNUSED_PRESERVE src0_sel:WORD_1
	v_exp_f16_sdwa v28, v24 dst_sel:WORD_1 dst_unused:UNUSED_PRESERVE src0_sel:WORD_1
	v_exp_f16_sdwa v29, v25 dst_sel:WORD_1 dst_unused:UNUSED_PRESERVE src0_sel:WORD_1
	v_pk_add_f16 v22, v58, v89
	v_pk_add_f16 v17, v17, v29
	v_pk_add_f16 v16, v16, v28
	v_pk_add_f16 v15, v15, v27
	v_pk_add_f16 v14, v14, v26
	v_pk_fma_f16 v21, v113, v29, v21
	v_pk_fma_f16 v20, v112, v28, v20
	v_pk_fma_f16 v19, v111, v27, v19
	v_pk_fma_f16 v18, v110, v26, v18
	v_pk_add_f16 v23, v59, v88
	v_pk_add_f16 v24, v60, v87
	v_pk_add_f16 v25, v61, v86
	v_exp_f16_sdwa v30, v22 dst_sel:WORD_0 dst_unused:UNUSED_PAD src0_sel:WORD_0
	v_exp_f16_sdwa v31, v23 dst_sel:WORD_0 dst_unused:UNUSED_PAD src0_sel:WORD_0
	v_exp_f16_sdwa v32, v24 dst_sel:WORD_0 dst_unused:UNUSED_PAD src0_sel:WORD_0
	v_exp_f16_sdwa v33, v25 dst_sel:WORD_0 dst_unused:UNUSED_PAD src0_sel:WORD_0
	v_exp_f16_sdwa v30, v22 dst_sel:WORD_1 dst_unused:UNUSED_PRESERVE src0_sel:WORD_1
	v_exp_f16_sdwa v31, v23 dst_sel:WORD_1 dst_unused:UNUSED_PRESERVE src0_sel:WORD_1
	v_exp_f16_sdwa v32, v24 dst_sel:WORD_1 dst_unused:UNUSED_PRESERVE src0_sel:WORD_1
	v_exp_f16_sdwa v33, v25 dst_sel:WORD_1 dst_unused:UNUSED_PRESERVE src0_sel:WORD_1
	s_nop 0

.Lmyf_C2_7:
	s_mov_b64 exec, -1
	s_waitcnt vmcnt(21)
	v_cvt_f16_f32_e32 v158, v147
	v_cvt_f16_f32_e32 v160, v146
	v_cvt_f16_f32_e32 v159, v148
	v_add_u32_e32 v251, 0x48000, v200
	buffer_load_dwordx4 v[146:149], v251, s[36:39], 0 offen
	v_mov_b32_e32 v251, v200
	s_waitcnt vmcnt(3)
	v_pk_mul_f16 v161, v160, v162 op_sel_hi:[0,1]
	v_pk_mul_f16 v204, v160, v165 op_sel_hi:[0,1]
	v_pk_mul_f16 v208, v158, v165 op_sel_hi:[0,1]
	v_pk_mul_f16 v212, v159, v165 op_sel_hi:[0,1]
	v_pk_mul_f16 v202, v160, v163 op_sel_hi:[0,1]
	v_pk_mul_f16 v203, v160, v164 op_sel_hi:[0,1]
	v_pk_mul_f16 v205, v158, v162 op_sel_hi:[0,1]
	s_mov_b64 exec, s[64:65]
	buffer_load_dwordx4 v[26:29], v245, s[36:39], 0 offen
	buffer_load_dwordx4 v[10:13], v245, s[36:39], 0 offen offset:512
	s_mov_b64 exec, -1
	v_pk_mul_f16 v206, v158, v163 op_sel_hi:[0,1]
	v_pk_mul_f16 v207, v158, v164 op_sel_hi:[0,1]
	v_pk_mul_f16 v209, v159, v162 op_sel_hi:[0,1]
	v_pk_mul_f16 v210, v159, v163 op_sel_hi:[0,1]
	v_pk_mul_f16 v211, v159, v164 op_sel_hi:[0,1]
	v_pk_fma_f16 v117, v117, v165, v204
	v_pk_fma_f16 v114, v114, v162, v161
	v_pk_fma_f16 v133, v133, v165, v204
	v_pk_fma_f16 v130, v130, v162, v161
	v_pk_fma_f16 v141, v141, v165, v204
	v_pk_fma_f16 v138, v138, v162, v161
	v_pk_fma_f16 v161, v89, v165, v208
	v_pk_fma_f16 v213, v113, v165, v208
	buffer_load_dwordx4 v[38:41], v246, s[36:39], 0 offen offset:512
	buffer_load_dwordx4 v[14:17], v246, s[36:39], 0 offen offset:1024
	v_pk_fma_f16 v208, v129, v165, v208
	v_pk_fma_f16 v217, v57, v165, v212
	v_pk_fma_f16 v221, v73, v165, v212
	v_pk_fma_f16 v165, v97, v165, v212
	v_pk_maximum3_f16 v212, v117, v133, v141
	v_pk_fma_f16 v116, v116, v164, v203
	v_pk_fma_f16 v115, v115, v163, v202
	v_pk_fma_f16 v132, v132, v164, v203
	v_pk_fma_f16 v131, v131, v163, v202
	v_pk_fma_f16 v140, v140, v164, v203
	v_pk_fma_f16 v139, v139, v163, v202
	v_pk_fma_f16 v202, v88, v164, v207
	v_pk_fma_f16 v203, v87, v163, v206
	v_pk_fma_f16 v204, v86, v162, v205
	v_pk_fma_f16 v214, v112, v164, v207
	v_pk_fma_f16 v215, v111, v163, v206
	s_mov_b64 exec, s[66:67]
	buffer_load_dwordx4 v[58:61], v246, s[36:39], 0 offen offset:2048
	buffer_load_dwordx4 v[18:21], v246, s[36:39], 0 offen offset:2560
	s_mov_b64 exec, -1
	v_pk_fma_f16 v216, v110, v162, v205
	v_pk_fma_f16 v207, v128, v164, v207
	v_pk_fma_f16 v206, v127, v163, v206
	v_pk_fma_f16 v205, v126, v162, v205
	v_pk_fma_f16 v218, v56, v164, v211
	v_pk_fma_f16 v219, v55, v163, v210
	v_pk_fma_f16 v220, v54, v162, v209
	v_pk_fma_f16 v222, v72, v164, v211
	v_pk_fma_f16 v223, v71, v163, v210
	v_pk_fma_f16 v224, v70, v162, v209
	v_pk_fma_f16 v164, v96, v164, v211
	v_pk_fma_f16 v163, v95, v163, v210
	v_pk_fma_f16 v162, v94, v162, v209
	v_pk_maximum3_f16 v209, v114, v130, v138
	v_pk_maximum3_f16 v210, v115, v131, v139
	v_pk_maximum3_f16 v211, v116, v132, v140
	v_pk_maximum3_f16 v228, v161, v213, v208
	v_pk_maximum3_f16 v232, v217, v221, v165
	v_pk_maximum3_f16 v225, v204, v216, v205
	v_pk_maximum3_f16 v226, v203, v215, v206
	v_pk_maximum3_f16 v227, v202, v214, v207
	v_pk_maximum3_f16 v229, v220, v224, v162
	v_pk_maximum3_f16 v230, v219, v223, v163
	v_pk_maximum3_f16 v212, v212, v228, v232
	v_pk_maximum3_f16 v231, v218, v222, v164
	v_pk_maximum3_f16 v209, v209, v225, v229
	v_pk_maximum3_f16 v210, v210, v226, v230
	v_pk_maximum3_f16 v211, v211, v227, v231
	v_pk_add_f16 v117, v117, v212 neg_lo:[0,1] neg_hi:[0,1]
	s_mov_b64 exec, s[64:65]
	buffer_load_dwordx4 v[78:81], v247, s[36:39], 0 offen
	buffer_load_dwordx4 v[30:33], v247, s[36:39], 0 offen offset:512
	s_mov_b64 exec, -1
	v_pk_add_f16 v114, v114, v209 neg_lo:[0,1] neg_hi:[0,1]
	v_pk_add_f16 v115, v115, v210 neg_lo:[0,1] neg_hi:[0,1]
	v_pk_add_f16 v116, v116, v211 neg_lo:[0,1] neg_hi:[0,1]
	v_pk_add_f16 v130, v130, v209 neg_lo:[0,1] neg_hi:[0,1]
	v_exp_f16_sdwa v225, v114 dst_sel:WORD_0 dst_unused:UNUSED_PAD src0_sel:WORD_0
	v_exp_f16_sdwa v226, v115 dst_sel:WORD_0 dst_unused:UNUSED_PAD src0_sel:WORD_0
	v_exp_f16_sdwa v227, v116 dst_sel:WORD_0 dst_unused:UNUSED_PAD src0_sel:WORD_0
	v_exp_f16_sdwa v228, v117 dst_sel:WORD_0 dst_unused:UNUSED_PAD src0_sel:WORD_0
	v_exp_f16_sdwa v225, v114 dst_sel:WORD_1 dst_unused:UNUSED_PRESERVE src0_sel:WORD_1
	v_exp_f16_sdwa v226, v115 dst_sel:WORD_1 dst_unused:UNUSED_PRESERVE src0_sel:WORD_1
	v_exp_f16_sdwa v227, v116 dst_sel:WORD_1 dst_unused:UNUSED_PRESERVE src0_sel:WORD_1
	v_exp_f16_sdwa v228, v117 dst_sel:WORD_1 dst_unused:UNUSED_PRESERVE src0_sel:WORD_1
	v_pk_add_f16 v131, v131, v210 neg_lo:[0,1] neg_hi:[0,1]
	v_pk_add_f16 v117, v225, 0
	v_pk_fma_f16 v77, v77, v228, 0
	v_pk_add_f16 v114, v228, 0
	v_pk_add_f16 v115, v227, 0
	v_pk_add_f16 v116, v226, 0
	v_pk_fma_f16 v76, v76, v227, 0
	v_pk_fma_f16 v75, v75, v226, 0
	v_pk_fma_f16 v74, v74, v225, 0
	v_pk_add_f16 v132, v132, v211 neg_lo:[0,1] neg_hi:[0,1]
	buffer_load_dwordx4 v[106:109], v248, s[36:39], 0 offen offset:512
	buffer_load_dwordx4 v[42:45], v248, s[36:39], 0 offen offset:1024
	v_pk_add_f16 v133, v133, v212 neg_lo:[0,1] neg_hi:[0,1]
	v_exp_f16_sdwa v225, v130 dst_sel:WORD_0 dst_unused:UNUSED_PAD src0_sel:WORD_0
	v_exp_f16_sdwa v226, v131 dst_sel:WORD_0 dst_unused:UNUSED_PAD src0_sel:WORD_0
	v_exp_f16_sdwa v227, v132 dst_sel:WORD_0 dst_unused:UNUSED_PAD src0_sel:WORD_0
	v_exp_f16_sdwa v228, v133 dst_sel:WORD_0 dst_unused:UNUSED_PAD src0_sel:WORD_0
	v_exp_f16_sdwa v225, v130 dst_sel:WORD_1 dst_unused:UNUSED_PRESERVE src0_sel:WORD_1
	v_exp_f16_sdwa v226, v131 dst_sel:WORD_1 dst_unused:UNUSED_PRESERVE src0_sel:WORD_1
	v_exp_f16_sdwa v227, v132 dst_sel:WORD_1 dst_unused:UNUSED_PRESERVE src0_sel:WORD_1
	v_exp_f16_sdwa v228, v133 dst_sel:WORD_1 dst_unused:UNUSED_PRESERVE src0_sel:WORD_1
	v_pk_add_f16 v117, v117, v225
	v_pk_fma_f16 v77, v101, v228, v77
	v_pk_add_f16 v101, v141, v212 neg_lo:[0,1] neg_hi:[0,1]
	v_pk_add_f16 v116, v116, v226
	v_pk_add_f16 v115, v115, v227
	v_pk_add_f16 v114, v114, v228
	v_pk_fma_f16 v74, v98, v225, v74
	v_pk_fma_f16 v75, v99, v226, v75
	v_pk_fma_f16 v76, v100, v227, v76
	v_pk_add_f16 v98, v138, v209 neg_lo:[0,1] neg_hi:[0,1]
	v_pk_add_f16 v99, v139, v210 neg_lo:[0,1] neg_hi:[0,1]
	v_pk_add_f16 v100, v140, v211 neg_lo:[0,1] neg_hi:[0,1]
	v_exp_f16_sdwa v130, v98 dst_sel:WORD_0 dst_unused:UNUSED_PAD src0_sel:WORD_0
	v_exp_f16_sdwa v131, v99 dst_sel:WORD_0 dst_unused:UNUSED_PAD src0_sel:WORD_0
	v_exp_f16_sdwa v132, v100 dst_sel:WORD_0 dst_unused:UNUSED_PAD src0_sel:WORD_0
	v_exp_f16_sdwa v133, v101 dst_sel:WORD_0 dst_unused:UNUSED_PAD src0_sel:WORD_0
	v_exp_f16_sdwa v130, v98 dst_sel:WORD_1 dst_unused:UNUSED_PRESERVE src0_sel:WORD_1
	v_exp_f16_sdwa v131, v99 dst_sel:WORD_1 dst_unused:UNUSED_PRESERVE src0_sel:WORD_1
	v_exp_f16_sdwa v132, v100 dst_sel:WORD_1 dst_unused:UNUSED_PRESERVE src0_sel:WORD_1
	v_exp_f16_sdwa v133, v101 dst_sel:WORD_1 dst_unused:UNUSED_PRESERVE src0_sel:WORD_1
	v_pk_add_f16 v101, v117, v130
	v_pk_add_f16 v98, v114, v133
	s_mov_b64 exec, s[66:67]
	buffer_load_dwordx4 v[122:125], v248, s[36:39], 0 offen offset:2048
	buffer_load_dwordx4 v[62:65], v248, s[36:39], 0 offen offset:2560
	s_mov_b64 exec, -1
	v_pk_add_f16 v99, v115, v132
	v_pk_add_f16 v100, v116, v131
	v_pk_fma_f16 v77, v121, v133, v77
	v_pk_fma_f16 v76, v120, v132, v76
	v_pk_fma_f16 v75, v119, v131, v75
	v_pk_fma_f16 v74, v118, v130, v74
	v_pk_add_f16 v114, v204, v209 neg_lo:[0,1] neg_hi:[0,1]
	v_pk_add_f16 v115, v203, v210 neg_lo:[0,1] neg_hi:[0,1]
	v_pk_add_f16 v116, v202, v211 neg_lo:[0,1] neg_hi:[0,1]
	v_pk_add_f16 v117, v161, v212 neg_lo:[0,1] neg_hi:[0,1]
	v_exp_f16_sdwa v118, v114 dst_sel:WORD_0 dst_unused:UNUSED_PAD src0_sel:WORD_0
	v_exp_f16_sdwa v119, v115 dst_sel:WORD_0 dst_unused:UNUSED_PAD src0_sel:WORD_0
	v_exp_f16_sdwa v120, v116 dst_sel:WORD_0 dst_unused:UNUSED_PAD src0_sel:WORD_0
	v_exp_f16_sdwa v121, v117 dst_sel:WORD_0 dst_unused:UNUSED_PAD src0_sel:WORD_0
	v_exp_f16_sdwa v118, v114 dst_sel:WORD_1 dst_unused:UNUSED_PRESERVE src0_sel:WORD_1
	v_exp_f16_sdwa v119, v115 dst_sel:WORD_1 dst_unused:UNUSED_PRESERVE src0_sel:WORD_1
	v_exp_f16_sdwa v120, v116 dst_sel:WORD_1 dst_unused:UNUSED_PRESERVE src0_sel:WORD_1
	v_exp_f16_sdwa v121, v117 dst_sel:WORD_1 dst_unused:UNUSED_PRESERVE src0_sel:WORD_1
	v_pk_add_f16 v114, v216, v209 neg_lo:[0,1] neg_hi:[0,1]
	v_pk_add_f16 v101, v101, v118
	v_pk_add_f16 v100, v100, v119
	v_pk_add_f16 v99, v99, v120
	s_mov_b64 exec, s[76:77]
	buffer_load_dwordx4 v[134:137], v249, s[36:39], 0 offen
	buffer_load_dwordx4 v[82:85], v249, s[36:39], 0 offen offset:512
	s_mov_b64 exec, -1
	v_pk_add_f16 v98, v98, v121
	v_pk_fma_f16 v74, v46, v118, v74
	v_pk_fma_f16 v75, v47, v119, v75
	v_pk_fma_f16 v76, v48, v120, v76
	v_pk_fma_f16 v77, v49, v121, v77
	v_pk_add_f16 v115, v215, v210 neg_lo:[0,1] neg_hi:[0,1]
	v_pk_add_f16 v116, v214, v211 neg_lo:[0,1] neg_hi:[0,1]
	v_pk_add_f16 v117, v213, v212 neg_lo:[0,1] neg_hi:[0,1]
	v_exp_f16_sdwa v118, v114 dst_sel:WORD_0 dst_unused:UNUSED_PAD src0_sel:WORD_0
	v_exp_f16_sdwa v119, v115 dst_sel:WORD_0 dst_unused:UNUSED_PAD src0_sel:WORD_0
	v_exp_f16_sdwa v120, v116 dst_sel:WORD_0 dst_unused:UNUSED_PAD src0_sel:WORD_0
	v_exp_f16_sdwa v121, v117 dst_sel:WORD_0 dst_unused:UNUSED_PAD src0_sel:WORD_0
	v_exp_f16_sdwa v118, v114 dst_sel:WORD_1 dst_unused:UNUSED_PRESERVE src0_sel:WORD_1
	v_exp_f16_sdwa v119, v115 dst_sel:WORD_1 dst_unused:UNUSED_PRESERVE src0_sel:WORD_1
	v_exp_f16_sdwa v120, v116 dst_sel:WORD_1 dst_unused:UNUSED_PRESERVE src0_sel:WORD_1
	v_exp_f16_sdwa v121, v117 dst_sel:WORD_1 dst_unused:UNUSED_PRESERVE src0_sel:WORD_1
	v_pk_add_f16 v114, v205, v209 neg_lo:[0,1] neg_hi:[0,1]
	v_pk_add_f16 v101, v101, v118
	v_pk_add_f16 v98, v98, v121
	v_pk_add_f16 v99, v99, v120
	v_pk_add_f16 v100, v100, v119
	v_pk_fma_f16 v77, v69, v121, v77
	v_pk_fma_f16 v76, v68, v120, v76
	s_mov_b64 exec, s[70:71]
	buffer_load_dwordx4 v[142:145], v250, s[36:39], 0 offen offset:512
	buffer_load_dwordx4 v[102:105], v250, s[36:39], 0 offen offset:1024
	s_mov_b64 exec, -1
	v_pk_fma_f16 v75, v67, v119, v75
	v_pk_fma_f16 v74, v66, v118, v74
	v_pk_add_f16 v115, v206, v210 neg_lo:[0,1] neg_hi:[0,1]
	v_pk_add_f16 v116, v207, v211 neg_lo:[0,1] neg_hi:[0,1]
	v_pk_add_f16 v117, v208, v212 neg_lo:[0,1] neg_hi:[0,1]
	v_exp_f16_sdwa v118, v114 dst_sel:WORD_0 dst_unused:UNUSED_PAD src0_sel:WORD_0
	v_exp_f16_sdwa v119, v115 dst_sel:WORD_0 dst_unused:UNUSED_PAD src0_sel:WORD_0
	v_exp_f16_sdwa v120, v116 dst_sel:WORD_0 dst_unused:UNUSED_PAD src0_sel:WORD_0
	v_exp_f16_sdwa v121, v117 dst_sel:WORD_0 dst_unused:UNUSED_PAD src0_sel:WORD_0
	v_exp_f16_sdwa v118, v114 dst_sel:WORD_1 dst_unused:UNUSED_PRESERVE src0_sel:WORD_1
	v_exp_f16_sdwa v119, v115 dst_sel:WORD_1 dst_unused:UNUSED_PRESERVE src0_sel:WORD_1
	v_exp_f16_sdwa v120, v116 dst_sel:WORD_1 dst_unused:UNUSED_PRESERVE src0_sel:WORD_1
	v_exp_f16_sdwa v121, v117 dst_sel:WORD_1 dst_unused:UNUSED_PRESERVE src0_sel:WORD_1
	v_pk_add_f16 v114, v220, v209 neg_lo:[0,1] neg_hi:[0,1]
	v_pk_add_f16 v101, v101, v118
	v_pk_add_f16 v100, v100, v119
	v_pk_add_f16 v99, v99, v120
	v_pk_add_f16 v98, v98, v121
	v_pk_fma_f16 v74, v90, v118, v74
	v_pk_fma_f16 v75, v91, v119, v75
	v_pk_fma_f16 v76, v92, v120, v76
	v_pk_fma_f16 v77, v93, v121, v77
	s_mov_b64 exec, s[78:79]
	buffer_load_dwordx4 v[6:9], v250, s[36:39], 0 offen offset:2048
	buffer_load_dwordx4 v[2:5], v250, s[36:39], 0 offen offset:2560
	s_mov_b64 exec, -1
	v_pk_add_f16 v115, v219, v210 neg_lo:[0,1] neg_hi:[0,1]
	v_pk_add_f16 v116, v218, v211 neg_lo:[0,1] neg_hi:[0,1]
	v_pk_add_f16 v117, v217, v212 neg_lo:[0,1] neg_hi:[0,1]
	v_exp_f16_sdwa v118, v114 dst_sel:WORD_0 dst_unused:UNUSED_PAD src0_sel:WORD_0
	v_exp_f16_sdwa v119, v115 dst_sel:WORD_0 dst_unused:UNUSED_PAD src0_sel:WORD_0
	v_exp_f16_sdwa v120, v116 dst_sel:WORD_0 dst_unused:UNUSED_PAD src0_sel:WORD_0
	v_exp_f16_sdwa v121, v117 dst_sel:WORD_0 dst_unused:UNUSED_PAD src0_sel:WORD_0
	v_exp_f16_sdwa v118, v114 dst_sel:WORD_1 dst_unused:UNUSED_PRESERVE src0_sel:WORD_1
	v_exp_f16_sdwa v119, v115 dst_sel:WORD_1 dst_unused:UNUSED_PRESERVE src0_sel:WORD_1
	v_exp_f16_sdwa v120, v116 dst_sel:WORD_1 dst_unused:UNUSED_PRESERVE src0_sel:WORD_1
	v_exp_f16_sdwa v121, v117 dst_sel:WORD_1 dst_unused:UNUSED_PRESERVE src0_sel:WORD_1
	v_pk_add_f16 v114, v224, v209 neg_lo:[0,1] neg_hi:[0,1]
	v_pk_add_f16 v101, v101, v118
	v_pk_add_f16 v98, v98, v121
	v_pk_add_f16 v99, v99, v120
	v_pk_add_f16 v100, v100, v119
	v_pk_fma_f16 v77, v25, v121, v77
	v_pk_fma_f16 v76, v24, v120, v76
	v_pk_fma_f16 v75, v23, v119, v75
	v_pk_fma_f16 v74, v22, v118, v74
	v_pk_add_f16 v115, v223, v210 neg_lo:[0,1] neg_hi:[0,1]
	v_pk_add_f16 v116, v222, v211 neg_lo:[0,1] neg_hi:[0,1]
	v_pk_add_f16 v117, v221, v212 neg_lo:[0,1] neg_hi:[0,1]
	v_exp_f16_sdwa v118, v114 dst_sel:WORD_0 dst_unused:UNUSED_PAD src0_sel:WORD_0
	v_exp_f16_sdwa v119, v115 dst_sel:WORD_0 dst_unused:UNUSED_PAD src0_sel:WORD_0
	v_exp_f16_sdwa v120, v116 dst_sel:WORD_0 dst_unused:UNUSED_PAD src0_sel:WORD_0
	v_exp_f16_sdwa v121, v117 dst_sel:WORD_0 dst_unused:UNUSED_PAD src0_sel:WORD_0
	v_exp_f16_sdwa v118, v114 dst_sel:WORD_1 dst_unused:UNUSED_PRESERVE src0_sel:WORD_1
	v_exp_f16_sdwa v119, v115 dst_sel:WORD_1 dst_unused:UNUSED_PRESERVE src0_sel:WORD_1
	v_exp_f16_sdwa v120, v116 dst_sel:WORD_1 dst_unused:UNUSED_PRESERVE src0_sel:WORD_1
	v_exp_f16_sdwa v121, v117 dst_sel:WORD_1 dst_unused:UNUSED_PRESERVE src0_sel:WORD_1
	v_pk_add_f16 v114, v162, v209 neg_lo:[0,1] neg_hi:[0,1]
	v_pk_add_f16 v101, v101, v118
	v_pk_add_f16 v100, v100, v119
	v_pk_add_f16 v99, v99, v120
	v_pk_add_f16 v98, v98, v121
	v_pk_fma_f16 v74, v34, v118, v74
	v_pk_fma_f16 v75, v35, v119, v75
	v_pk_fma_f16 v76, v36, v120, v76
	v_pk_fma_f16 v77, v37, v121, v77
	v_pk_add_f16 v115, v163, v210 neg_lo:[0,1] neg_hi:[0,1]
	v_pk_add_f16 v116, v164, v211 neg_lo:[0,1] neg_hi:[0,1]
	v_pk_add_f16 v117, v165, v212 neg_lo:[0,1] neg_hi:[0,1]
	v_exp_f16_sdwa v118, v114 dst_sel:WORD_0 dst_unused:UNUSED_PAD src0_sel:WORD_0
	v_exp_f16_sdwa v119, v115 dst_sel:WORD_0 dst_unused:UNUSED_PAD src0_sel:WORD_0
	v_exp_f16_sdwa v120, v116 dst_sel:WORD_0 dst_unused:UNUSED_PAD src0_sel:WORD_0
	v_exp_f16_sdwa v121, v117 dst_sel:WORD_0 dst_unused:UNUSED_PAD src0_sel:WORD_0
	v_exp_f16_sdwa v118, v114 dst_sel:WORD_1 dst_unused:UNUSED_PRESERVE src0_sel:WORD_1
	v_exp_f16_sdwa v119, v115 dst_sel:WORD_1 dst_unused:UNUSED_PRESERVE src0_sel:WORD_1
	v_exp_f16_sdwa v120, v116 dst_sel:WORD_1 dst_unused:UNUSED_PRESERVE src0_sel:WORD_1
	v_exp_f16_sdwa v121, v117 dst_sel:WORD_1 dst_unused:UNUSED_PRESERVE src0_sel:WORD_1
	v_pk_add_f16 v101, v101, v118
	v_pk_add_f16 v100, v100, v119
	v_rcp_f16_e32 v114, v101
	v_rcp_f16_sdwa v101, v101 dst_sel:DWORD dst_unused:UNUSED_PAD src0_sel:WORD_1
	v_pk_add_f16 v99, v99, v120
	v_rcp_f16_e32 v115, v100
	v_rcp_f16_sdwa v100, v100 dst_sel:DWORD dst_unused:UNUSED_PAD src0_sel:WORD_1
	v_pk_add_f16 v98, v98, v121
	v_rcp_f16_e32 v116, v99
	v_rcp_f16_sdwa v99, v99 dst_sel:DWORD dst_unused:UNUSED_PAD src0_sel:WORD_1
	v_rcp_f16_e32 v117, v98
	v_rcp_f16_sdwa v98, v98 dst_sel:DWORD dst_unused:UNUSED_PAD src0_sel:WORD_1
	v_pk_fma_f16 v74, v50, v118, v74
	v_pack_b32_f16 v101, v114, v101
	v_pk_fma_f16 v75, v51, v119, v75
	v_pk_mul_f16 v138, v74, v101
	v_pack_b32_f16 v74, v115, v100
	v_pk_fma_f16 v76, v52, v120, v76
	v_pk_mul_f16 v139, v75, v74
	v_pack_b32_f16 v74, v116, v99
	v_pk_fma_f16 v77, v53, v121, v77
	v_pk_mul_f16 v140, v76, v74
	v_pack_b32_f16 v74, v117, v98
	v_pk_mul_f16 v141, v77, v74
	s_waitcnt vmcnt(12)
	v_pk_mul_f16 v74, v160, v154 op_sel_hi:[0,1]
	v_pk_mul_f16 v77, v160, v157 op_sel_hi:[0,1]
	v_pk_mul_f16 v101, v158, v157 op_sel_hi:[0,1]
	v_pk_mul_f16 v117, v159, v157 op_sel_hi:[0,1]
	v_pk_mul_f16 v75, v160, v155 op_sel_hi:[0,1]
	v_pk_mul_f16 v76, v160, v156 op_sel_hi:[0,1]
	v_pk_mul_f16 v98, v158, v154 op_sel_hi:[0,1]
	v_pk_mul_f16 v99, v158, v155 op_sel_hi:[0,1]
	v_pk_mul_f16 v100, v158, v156 op_sel_hi:[0,1]
	v_pk_mul_f16 v114, v159, v154 op_sel_hi:[0,1]
	v_pk_mul_f16 v115, v159, v155 op_sel_hi:[0,1]
	v_pk_mul_f16 v116, v159, v156 op_sel_hi:[0,1]
	v_pk_fma_f16 v89, v89, v157, v77
	v_pk_fma_f16 v86, v86, v154, v74
	v_pk_fma_f16 v113, v113, v157, v77
	v_pk_fma_f16 v110, v110, v154, v74
	v_pk_fma_f16 v77, v129, v157, v77
	v_pk_fma_f16 v74, v126, v154, v74
	v_pk_fma_f16 v118, v57, v157, v101
	v_pk_fma_f16 v126, v73, v157, v101
	v_pk_fma_f16 v101, v97, v157, v101
	v_pk_fma_f16 v130, v29, v157, v117
	v_pk_fma_f16 v161, v41, v157, v117
	v_pk_fma_f16 v117, v61, v157, v117
	v_pk_maximum3_f16 v157, v89, v113, v77
	v_pk_fma_f16 v88, v88, v156, v76
	v_pk_fma_f16 v87, v87, v155, v75
	v_pk_fma_f16 v112, v112, v156, v76
	v_pk_fma_f16 v111, v111, v155, v75
	v_pk_fma_f16 v76, v128, v156, v76
	v_pk_fma_f16 v75, v127, v155, v75
	v_pk_fma_f16 v119, v56, v156, v100
	v_pk_fma_f16 v120, v55, v155, v99
	v_pk_fma_f16 v121, v54, v154, v98
	v_pk_fma_f16 v127, v72, v156, v100
	v_pk_fma_f16 v128, v71, v155, v99
	v_pk_fma_f16 v129, v70, v154, v98
	v_pk_fma_f16 v100, v96, v156, v100
	v_pk_fma_f16 v99, v95, v155, v99
	v_pk_fma_f16 v98, v94, v154, v98
	v_pk_fma_f16 v131, v28, v156, v116
	v_pk_fma_f16 v132, v27, v155, v115
	v_pk_fma_f16 v133, v26, v154, v114
	v_pk_fma_f16 v162, v40, v156, v116
	v_pk_fma_f16 v163, v39, v155, v115
	v_pk_fma_f16 v164, v38, v154, v114
	v_pk_fma_f16 v116, v60, v156, v116
	v_pk_fma_f16 v115, v59, v155, v115
	v_pk_fma_f16 v114, v58, v154, v114
	v_pk_maximum3_f16 v154, v86, v110, v74
	v_pk_maximum3_f16 v155, v87, v111, v75
	v_pk_maximum3_f16 v156, v88, v112, v76
	v_pk_maximum3_f16 v204, v118, v126, v101
	v_pk_maximum3_f16 v208, v130, v161, v117
	v_pk_maximum3_f16 v165, v121, v129, v98
	v_pk_maximum3_f16 v202, v120, v128, v99
	v_pk_maximum3_f16 v203, v119, v127, v100
	v_pk_maximum3_f16 v205, v133, v164, v114
	v_pk_maximum3_f16 v206, v132, v163, v115
	v_pk_maximum3_f16 v157, v157, v204, v208
	v_pk_maximum3_f16 v207, v131, v162, v116
	v_pk_maximum3_f16 v154, v154, v165, v205
	v_pk_maximum3_f16 v155, v155, v202, v206
	v_pk_maximum3_f16 v156, v156, v203, v207
	v_pk_add_f16 v89, v89, v157 neg_lo:[0,1] neg_hi:[0,1]
	v_pk_add_f16 v86, v86, v154 neg_lo:[0,1] neg_hi:[0,1]
	v_pk_add_f16 v87, v87, v155 neg_lo:[0,1] neg_hi:[0,1]
	v_pk_add_f16 v88, v88, v156 neg_lo:[0,1] neg_hi:[0,1]
	v_pk_add_f16 v110, v110, v154 neg_lo:[0,1] neg_hi:[0,1]
	v_exp_f16_sdwa v165, v86 dst_sel:WORD_0 dst_unused:UNUSED_PAD src0_sel:WORD_0
	v_exp_f16_sdwa v202, v87 dst_sel:WORD_0 dst_unused:UNUSED_PAD src0_sel:WORD_0
	v_exp_f16_sdwa v203, v88 dst_sel:WORD_0 dst_unused:UNUSED_PAD src0_sel:WORD_0
	v_exp_f16_sdwa v204, v89 dst_sel:WORD_0 dst_unused:UNUSED_PAD src0_sel:WORD_0
	v_exp_f16_sdwa v165, v86 dst_sel:WORD_1 dst_unused:UNUSED_PRESERVE src0_sel:WORD_1
	v_exp_f16_sdwa v202, v87 dst_sel:WORD_1 dst_unused:UNUSED_PRESERVE src0_sel:WORD_1
	v_exp_f16_sdwa v203, v88 dst_sel:WORD_1 dst_unused:UNUSED_PRESERVE src0_sel:WORD_1
	v_exp_f16_sdwa v204, v89 dst_sel:WORD_1 dst_unused:UNUSED_PRESERVE src0_sel:WORD_1
	v_pk_add_f16 v111, v111, v155 neg_lo:[0,1] neg_hi:[0,1]
	v_pk_add_f16 v89, v165, 0
	v_pk_fma_f16 v49, v49, v204, 0
	v_pk_add_f16 v86, v204, 0
	v_pk_add_f16 v87, v203, 0
	v_pk_add_f16 v88, v202, 0
	v_pk_fma_f16 v48, v48, v203, 0
	v_pk_fma_f16 v47, v47, v202, 0
	v_pk_fma_f16 v46, v46, v165, 0
	v_pk_add_f16 v112, v112, v156 neg_lo:[0,1] neg_hi:[0,1]
	v_pk_add_f16 v113, v113, v157 neg_lo:[0,1] neg_hi:[0,1]
	v_exp_f16_sdwa v165, v110 dst_sel:WORD_0 dst_unused:UNUSED_PAD src0_sel:WORD_0
	v_exp_f16_sdwa v202, v111 dst_sel:WORD_0 dst_unused:UNUSED_PAD src0_sel:WORD_0
	v_exp_f16_sdwa v203, v112 dst_sel:WORD_0 dst_unused:UNUSED_PAD src0_sel:WORD_0
	v_exp_f16_sdwa v204, v113 dst_sel:WORD_0 dst_unused:UNUSED_PAD src0_sel:WORD_0
	v_exp_f16_sdwa v165, v110 dst_sel:WORD_1 dst_unused:UNUSED_PRESERVE src0_sel:WORD_1
	v_exp_f16_sdwa v202, v111 dst_sel:WORD_1 dst_unused:UNUSED_PRESERVE src0_sel:WORD_1
	v_exp_f16_sdwa v203, v112 dst_sel:WORD_1 dst_unused:UNUSED_PRESERVE src0_sel:WORD_1
	v_exp_f16_sdwa v204, v113 dst_sel:WORD_1 dst_unused:UNUSED_PRESERVE src0_sel:WORD_1
	v_pk_add_f16 v89, v89, v165
	v_pk_fma_f16 v49, v69, v204, v49
	v_pk_add_f16 v69, v77, v157 neg_lo:[0,1] neg_hi:[0,1]
	v_pk_add_f16 v88, v88, v202
	v_pk_add_f16 v87, v87, v203
	v_pk_add_f16 v86, v86, v204
	v_pk_fma_f16 v46, v66, v165, v46
	v_pk_fma_f16 v47, v67, v202, v47
	v_pk_fma_f16 v48, v68, v203, v48
	v_pk_add_f16 v66, v74, v154 neg_lo:[0,1] neg_hi:[0,1]
	v_pk_add_f16 v67, v75, v155 neg_lo:[0,1] neg_hi:[0,1]
	v_pk_add_f16 v68, v76, v156 neg_lo:[0,1] neg_hi:[0,1]
	v_exp_f16_sdwa v74, v66 dst_sel:WORD_0 dst_unused:UNUSED_PAD src0_sel:WORD_0
	v_exp_f16_sdwa v75, v67 dst_sel:WORD_0 dst_unused:UNUSED_PAD src0_sel:WORD_0
	v_exp_f16_sdwa v76, v68 dst_sel:WORD_0 dst_unused:UNUSED_PAD src0_sel:WORD_0
	v_exp_f16_sdwa v77, v69 dst_sel:WORD_0 dst_unused:UNUSED_PAD src0_sel:WORD_0
	v_exp_f16_sdwa v74, v66 dst_sel:WORD_1 dst_unused:UNUSED_PRESERVE src0_sel:WORD_1
	v_exp_f16_sdwa v75, v67 dst_sel:WORD_1 dst_unused:UNUSED_PRESERVE src0_sel:WORD_1
	v_exp_f16_sdwa v76, v68 dst_sel:WORD_1 dst_unused:UNUSED_PRESERVE src0_sel:WORD_1
	v_exp_f16_sdwa v77, v69 dst_sel:WORD_1 dst_unused:UNUSED_PRESERVE src0_sel:WORD_1
	v_pk_add_f16 v69, v89, v74
	v_pk_add_f16 v66, v86, v77
	v_pk_add_f16 v67, v87, v76
	v_pk_add_f16 v68, v88, v75
	v_pk_fma_f16 v49, v93, v77, v49
	v_pk_fma_f16 v48, v92, v76, v48
	v_pk_fma_f16 v47, v91, v75, v47
	v_pk_fma_f16 v46, v90, v74, v46
	v_pk_add_f16 v74, v121, v154 neg_lo:[0,1] neg_hi:[0,1]
	v_pk_add_f16 v75, v120, v155 neg_lo:[0,1] neg_hi:[0,1]
	v_pk_add_f16 v76, v119, v156 neg_lo:[0,1] neg_hi:[0,1]
	v_pk_add_f16 v77, v118, v157 neg_lo:[0,1] neg_hi:[0,1]
	v_exp_f16_sdwa v86, v74 dst_sel:WORD_0 dst_unused:UNUSED_PAD src0_sel:WORD_0
	v_exp_f16_sdwa v87, v75 dst_sel:WORD_0 dst_unused:UNUSED_PAD src0_sel:WORD_0
	v_exp_f16_sdwa v88, v76 dst_sel:WORD_0 dst_unused:UNUSED_PAD src0_sel:WORD_0
	v_exp_f16_sdwa v89, v77 dst_sel:WORD_0 dst_unused:UNUSED_PAD src0_sel:WORD_0
	v_exp_f16_sdwa v86, v74 dst_sel:WORD_1 dst_unused:UNUSED_PRESERVE src0_sel:WORD_1
	v_exp_f16_sdwa v87, v75 dst_sel:WORD_1 dst_unused:UNUSED_PRESERVE src0_sel:WORD_1
	v_exp_f16_sdwa v88, v76 dst_sel:WORD_1 dst_unused:UNUSED_PRESERVE src0_sel:WORD_1
	v_exp_f16_sdwa v89, v77 dst_sel:WORD_1 dst_unused:UNUSED_PRESERVE src0_sel:WORD_1
	v_pk_add_f16 v74, v129, v154 neg_lo:[0,1] neg_hi:[0,1]
	v_pk_add_f16 v69, v69, v86
	v_pk_add_f16 v68, v68, v87
	v_pk_add_f16 v67, v67, v88
	v_pk_add_f16 v66, v66, v89
	v_pk_fma_f16 v46, v22, v86, v46
	v_pk_fma_f16 v47, v23, v87, v47
	v_pk_fma_f16 v48, v24, v88, v48
	v_pk_fma_f16 v49, v25, v89, v49
	v_pk_add_f16 v75, v128, v155 neg_lo:[0,1] neg_hi:[0,1]
	v_pk_add_f16 v76, v127, v156 neg_lo:[0,1] neg_hi:[0,1]
	v_pk_add_f16 v77, v126, v157 neg_lo:[0,1] neg_hi:[0,1]
	v_exp_f16_sdwa v86, v74 dst_sel:WORD_0 dst_unused:UNUSED_PAD src0_sel:WORD_0
	v_exp_f16_sdwa v87, v75 dst_sel:WORD_0 dst_unused:UNUSED_PAD src0_sel:WORD_0
	v_exp_f16_sdwa v88, v76 dst_sel:WORD_0 dst_unused:UNUSED_PAD src0_sel:WORD_0
	v_exp_f16_sdwa v89, v77 dst_sel:WORD_0 dst_unused:UNUSED_PAD src0_sel:WORD_0
	v_exp_f16_sdwa v86, v74 dst_sel:WORD_1 dst_unused:UNUSED_PRESERVE src0_sel:WORD_1
	v_exp_f16_sdwa v87, v75 dst_sel:WORD_1 dst_unused:UNUSED_PRESERVE src0_sel:WORD_1
	v_exp_f16_sdwa v88, v76 dst_sel:WORD_1 dst_unused:UNUSED_PRESERVE src0_sel:WORD_1
	v_exp_f16_sdwa v89, v77 dst_sel:WORD_1 dst_unused:UNUSED_PRESERVE src0_sel:WORD_1
	v_pk_add_f16 v74, v98, v154 neg_lo:[0,1] neg_hi:[0,1]
	v_pk_add_f16 v69, v69, v86
	v_pk_add_f16 v66, v66, v89
	v_pk_add_f16 v67, v67, v88
	v_pk_add_f16 v68, v68, v87
	v_pk_fma_f16 v49, v37, v89, v49
	v_pk_fma_f16 v48, v36, v88, v48
	v_pk_fma_f16 v47, v35, v87, v47
	v_pk_fma_f16 v46, v34, v86, v46
	v_pk_add_f16 v75, v99, v155 neg_lo:[0,1] neg_hi:[0,1]
	v_pk_add_f16 v76, v100, v156 neg_lo:[0,1] neg_hi:[0,1]
	v_pk_add_f16 v77, v101, v157 neg_lo:[0,1] neg_hi:[0,1]
	v_exp_f16_sdwa v86, v74 dst_sel:WORD_0 dst_unused:UNUSED_PAD src0_sel:WORD_0
	v_exp_f16_sdwa v87, v75 dst_sel:WORD_0 dst_unused:UNUSED_PAD src0_sel:WORD_0
	v_exp_f16_sdwa v88, v76 dst_sel:WORD_0 dst_unused:UNUSED_PAD src0_sel:WORD_0
	v_exp_f16_sdwa v89, v77 dst_sel:WORD_0 dst_unused:UNUSED_PAD src0_sel:WORD_0
	v_exp_f16_sdwa v86, v74 dst_sel:WORD_1 dst_unused:UNUSED_PRESERVE src0_sel:WORD_1
	v_exp_f16_sdwa v87, v75 dst_sel:WORD_1 dst_unused:UNUSED_PRESERVE src0_sel:WORD_1
	v_exp_f16_sdwa v88, v76 dst_sel:WORD_1 dst_unused:UNUSED_PRESERVE src0_sel:WORD_1
	v_exp_f16_sdwa v89, v77 dst_sel:WORD_1 dst_unused:UNUSED_PRESERVE src0_sel:WORD_1
	v_pk_add_f16 v74, v133, v154 neg_lo:[0,1] neg_hi:[0,1]
	v_pk_add_f16 v69, v69, v86
	v_pk_add_f16 v68, v68, v87
	v_pk_add_f16 v67, v67, v88
	v_pk_add_f16 v66, v66, v89
	v_pk_fma_f16 v46, v50, v86, v46
	v_pk_fma_f16 v47, v51, v87, v47
	v_pk_fma_f16 v48, v52, v88, v48
	v_pk_fma_f16 v49, v53, v89, v49
	v_pk_add_f16 v75, v132, v155 neg_lo:[0,1] neg_hi:[0,1]
	v_pk_add_f16 v76, v131, v156 neg_lo:[0,1] neg_hi:[0,1]
	v_pk_add_f16 v77, v130, v157 neg_lo:[0,1] neg_hi:[0,1]
	v_exp_f16_sdwa v86, v74 dst_sel:WORD_0 dst_unused:UNUSED_PAD src0_sel:WORD_0
	v_exp_f16_sdwa v87, v75 dst_sel:WORD_0 dst_unused:UNUSED_PAD src0_sel:WORD_0
	v_exp_f16_sdwa v88, v76 dst_sel:WORD_0 dst_unused:UNUSED_PAD src0_sel:WORD_0
	v_exp_f16_sdwa v89, v77 dst_sel:WORD_0 dst_unused:UNUSED_PAD src0_sel:WORD_0
	v_exp_f16_sdwa v86, v74 dst_sel:WORD_1 dst_unused:UNUSED_PRESERVE src0_sel:WORD_1
	v_exp_f16_sdwa v87, v75 dst_sel:WORD_1 dst_unused:UNUSED_PRESERVE src0_sel:WORD_1
	v_exp_f16_sdwa v88, v76 dst_sel:WORD_1 dst_unused:UNUSED_PRESERVE src0_sel:WORD_1
	v_exp_f16_sdwa v89, v77 dst_sel:WORD_1 dst_unused:UNUSED_PRESERVE src0_sel:WORD_1
	v_pk_add_f16 v74, v164, v154 neg_lo:[0,1] neg_hi:[0,1]
	v_pk_add_f16 v69, v69, v86
	v_pk_add_f16 v66, v66, v89
	v_pk_add_f16 v67, v67, v88
	v_pk_add_f16 v68, v68, v87
	v_pk_fma_f16 v49, v13, v89, v49
	v_pk_fma_f16 v48, v12, v88, v48
	v_pk_fma_f16 v47, v11, v87, v47
	v_pk_fma_f16 v46, v10, v86, v46
	v_pk_add_f16 v75, v163, v155 neg_lo:[0,1] neg_hi:[0,1]
	v_pk_add_f16 v76, v162, v156 neg_lo:[0,1] neg_hi:[0,1]
	v_pk_add_f16 v77, v161, v157 neg_lo:[0,1] neg_hi:[0,1]
	v_exp_f16_sdwa v86, v74 dst_sel:WORD_0 dst_unused:UNUSED_PAD src0_sel:WORD_0
	v_exp_f16_sdwa v87, v75 dst_sel:WORD_0 dst_unused:UNUSED_PAD src0_sel:WORD_0
	v_exp_f16_sdwa v88, v76 dst_sel:WORD_0 dst_unused:UNUSED_PAD src0_sel:WORD_0
	v_exp_f16_sdwa v89, v77 dst_sel:WORD_0 dst_unused:UNUSED_PAD src0_sel:WORD_0
	v_exp_f16_sdwa v86, v74 dst_sel:WORD_1 dst_unused:UNUSED_PRESERVE src0_sel:WORD_1
	v_exp_f16_sdwa v87, v75 dst_sel:WORD_1 dst_unused:UNUSED_PRESERVE src0_sel:WORD_1
	v_exp_f16_sdwa v88, v76 dst_sel:WORD_1 dst_unused:UNUSED_PRESERVE src0_sel:WORD_1
	v_exp_f16_sdwa v89, v77 dst_sel:WORD_1 dst_unused:UNUSED_PRESERVE src0_sel:WORD_1
	v_pk_add_f16 v74, v114, v154 neg_lo:[0,1] neg_hi:[0,1]
	v_pk_add_f16 v69, v69, v86
	v_pk_add_f16 v68, v68, v87
	v_pk_add_f16 v67, v67, v88
	v_pk_add_f16 v66, v66, v89
	v_pk_fma_f16 v46, v14, v86, v46
	v_pk_fma_f16 v47, v15, v87, v47
	v_pk_fma_f16 v48, v16, v88, v48
	v_pk_fma_f16 v49, v17, v89, v49
	v_pk_add_f16 v75, v115, v155 neg_lo:[0,1] neg_hi:[0,1]
	v_pk_add_f16 v76, v116, v156 neg_lo:[0,1] neg_hi:[0,1]
	v_pk_add_f16 v77, v117, v157 neg_lo:[0,1] neg_hi:[0,1]
	v_exp_f16_sdwa v86, v74 dst_sel:WORD_0 dst_unused:UNUSED_PAD src0_sel:WORD_0
	v_exp_f16_sdwa v87, v75 dst_sel:WORD_0 dst_unused:UNUSED_PAD src0_sel:WORD_0
	v_exp_f16_sdwa v88, v76 dst_sel:WORD_0 dst_unused:UNUSED_PAD src0_sel:WORD_0
	v_exp_f16_sdwa v89, v77 dst_sel:WORD_0 dst_unused:UNUSED_PAD src0_sel:WORD_0
	v_exp_f16_sdwa v86, v74 dst_sel:WORD_1 dst_unused:UNUSED_PRESERVE src0_sel:WORD_1
	v_exp_f16_sdwa v87, v75 dst_sel:WORD_1 dst_unused:UNUSED_PRESERVE src0_sel:WORD_1
	v_exp_f16_sdwa v88, v76 dst_sel:WORD_1 dst_unused:UNUSED_PRESERVE src0_sel:WORD_1
	v_exp_f16_sdwa v89, v77 dst_sel:WORD_1 dst_unused:UNUSED_PRESERVE src0_sel:WORD_1
	v_pk_add_f16 v69, v69, v86
	v_pk_add_f16 v68, v68, v87
	v_rcp_f16_e32 v74, v69
	v_rcp_f16_sdwa v69, v69 dst_sel:DWORD dst_unused:UNUSED_PAD src0_sel:WORD_1
	v_pk_add_f16 v67, v67, v88
	v_rcp_f16_e32 v75, v68
	v_rcp_f16_sdwa v68, v68 dst_sel:DWORD dst_unused:UNUSED_PAD src0_sel:WORD_1
	v_pk_add_f16 v66, v66, v89
	v_pk_fma_f16 v46, v18, v86, v46
	v_rcp_f16_e32 v86, v67
	v_rcp_f16_sdwa v67, v67 dst_sel:DWORD dst_unused:UNUSED_PAD src0_sel:WORD_1
	v_pk_fma_f16 v47, v19, v87, v47
	v_rcp_f16_e32 v87, v66
	v_rcp_f16_sdwa v66, v66 dst_sel:DWORD dst_unused:UNUSED_PAD src0_sel:WORD_1
	v_pack_b32_f16 v69, v74, v69
	v_pk_mul_f16 v77, v46, v69
	v_pack_b32_f16 v46, v75, v68
	v_pk_fma_f16 v48, v20, v88, v48
	v_pk_mul_f16 v76, v47, v46
	v_pack_b32_f16 v46, v86, v67
	v_pk_fma_f16 v49, v21, v89, v49
	v_pk_mul_f16 v75, v48, v46
	v_pack_b32_f16 v46, v87, v66
	v_pk_mul_f16 v74, v49, v46
	s_waitcnt vmcnt(6)
	v_pk_mul_f16 v49, v160, v153 op_sel_hi:[0,1]
	v_pk_mul_f16 v46, v160, v150 op_sel_hi:[0,1]
	v_pk_mul_f16 v47, v160, v151 op_sel_hi:[0,1]
	v_pk_mul_f16 v48, v160, v152 op_sel_hi:[0,1]
	v_pk_mul_f16 v69, v158, v153 op_sel_hi:[0,1]
	v_pk_mul_f16 v89, v159, v153 op_sel_hi:[0,1]
	v_pk_fma_f16 v57, v57, v153, v49
	v_pk_fma_f16 v73, v73, v153, v49
	v_pk_fma_f16 v49, v97, v153, v49
	v_pk_mul_f16 v66, v158, v150 op_sel_hi:[0,1]
	v_pk_maximum3_f16 v117, v57, v73, v49
	v_pk_mul_f16 v67, v158, v151 op_sel_hi:[0,1]
	v_pk_mul_f16 v68, v158, v152 op_sel_hi:[0,1]
	v_pk_mul_f16 v86, v159, v150 op_sel_hi:[0,1]
	v_pk_mul_f16 v87, v159, v151 op_sel_hi:[0,1]
	v_pk_mul_f16 v88, v159, v152 op_sel_hi:[0,1]
	v_pk_fma_f16 v56, v56, v152, v48
	v_pk_fma_f16 v55, v55, v151, v47
	v_pk_fma_f16 v54, v54, v150, v46
	v_pk_fma_f16 v72, v72, v152, v48
	v_pk_fma_f16 v71, v71, v151, v47
	v_pk_fma_f16 v70, v70, v150, v46
	v_pk_fma_f16 v48, v96, v152, v48
	v_pk_fma_f16 v47, v95, v151, v47
	v_pk_fma_f16 v46, v94, v150, v46
	v_pk_fma_f16 v90, v29, v153, v69
	v_pk_fma_f16 v94, v41, v153, v69
	v_pk_fma_f16 v69, v61, v153, v69
	v_pk_fma_f16 v98, v81, v153, v89
	v_pk_fma_f16 v110, v109, v153, v89
	v_pk_fma_f16 v89, v125, v153, v89
	v_pk_maximum3_f16 v114, v54, v70, v46
	v_pk_maximum3_f16 v115, v55, v71, v47
	v_pk_maximum3_f16 v116, v56, v72, v48
	v_pk_maximum3_f16 v121, v90, v94, v69
	v_pk_fma_f16 v91, v28, v152, v68
	v_pk_maximum3_f16 v129, v98, v110, v89
	v_pk_fma_f16 v92, v27, v151, v67
	v_pk_maximum3_f16 v117, v117, v121, v129
	v_pk_fma_f16 v93, v26, v150, v66
	v_pk_fma_f16 v95, v40, v152, v68
	v_pk_fma_f16 v96, v39, v151, v67
	v_pk_fma_f16 v97, v38, v150, v66
	v_pk_fma_f16 v68, v60, v152, v68
	v_pk_fma_f16 v67, v59, v151, v67
	v_pk_fma_f16 v66, v58, v150, v66
	v_pk_fma_f16 v99, v80, v152, v88
	v_pk_fma_f16 v100, v79, v151, v87
	v_pk_fma_f16 v101, v78, v150, v86
	v_pk_fma_f16 v111, v108, v152, v88
	v_pk_fma_f16 v112, v107, v151, v87
	v_pk_fma_f16 v113, v106, v150, v86
	v_pk_fma_f16 v88, v124, v152, v88
	v_pk_fma_f16 v87, v123, v151, v87
	v_pk_fma_f16 v86, v122, v150, v86
	v_pk_maximum3_f16 v118, v93, v97, v66
	v_pk_maximum3_f16 v119, v92, v96, v67
	v_pk_maximum3_f16 v120, v91, v95, v68
	v_pk_maximum3_f16 v127, v100, v112, v87
	v_pk_maximum3_f16 v128, v99, v111, v88
	v_pk_maximum3_f16 v126, v101, v113, v86
	v_pk_maximum3_f16 v114, v114, v118, v126
	v_pk_maximum3_f16 v115, v115, v119, v127
	v_pk_maximum3_f16 v116, v116, v120, v128
	v_pk_add_f16 v57, v57, v117 neg_lo:[0,1] neg_hi:[0,1]
	v_pk_add_f16 v54, v54, v114 neg_lo:[0,1] neg_hi:[0,1]
	v_pk_add_f16 v55, v55, v115 neg_lo:[0,1] neg_hi:[0,1]
	v_pk_add_f16 v56, v56, v116 neg_lo:[0,1] neg_hi:[0,1]
	v_pk_add_f16 v70, v70, v114 neg_lo:[0,1] neg_hi:[0,1]
	v_exp_f16_sdwa v118, v54 dst_sel:WORD_0 dst_unused:UNUSED_PAD src0_sel:WORD_0
	v_exp_f16_sdwa v119, v55 dst_sel:WORD_0 dst_unused:UNUSED_PAD src0_sel:WORD_0
	v_exp_f16_sdwa v120, v56 dst_sel:WORD_0 dst_unused:UNUSED_PAD src0_sel:WORD_0
	v_exp_f16_sdwa v121, v57 dst_sel:WORD_0 dst_unused:UNUSED_PAD src0_sel:WORD_0
	v_exp_f16_sdwa v118, v54 dst_sel:WORD_1 dst_unused:UNUSED_PRESERVE src0_sel:WORD_1
	v_exp_f16_sdwa v119, v55 dst_sel:WORD_1 dst_unused:UNUSED_PRESERVE src0_sel:WORD_1
	v_exp_f16_sdwa v120, v56 dst_sel:WORD_1 dst_unused:UNUSED_PRESERVE src0_sel:WORD_1
	v_exp_f16_sdwa v121, v57 dst_sel:WORD_1 dst_unused:UNUSED_PRESERVE src0_sel:WORD_1
	v_pk_add_f16 v71, v71, v115 neg_lo:[0,1] neg_hi:[0,1]
	v_pk_add_f16 v57, v118, 0
	v_pk_fma_f16 v25, v25, v121, 0
	v_pk_add_f16 v54, v121, 0
	v_pk_add_f16 v55, v120, 0
	v_pk_add_f16 v56, v119, 0
	v_pk_fma_f16 v24, v24, v120, 0
	v_pk_fma_f16 v23, v23, v119, 0
	v_pk_fma_f16 v22, v22, v118, 0
	v_pk_add_f16 v72, v72, v116 neg_lo:[0,1] neg_hi:[0,1]
	v_pk_add_f16 v73, v73, v117 neg_lo:[0,1] neg_hi:[0,1]
	v_exp_f16_sdwa v118, v70 dst_sel:WORD_0 dst_unused:UNUSED_PAD src0_sel:WORD_0
	v_exp_f16_sdwa v119, v71 dst_sel:WORD_0 dst_unused:UNUSED_PAD src0_sel:WORD_0
	v_exp_f16_sdwa v120, v72 dst_sel:WORD_0 dst_unused:UNUSED_PAD src0_sel:WORD_0
	v_exp_f16_sdwa v121, v73 dst_sel:WORD_0 dst_unused:UNUSED_PAD src0_sel:WORD_0
	v_exp_f16_sdwa v118, v70 dst_sel:WORD_1 dst_unused:UNUSED_PRESERVE src0_sel:WORD_1
	v_exp_f16_sdwa v119, v71 dst_sel:WORD_1 dst_unused:UNUSED_PRESERVE src0_sel:WORD_1
	v_exp_f16_sdwa v120, v72 dst_sel:WORD_1 dst_unused:UNUSED_PRESERVE src0_sel:WORD_1
	v_exp_f16_sdwa v121, v73 dst_sel:WORD_1 dst_unused:UNUSED_PRESERVE src0_sel:WORD_1
	v_pk_add_f16 v57, v57, v118
	v_pk_fma_f16 v25, v37, v121, v25
	v_pk_add_f16 v37, v49, v117 neg_lo:[0,1] neg_hi:[0,1]
	v_pk_add_f16 v56, v56, v119
	v_pk_add_f16 v55, v55, v120
	v_pk_add_f16 v54, v54, v121
	v_pk_fma_f16 v22, v34, v118, v22
	v_pk_fma_f16 v23, v35, v119, v23
	v_pk_fma_f16 v24, v36, v120, v24
	v_pk_add_f16 v34, v46, v114 neg_lo:[0,1] neg_hi:[0,1]
	v_pk_add_f16 v35, v47, v115 neg_lo:[0,1] neg_hi:[0,1]
	v_pk_add_f16 v36, v48, v116 neg_lo:[0,1] neg_hi:[0,1]
	v_exp_f16_sdwa v46, v34 dst_sel:WORD_0 dst_unused:UNUSED_PAD src0_sel:WORD_0
	v_exp_f16_sdwa v47, v35 dst_sel:WORD_0 dst_unused:UNUSED_PAD src0_sel:WORD_0
	v_exp_f16_sdwa v48, v36 dst_sel:WORD_0 dst_unused:UNUSED_PAD src0_sel:WORD_0
	v_exp_f16_sdwa v49, v37 dst_sel:WORD_0 dst_unused:UNUSED_PAD src0_sel:WORD_0
	v_exp_f16_sdwa v46, v34 dst_sel:WORD_1 dst_unused:UNUSED_PRESERVE src0_sel:WORD_1
	v_exp_f16_sdwa v47, v35 dst_sel:WORD_1 dst_unused:UNUSED_PRESERVE src0_sel:WORD_1
	v_exp_f16_sdwa v48, v36 dst_sel:WORD_1 dst_unused:UNUSED_PRESERVE src0_sel:WORD_1
	v_exp_f16_sdwa v49, v37 dst_sel:WORD_1 dst_unused:UNUSED_PRESERVE src0_sel:WORD_1
	v_pk_add_f16 v37, v57, v46
	v_pk_add_f16 v34, v54, v49
	v_pk_add_f16 v35, v55, v48
	v_pk_add_f16 v36, v56, v47
	v_pk_fma_f16 v25, v53, v49, v25
	v_pk_fma_f16 v24, v52, v48, v24
	v_pk_fma_f16 v23, v51, v47, v23
	v_pk_fma_f16 v22, v50, v46, v22
	v_pk_add_f16 v46, v93, v114 neg_lo:[0,1] neg_hi:[0,1]
	v_pk_add_f16 v47, v92, v115 neg_lo:[0,1] neg_hi:[0,1]
	v_pk_add_f16 v48, v91, v116 neg_lo:[0,1] neg_hi:[0,1]
	v_pk_add_f16 v49, v90, v117 neg_lo:[0,1] neg_hi:[0,1]
	v_exp_f16_sdwa v50, v46 dst_sel:WORD_0 dst_unused:UNUSED_PAD src0_sel:WORD_0
	v_exp_f16_sdwa v51, v47 dst_sel:WORD_0 dst_unused:UNUSED_PAD src0_sel:WORD_0
	v_exp_f16_sdwa v52, v48 dst_sel:WORD_0 dst_unused:UNUSED_PAD src0_sel:WORD_0
	v_exp_f16_sdwa v53, v49 dst_sel:WORD_0 dst_unused:UNUSED_PAD src0_sel:WORD_0
	v_exp_f16_sdwa v50, v46 dst_sel:WORD_1 dst_unused:UNUSED_PRESERVE src0_sel:WORD_1
	v_exp_f16_sdwa v51, v47 dst_sel:WORD_1 dst_unused:UNUSED_PRESERVE src0_sel:WORD_1
	v_exp_f16_sdwa v52, v48 dst_sel:WORD_1 dst_unused:UNUSED_PRESERVE src0_sel:WORD_1
	v_exp_f16_sdwa v53, v49 dst_sel:WORD_1 dst_unused:UNUSED_PRESERVE src0_sel:WORD_1
	v_pk_add_f16 v46, v97, v114 neg_lo:[0,1] neg_hi:[0,1]
	v_pk_add_f16 v37, v37, v50
	v_pk_add_f16 v36, v36, v51
	v_pk_add_f16 v35, v35, v52
	v_pk_add_f16 v34, v34, v53
	v_pk_fma_f16 v22, v10, v50, v22
	v_pk_fma_f16 v23, v11, v51, v23
	v_pk_fma_f16 v24, v12, v52, v24
	v_pk_fma_f16 v25, v13, v53, v25
	v_pk_add_f16 v47, v96, v115 neg_lo:[0,1] neg_hi:[0,1]
	v_pk_add_f16 v48, v95, v116 neg_lo:[0,1] neg_hi:[0,1]
	v_pk_add_f16 v49, v94, v117 neg_lo:[0,1] neg_hi:[0,1]
	v_exp_f16_sdwa v50, v46 dst_sel:WORD_0 dst_unused:UNUSED_PAD src0_sel:WORD_0
	v_exp_f16_sdwa v51, v47 dst_sel:WORD_0 dst_unused:UNUSED_PAD src0_sel:WORD_0
	v_exp_f16_sdwa v52, v48 dst_sel:WORD_0 dst_unused:UNUSED_PAD src0_sel:WORD_0
	v_exp_f16_sdwa v53, v49 dst_sel:WORD_0 dst_unused:UNUSED_PAD src0_sel:WORD_0
	v_exp_f16_sdwa v50, v46 dst_sel:WORD_1 dst_unused:UNUSED_PRESERVE src0_sel:WORD_1
	v_exp_f16_sdwa v51, v47 dst_sel:WORD_1 dst_unused:UNUSED_PRESERVE src0_sel:WORD_1
	v_exp_f16_sdwa v52, v48 dst_sel:WORD_1 dst_unused:UNUSED_PRESERVE src0_sel:WORD_1
	v_exp_f16_sdwa v53, v49 dst_sel:WORD_1 dst_unused:UNUSED_PRESERVE src0_sel:WORD_1
	v_pk_add_f16 v46, v66, v114 neg_lo:[0,1] neg_hi:[0,1]
	v_pk_add_f16 v37, v37, v50
	v_pk_add_f16 v34, v34, v53
	v_pk_add_f16 v35, v35, v52
	v_pk_add_f16 v36, v36, v51
	v_pk_fma_f16 v25, v17, v53, v25
	v_pk_fma_f16 v24, v16, v52, v24
	v_pk_fma_f16 v23, v15, v51, v23
	v_pk_fma_f16 v22, v14, v50, v22
	v_pk_add_f16 v47, v67, v115 neg_lo:[0,1] neg_hi:[0,1]
	v_pk_add_f16 v48, v68, v116 neg_lo:[0,1] neg_hi:[0,1]
	v_pk_add_f16 v49, v69, v117 neg_lo:[0,1] neg_hi:[0,1]
	v_exp_f16_sdwa v50, v46 dst_sel:WORD_0 dst_unused:UNUSED_PAD src0_sel:WORD_0
	v_exp_f16_sdwa v51, v47 dst_sel:WORD_0 dst_unused:UNUSED_PAD src0_sel:WORD_0
	v_exp_f16_sdwa v52, v48 dst_sel:WORD_0 dst_unused:UNUSED_PAD src0_sel:WORD_0
	v_exp_f16_sdwa v53, v49 dst_sel:WORD_0 dst_unused:UNUSED_PAD src0_sel:WORD_0
	v_exp_f16_sdwa v50, v46 dst_sel:WORD_1 dst_unused:UNUSED_PRESERVE src0_sel:WORD_1
	v_exp_f16_sdwa v51, v47 dst_sel:WORD_1 dst_unused:UNUSED_PRESERVE src0_sel:WORD_1
	v_exp_f16_sdwa v52, v48 dst_sel:WORD_1 dst_unused:UNUSED_PRESERVE src0_sel:WORD_1
	v_exp_f16_sdwa v53, v49 dst_sel:WORD_1 dst_unused:UNUSED_PRESERVE src0_sel:WORD_1
	v_pk_add_f16 v46, v101, v114 neg_lo:[0,1] neg_hi:[0,1]
	v_pk_add_f16 v37, v37, v50
	v_pk_add_f16 v36, v36, v51
	v_pk_add_f16 v35, v35, v52
	v_pk_add_f16 v34, v34, v53
	v_pk_fma_f16 v22, v18, v50, v22
	v_pk_fma_f16 v23, v19, v51, v23
	v_pk_fma_f16 v24, v20, v52, v24
	v_pk_fma_f16 v25, v21, v53, v25
	v_pk_add_f16 v47, v100, v115 neg_lo:[0,1] neg_hi:[0,1]
	v_pk_add_f16 v48, v99, v116 neg_lo:[0,1] neg_hi:[0,1]
	v_pk_add_f16 v49, v98, v117 neg_lo:[0,1] neg_hi:[0,1]
	v_exp_f16_sdwa v50, v46 dst_sel:WORD_0 dst_unused:UNUSED_PAD src0_sel:WORD_0
	v_exp_f16_sdwa v51, v47 dst_sel:WORD_0 dst_unused:UNUSED_PAD src0_sel:WORD_0
	v_exp_f16_sdwa v52, v48 dst_sel:WORD_0 dst_unused:UNUSED_PAD src0_sel:WORD_0
	v_exp_f16_sdwa v53, v49 dst_sel:WORD_0 dst_unused:UNUSED_PAD src0_sel:WORD_0
	v_exp_f16_sdwa v50, v46 dst_sel:WORD_1 dst_unused:UNUSED_PRESERVE src0_sel:WORD_1
	v_exp_f16_sdwa v51, v47 dst_sel:WORD_1 dst_unused:UNUSED_PRESERVE src0_sel:WORD_1
	v_exp_f16_sdwa v52, v48 dst_sel:WORD_1 dst_unused:UNUSED_PRESERVE src0_sel:WORD_1
	v_exp_f16_sdwa v53, v49 dst_sel:WORD_1 dst_unused:UNUSED_PRESERVE src0_sel:WORD_1
	v_pk_add_f16 v46, v113, v114 neg_lo:[0,1] neg_hi:[0,1]
	v_pk_add_f16 v37, v37, v50
	v_pk_add_f16 v34, v34, v53
	v_pk_add_f16 v35, v35, v52
	v_pk_add_f16 v36, v36, v51
	v_pk_fma_f16 v25, v33, v53, v25
	v_pk_fma_f16 v24, v32, v52, v24
	v_pk_fma_f16 v23, v31, v51, v23
	v_pk_fma_f16 v22, v30, v50, v22
	v_pk_add_f16 v47, v112, v115 neg_lo:[0,1] neg_hi:[0,1]
	v_pk_add_f16 v48, v111, v116 neg_lo:[0,1] neg_hi:[0,1]
	v_pk_add_f16 v49, v110, v117 neg_lo:[0,1] neg_hi:[0,1]
	v_exp_f16_sdwa v50, v46 dst_sel:WORD_0 dst_unused:UNUSED_PAD src0_sel:WORD_0
	v_exp_f16_sdwa v51, v47 dst_sel:WORD_0 dst_unused:UNUSED_PAD src0_sel:WORD_0
	v_exp_f16_sdwa v52, v48 dst_sel:WORD_0 dst_unused:UNUSED_PAD src0_sel:WORD_0
	v_exp_f16_sdwa v53, v49 dst_sel:WORD_0 dst_unused:UNUSED_PAD src0_sel:WORD_0
	v_exp_f16_sdwa v50, v46 dst_sel:WORD_1 dst_unused:UNUSED_PRESERVE src0_sel:WORD_1
	v_exp_f16_sdwa v51, v47 dst_sel:WORD_1 dst_unused:UNUSED_PRESERVE src0_sel:WORD_1
	v_exp_f16_sdwa v52, v48 dst_sel:WORD_1 dst_unused:UNUSED_PRESERVE src0_sel:WORD_1
	v_exp_f16_sdwa v53, v49 dst_sel:WORD_1 dst_unused:UNUSED_PRESERVE src0_sel:WORD_1
	v_pk_add_f16 v46, v86, v114 neg_lo:[0,1] neg_hi:[0,1]
	v_pk_add_f16 v37, v37, v50
	v_pk_add_f16 v36, v36, v51
	v_pk_add_f16 v35, v35, v52
	v_pk_add_f16 v34, v34, v53
	v_pk_fma_f16 v22, v42, v50, v22
	v_pk_fma_f16 v23, v43, v51, v23
	v_pk_fma_f16 v24, v44, v52, v24
	v_pk_fma_f16 v25, v45, v53, v25
	v_pk_add_f16 v47, v87, v115 neg_lo:[0,1] neg_hi:[0,1]
	v_pk_add_f16 v48, v88, v116 neg_lo:[0,1] neg_hi:[0,1]
	v_pk_add_f16 v49, v89, v117 neg_lo:[0,1] neg_hi:[0,1]
	v_exp_f16_sdwa v50, v46 dst_sel:WORD_0 dst_unused:UNUSED_PAD src0_sel:WORD_0
	v_exp_f16_sdwa v51, v47 dst_sel:WORD_0 dst_unused:UNUSED_PAD src0_sel:WORD_0
	v_exp_f16_sdwa v52, v48 dst_sel:WORD_0 dst_unused:UNUSED_PAD src0_sel:WORD_0
	v_exp_f16_sdwa v53, v49 dst_sel:WORD_0 dst_unused:UNUSED_PAD src0_sel:WORD_0
	v_exp_f16_sdwa v50, v46 dst_sel:WORD_1 dst_unused:UNUSED_PRESERVE src0_sel:WORD_1
	v_exp_f16_sdwa v51, v47 dst_sel:WORD_1 dst_unused:UNUSED_PRESERVE src0_sel:WORD_1
	v_exp_f16_sdwa v52, v48 dst_sel:WORD_1 dst_unused:UNUSED_PRESERVE src0_sel:WORD_1
	v_exp_f16_sdwa v53, v49 dst_sel:WORD_1 dst_unused:UNUSED_PRESERVE src0_sel:WORD_1
	v_pk_add_f16 v37, v37, v50
	v_pk_add_f16 v36, v36, v51
	v_rcp_f16_e32 v46, v37
	v_rcp_f16_sdwa v37, v37 dst_sel:DWORD dst_unused:UNUSED_PAD src0_sel:WORD_1
	v_pk_add_f16 v35, v35, v52
	v_rcp_f16_e32 v47, v36
	v_rcp_f16_sdwa v36, v36 dst_sel:DWORD dst_unused:UNUSED_PAD src0_sel:WORD_1
	v_pk_add_f16 v34, v34, v53
	v_rcp_f16_e32 v48, v35
	v_rcp_f16_sdwa v35, v35 dst_sel:DWORD dst_unused:UNUSED_PAD src0_sel:WORD_1
	v_rcp_f16_e32 v49, v34
	v_rcp_f16_sdwa v34, v34 dst_sel:DWORD dst_unused:UNUSED_PAD src0_sel:WORD_1
	v_pk_fma_f16 v22, v62, v50, v22
	v_pack_b32_f16 v37, v46, v37
	v_pk_fma_f16 v23, v63, v51, v23
	v_pk_mul_f16 v57, v22, v37
	v_pack_b32_f16 v22, v47, v36
	v_pk_fma_f16 v24, v64, v52, v24
	v_pk_mul_f16 v56, v23, v22
	v_pack_b32_f16 v22, v48, v35
	v_pk_fma_f16 v25, v65, v53, v25
	v_pk_mul_f16 v55, v24, v22
	v_pack_b32_f16 v22, v49, v34
	v_pk_mul_f16 v54, v25, v22
	s_waitcnt vmcnt(0)
	s_mov_b32 s14, s38
	s_mov_b32 s15, s39
	v_add_u32_e32 v250, 0x0, v251
	buffer_load_dwordx4 v[252:255], v250, s[12:15], 0 offen
	v_add_u32_e32 v250, 0xfffe7c00, v251
	buffer_load_dwordx4 v[252:255], v250, s[12:15], 0 offen
	v_add_u32_e32 v250, 0xfffe7e00, v251
	buffer_load_dwordx4 v[252:255], v250, s[12:15], 0 offen
	v_add_u32_e32 v250, 0xfffe8200, v251
	buffer_load_dwordx4 v[252:255], v250, s[12:15], 0 offen
	v_add_u32_e32 v250, 0xfffe8400, v251
	buffer_load_dwordx4 v[252:255], v250, s[12:15], 0 offen
	v_add_u32_e32 v250, 0xfffe8800, v251
	buffer_load_dwordx4 v[252:255], v250, s[12:15], 0 offen
	v_add_u32_e32 v250, 0xfffe8a00, v251
	buffer_load_dwordx4 v[252:255], v250, s[12:15], 0 offen
	v_add_u32_e32 v250, 0xfffffc00, v251
	buffer_load_dwordx4 v[252:255], v250, s[12:15], 0 offen
	v_add_u32_e32 v250, 0xfffffe00, v251
	buffer_load_dwordx4 v[252:255], v250, s[12:15], 0 offen
	v_add_u32_e32 v250, 0x200, v251
	buffer_load_dwordx4 v[252:255], v250, s[12:15], 0 offen
	v_add_u32_e32 v250, 0x400, v251
	buffer_load_dwordx4 v[252:255], v250, s[12:15], 0 offen
	v_add_u32_e32 v250, 0x800, v251
	buffer_load_dwordx4 v[252:255], v250, s[12:15], 0 offen
	v_add_u32_e32 v250, 0xa00, v251
	buffer_load_dwordx4 v[252:255], v250, s[12:15], 0 offen
	v_add_u32_e32 v250, 0x17c00, v251
	buffer_load_dwordx4 v[252:255], v250, s[12:15], 0 offen
	v_add_u32_e32 v250, 0x17e00, v251
	buffer_load_dwordx4 v[252:255], v250, s[12:15], 0 offen
	v_add_u32_e32 v250, 0x18200, v251
	buffer_load_dwordx4 v[252:255], v250, s[12:15], 0 offen
	v_add_u32_e32 v250, 0x18400, v251
	buffer_load_dwordx4 v[252:255], v250, s[12:15], 0 offen
	v_add_u32_e32 v250, 0x18800, v251
	buffer_load_dwordx4 v[252:255], v250, s[12:15], 0 offen
	v_add_u32_e32 v250, 0x18a00, v251
	buffer_load_dwordx4 v[252:255], v250, s[12:15], 0 offen
	v_add_u32_e32 v250, 0x18000, v251
	buffer_load_dwordx4 v[252:255], v250, s[12:15], 0 offen
	v_add_u32_e32 v250, 0x30000, v251
	buffer_load_dwordx4 v[252:255], v250, s[12:15], 0 offen
	v_add_u32_e32 v250, 0x48000, v251
	buffer_load_dwordx4 v[252:255], v250, s[12:15], 0 offen
	v_pk_mul_f16 v22, v160, v146 op_sel_hi:[0,1]
	v_pk_mul_f16 v23, v160, v147 op_sel_hi:[0,1]
	v_pk_mul_f16 v24, v160, v148 op_sel_hi:[0,1]
	v_pk_mul_f16 v25, v160, v149 op_sel_hi:[0,1]
	v_pk_mul_f16 v46, v159, v146 op_sel_hi:[0,1]
	v_pk_mul_f16 v47, v159, v147 op_sel_hi:[0,1]
	v_pk_mul_f16 v48, v159, v148 op_sel_hi:[0,1]
	v_pk_mul_f16 v49, v159, v149 op_sel_hi:[0,1]
	v_pk_mul_f16 v34, v158, v146 op_sel_hi:[0,1]
	v_pk_mul_f16 v35, v158, v147 op_sel_hi:[0,1]
	v_pk_mul_f16 v36, v158, v148 op_sel_hi:[0,1]
	v_pk_mul_f16 v37, v158, v149 op_sel_hi:[0,1]
	v_pk_fma_f16 v29, v29, v149, v25
	v_pk_fma_f16 v28, v28, v148, v24
	v_pk_fma_f16 v27, v27, v147, v23
	v_pk_fma_f16 v26, v26, v146, v22
	v_pk_fma_f16 v41, v41, v149, v25
	v_pk_fma_f16 v40, v40, v148, v24
	v_pk_fma_f16 v39, v39, v147, v23
	v_pk_fma_f16 v38, v38, v146, v22
	v_pk_fma_f16 v25, v61, v149, v25
	v_pk_fma_f16 v24, v60, v148, v24
	v_pk_fma_f16 v23, v59, v147, v23
	v_pk_fma_f16 v22, v58, v146, v22
	v_pk_fma_f16 v66, v137, v149, v49
	v_pk_fma_f16 v67, v136, v148, v48
	v_pk_fma_f16 v68, v135, v147, v47
	v_pk_fma_f16 v69, v134, v146, v46
	v_pk_fma_f16 v70, v145, v149, v49
	v_pk_fma_f16 v71, v144, v148, v48
	v_pk_fma_f16 v72, v143, v147, v47
	v_pk_fma_f16 v73, v142, v146, v46
	v_pk_fma_f16 v9, v9, v149, v49
	v_pk_fma_f16 v8, v8, v148, v48
	v_pk_fma_f16 v7, v7, v147, v47
	v_pk_fma_f16 v6, v6, v146, v46
	v_pk_maximum3_f16 v46, v26, v38, v22
	v_pk_maximum3_f16 v47, v27, v39, v23
	v_pk_maximum3_f16 v48, v28, v40, v24
	v_pk_maximum3_f16 v49, v29, v41, v25
	v_pk_fma_f16 v50, v81, v149, v37
	v_pk_fma_f16 v51, v80, v148, v36
	v_pk_fma_f16 v52, v79, v147, v35
	v_pk_fma_f16 v53, v78, v146, v34
	v_pk_fma_f16 v58, v109, v149, v37
	v_pk_fma_f16 v59, v108, v148, v36
	v_pk_fma_f16 v60, v107, v147, v35
	v_pk_fma_f16 v61, v106, v146, v34
	v_pk_fma_f16 v37, v125, v149, v37
	v_pk_fma_f16 v36, v124, v148, v36
	v_pk_fma_f16 v35, v123, v147, v35
	v_pk_fma_f16 v34, v122, v146, v34
	v_pk_maximum3_f16 v79, v52, v60, v35
	v_pk_maximum3_f16 v80, v51, v59, v36
	v_pk_maximum3_f16 v81, v50, v58, v37
	v_pk_maximum3_f16 v86, v69, v73, v6
	v_pk_maximum3_f16 v87, v68, v72, v7
	v_pk_maximum3_f16 v78, v53, v61, v34
	v_pk_maximum3_f16 v88, v67, v71, v8
	v_pk_maximum3_f16 v89, v66, v70, v9
	v_pk_maximum3_f16 v46, v46, v78, v86
	v_pk_maximum3_f16 v47, v47, v79, v87
	v_pk_maximum3_f16 v48, v48, v80, v88
	v_pk_maximum3_f16 v49, v49, v81, v89
	s_nop 0
	v_pk_add_f16 v26, v26, v46 neg_lo:[0,1] neg_hi:[0,1]
	v_pk_add_f16 v27, v27, v47 neg_lo:[0,1] neg_hi:[0,1]
	v_pk_add_f16 v28, v28, v48 neg_lo:[0,1] neg_hi:[0,1]
	v_pk_add_f16 v29, v29, v49 neg_lo:[0,1] neg_hi:[0,1]
	v_pk_add_f16 v38, v38, v46 neg_lo:[0,1] neg_hi:[0,1]
	v_exp_f16_sdwa v78, v26 dst_sel:WORD_0 dst_unused:UNUSED_PAD src0_sel:WORD_0
	v_exp_f16_sdwa v79, v27 dst_sel:WORD_0 dst_unused:UNUSED_PAD src0_sel:WORD_0
	v_exp_f16_sdwa v80, v28 dst_sel:WORD_0 dst_unused:UNUSED_PAD src0_sel:WORD_0
	v_exp_f16_sdwa v81, v29 dst_sel:WORD_0 dst_unused:UNUSED_PAD src0_sel:WORD_0
	v_exp_f16_sdwa v78, v26 dst_sel:WORD_1 dst_unused:UNUSED_PRESERVE src0_sel:WORD_1
	v_exp_f16_sdwa v79, v27 dst_sel:WORD_1 dst_unused:UNUSED_PRESERVE src0_sel:WORD_1
	v_exp_f16_sdwa v80, v28 dst_sel:WORD_1 dst_unused:UNUSED_PRESERVE src0_sel:WORD_1
	v_exp_f16_sdwa v81, v29 dst_sel:WORD_1 dst_unused:UNUSED_PRESERVE src0_sel:WORD_1
	v_pk_add_f16 v39, v39, v47 neg_lo:[0,1] neg_hi:[0,1]
	v_pk_add_f16 v26, v78, 0
	v_pk_add_f16 v27, v79, 0
	v_pk_add_f16 v28, v80, 0
	v_pk_add_f16 v29, v81, 0
	v_pk_fma_f16 v10, v10, v78, 0
	v_pk_fma_f16 v11, v11, v79, 0
	v_pk_fma_f16 v12, v12, v80, 0
	v_pk_fma_f16 v13, v13, v81, 0
	v_pk_add_f16 v40, v40, v48 neg_lo:[0,1] neg_hi:[0,1]
	v_pk_add_f16 v41, v41, v49 neg_lo:[0,1] neg_hi:[0,1]
	v_pk_add_f16 v6, v6, v46 neg_lo:[0,1] neg_hi:[0,1]
	v_exp_f16_sdwa v78, v38 dst_sel:WORD_0 dst_unused:UNUSED_PAD src0_sel:WORD_0
	v_exp_f16_sdwa v79, v39 dst_sel:WORD_0 dst_unused:UNUSED_PAD src0_sel:WORD_0
	v_exp_f16_sdwa v80, v40 dst_sel:WORD_0 dst_unused:UNUSED_PAD src0_sel:WORD_0
	v_exp_f16_sdwa v81, v41 dst_sel:WORD_0 dst_unused:UNUSED_PAD src0_sel:WORD_0
	v_exp_f16_sdwa v78, v38 dst_sel:WORD_1 dst_unused:UNUSED_PRESERVE src0_sel:WORD_1
	v_exp_f16_sdwa v79, v39 dst_sel:WORD_1 dst_unused:UNUSED_PRESERVE src0_sel:WORD_1
	v_exp_f16_sdwa v80, v40 dst_sel:WORD_1 dst_unused:UNUSED_PRESERVE src0_sel:WORD_1
	v_exp_f16_sdwa v81, v41 dst_sel:WORD_1 dst_unused:UNUSED_PRESERVE src0_sel:WORD_1
	v_pk_add_f16 v7, v7, v47 neg_lo:[0,1] neg_hi:[0,1]
	v_pk_add_f16 v29, v29, v81
	v_pk_add_f16 v28, v28, v80
	v_pk_add_f16 v27, v27, v79
	v_pk_add_f16 v26, v26, v78
	v_pk_fma_f16 v13, v17, v81, v13
	v_pk_fma_f16 v12, v16, v80, v12
	v_pk_fma_f16 v11, v15, v79, v11
	v_pk_fma_f16 v10, v14, v78, v10
	v_pk_add_f16 v14, v22, v46 neg_lo:[0,1] neg_hi:[0,1]
	v_pk_add_f16 v15, v23, v47 neg_lo:[0,1] neg_hi:[0,1]
	v_pk_add_f16 v16, v24, v48 neg_lo:[0,1] neg_hi:[0,1]
	v_pk_add_f16 v17, v25, v49 neg_lo:[0,1] neg_hi:[0,1]
	v_pk_add_f16 v8, v8, v48 neg_lo:[0,1] neg_hi:[0,1]
	v_exp_f16_sdwa v22, v14 dst_sel:WORD_0 dst_unused:UNUSED_PAD src0_sel:WORD_0
	v_exp_f16_sdwa v23, v15 dst_sel:WORD_0 dst_unused:UNUSED_PAD src0_sel:WORD_0
	v_exp_f16_sdwa v24, v16 dst_sel:WORD_0 dst_unused:UNUSED_PAD src0_sel:WORD_0
	v_exp_f16_sdwa v25, v17 dst_sel:WORD_0 dst_unused:UNUSED_PAD src0_sel:WORD_0
	v_exp_f16_sdwa v22, v14 dst_sel:WORD_1 dst_unused:UNUSED_PRESERVE src0_sel:WORD_1
	v_exp_f16_sdwa v23, v15 dst_sel:WORD_1 dst_unused:UNUSED_PRESERVE src0_sel:WORD_1
	v_exp_f16_sdwa v24, v16 dst_sel:WORD_1 dst_unused:UNUSED_PRESERVE src0_sel:WORD_1
	v_exp_f16_sdwa v25, v17 dst_sel:WORD_1 dst_unused:UNUSED_PRESERVE src0_sel:WORD_1
	v_pk_add_f16 v9, v9, v49 neg_lo:[0,1] neg_hi:[0,1]
	v_pk_add_f16 v14, v26, v22
	v_pk_add_f16 v15, v27, v23
	v_pk_add_f16 v16, v28, v24
	v_pk_add_f16 v17, v29, v25
	v_pk_fma_f16 v10, v18, v22, v10
	v_pk_fma_f16 v11, v19, v23, v11
	v_pk_fma_f16 v12, v20, v24, v12
	v_pk_fma_f16 v13, v21, v25, v13
	v_pk_add_f16 v18, v53, v46 neg_lo:[0,1] neg_hi:[0,1]
	v_pk_add_f16 v19, v52, v47 neg_lo:[0,1] neg_hi:[0,1]
	v_pk_add_f16 v20, v51, v48 neg_lo:[0,1] neg_hi:[0,1]
	v_pk_add_f16 v21, v50, v49 neg_lo:[0,1] neg_hi:[0,1]
	v_exp_f16_sdwa v22, v18 dst_sel:WORD_0 dst_unused:UNUSED_PAD src0_sel:WORD_0
	v_exp_f16_sdwa v23, v19 dst_sel:WORD_0 dst_unused:UNUSED_PAD src0_sel:WORD_0
	v_exp_f16_sdwa v24, v20 dst_sel:WORD_0 dst_unused:UNUSED_PAD src0_sel:WORD_0
	v_exp_f16_sdwa v25, v21 dst_sel:WORD_0 dst_unused:UNUSED_PAD src0_sel:WORD_0
	v_exp_f16_sdwa v22, v18 dst_sel:WORD_1 dst_unused:UNUSED_PRESERVE src0_sel:WORD_1
	v_exp_f16_sdwa v23, v19 dst_sel:WORD_1 dst_unused:UNUSED_PRESERVE src0_sel:WORD_1
	v_exp_f16_sdwa v24, v20 dst_sel:WORD_1 dst_unused:UNUSED_PRESERVE src0_sel:WORD_1
	v_exp_f16_sdwa v25, v21 dst_sel:WORD_1 dst_unused:UNUSED_PRESERVE src0_sel:WORD_1
	v_pk_add_f16 v18, v61, v46 neg_lo:[0,1] neg_hi:[0,1]
	v_pk_add_f16 v17, v17, v25
	v_pk_add_f16 v16, v16, v24
	v_pk_add_f16 v15, v15, v23
	v_pk_add_f16 v14, v14, v22
	v_pk_fma_f16 v13, v33, v25, v13
	v_pk_fma_f16 v12, v32, v24, v12
	v_pk_fma_f16 v11, v31, v23, v11
	v_pk_fma_f16 v10, v30, v22, v10
	v_pk_add_f16 v19, v60, v47 neg_lo:[0,1] neg_hi:[0,1]
	v_pk_add_f16 v20, v59, v48 neg_lo:[0,1] neg_hi:[0,1]
	v_pk_add_f16 v21, v58, v49 neg_lo:[0,1] neg_hi:[0,1]
	v_exp_f16_sdwa v30, v6 dst_sel:WORD_0 dst_unused:UNUSED_PAD src0_sel:WORD_0
	v_exp_f16_sdwa v31, v7 dst_sel:WORD_0 dst_unused:UNUSED_PAD src0_sel:WORD_0
	v_exp_f16_sdwa v32, v8 dst_sel:WORD_0 dst_unused:UNUSED_PAD src0_sel:WORD_0
	v_exp_f16_sdwa v33, v9 dst_sel:WORD_0 dst_unused:UNUSED_PAD src0_sel:WORD_0
	v_exp_f16_sdwa v30, v6 dst_sel:WORD_1 dst_unused:UNUSED_PRESERVE src0_sel:WORD_1
	v_exp_f16_sdwa v31, v7 dst_sel:WORD_1 dst_unused:UNUSED_PRESERVE src0_sel:WORD_1
	v_exp_f16_sdwa v32, v8 dst_sel:WORD_1 dst_unused:UNUSED_PRESERVE src0_sel:WORD_1
	v_exp_f16_sdwa v33, v9 dst_sel:WORD_1 dst_unused:UNUSED_PRESERVE src0_sel:WORD_1
	v_exp_f16_sdwa v22, v18 dst_sel:WORD_0 dst_unused:UNUSED_PAD src0_sel:WORD_0
	v_exp_f16_sdwa v23, v19 dst_sel:WORD_0 dst_unused:UNUSED_PAD src0_sel:WORD_0
	v_exp_f16_sdwa v24, v20 dst_sel:WORD_0 dst_unused:UNUSED_PAD src0_sel:WORD_0
	v_exp_f16_sdwa v25, v21 dst_sel:WORD_0 dst_unused:UNUSED_PAD src0_sel:WORD_0
	v_exp_f16_sdwa v22, v18 dst_sel:WORD_1 dst_unused:UNUSED_PRESERVE src0_sel:WORD_1
	v_exp_f16_sdwa v23, v19 dst_sel:WORD_1 dst_unused:UNUSED_PRESERVE src0_sel:WORD_1
	v_exp_f16_sdwa v24, v20 dst_sel:WORD_1 dst_unused:UNUSED_PRESERVE src0_sel:WORD_1
	v_exp_f16_sdwa v25, v21 dst_sel:WORD_1 dst_unused:UNUSED_PRESERVE src0_sel:WORD_1
	v_pk_add_f16 v18, v34, v46 neg_lo:[0,1] neg_hi:[0,1]
	v_pk_add_f16 v14, v14, v22
	v_pk_add_f16 v15, v15, v23
	v_pk_add_f16 v16, v16, v24
	v_pk_add_f16 v17, v17, v25
	v_pk_fma_f16 v10, v42, v22, v10
	v_pk_fma_f16 v11, v43, v23, v11
	v_pk_fma_f16 v12, v44, v24, v12
	v_pk_fma_f16 v13, v45, v25, v13
	v_pk_add_f16 v19, v35, v47 neg_lo:[0,1] neg_hi:[0,1]
	v_pk_add_f16 v20, v36, v48 neg_lo:[0,1] neg_hi:[0,1]
	v_pk_add_f16 v21, v37, v49 neg_lo:[0,1] neg_hi:[0,1]
	v_exp_f16_sdwa v22, v18 dst_sel:WORD_0 dst_unused:UNUSED_PAD src0_sel:WORD_0
	v_exp_f16_sdwa v23, v19 dst_sel:WORD_0 dst_unused:UNUSED_PAD src0_sel:WORD_0
	v_exp_f16_sdwa v24, v20 dst_sel:WORD_0 dst_unused:UNUSED_PAD src0_sel:WORD_0
	v_exp_f16_sdwa v25, v21 dst_sel:WORD_0 dst_unused:UNUSED_PAD src0_sel:WORD_0
	v_exp_f16_sdwa v22, v18 dst_sel:WORD_1 dst_unused:UNUSED_PRESERVE src0_sel:WORD_1
	v_exp_f16_sdwa v23, v19 dst_sel:WORD_1 dst_unused:UNUSED_PRESERVE src0_sel:WORD_1
	v_exp_f16_sdwa v24, v20 dst_sel:WORD_1 dst_unused:UNUSED_PRESERVE src0_sel:WORD_1
	v_exp_f16_sdwa v25, v21 dst_sel:WORD_1 dst_unused:UNUSED_PRESERVE src0_sel:WORD_1
	v_pk_add_f16 v18, v69, v46 neg_lo:[0,1] neg_hi:[0,1]
	v_pk_add_f16 v17, v17, v25
	v_pk_add_f16 v16, v16, v24
	v_pk_add_f16 v15, v15, v23
	v_pk_add_f16 v14, v14, v22
	v_pk_fma_f16 v13, v65, v25, v13
	v_pk_fma_f16 v12, v64, v24, v12
	v_pk_fma_f16 v11, v63, v23, v11
	v_pk_fma_f16 v10, v62, v22, v10
	v_pk_add_f16 v19, v68, v47 neg_lo:[0,1] neg_hi:[0,1]
	v_pk_add_f16 v20, v67, v48 neg_lo:[0,1] neg_hi:[0,1]
	v_pk_add_f16 v21, v66, v49 neg_lo:[0,1] neg_hi:[0,1]
	v_exp_f16_sdwa v22, v18 dst_sel:WORD_0 dst_unused:UNUSED_PAD src0_sel:WORD_0
	v_exp_f16_sdwa v23, v19 dst_sel:WORD_0 dst_unused:UNUSED_PAD src0_sel:WORD_0
	v_exp_f16_sdwa v24, v20 dst_sel:WORD_0 dst_unused:UNUSED_PAD src0_sel:WORD_0
	v_exp_f16_sdwa v25, v21 dst_sel:WORD_0 dst_unused:UNUSED_PAD src0_sel:WORD_0
	v_exp_f16_sdwa v22, v18 dst_sel:WORD_1 dst_unused:UNUSED_PRESERVE src0_sel:WORD_1
	v_exp_f16_sdwa v23, v19 dst_sel:WORD_1 dst_unused:UNUSED_PRESERVE src0_sel:WORD_1
	v_exp_f16_sdwa v24, v20 dst_sel:WORD_1 dst_unused:UNUSED_PRESERVE src0_sel:WORD_1
	v_exp_f16_sdwa v25, v21 dst_sel:WORD_1 dst_unused:UNUSED_PRESERVE src0_sel:WORD_1
	v_pk_add_f16 v18, v73, v46 neg_lo:[0,1] neg_hi:[0,1]
	v_pk_add_f16 v14, v14, v22
	v_pk_add_f16 v15, v15, v23
	v_pk_add_f16 v16, v16, v24
	v_pk_add_f16 v17, v17, v25
	v_pk_fma_f16 v10, v82, v22, v10
	v_pk_fma_f16 v11, v83, v23, v11
	v_pk_fma_f16 v12, v84, v24, v12
	v_pk_fma_f16 v13, v85, v25, v13
	v_pk_add_f16 v19, v72, v47 neg_lo:[0,1] neg_hi:[0,1]
	v_pk_add_f16 v20, v71, v48 neg_lo:[0,1] neg_hi:[0,1]
	v_pk_add_f16 v21, v70, v49 neg_lo:[0,1] neg_hi:[0,1]
	v_exp_f16_sdwa v22, v18 dst_sel:WORD_0 dst_unused:UNUSED_PAD src0_sel:WORD_0
	v_exp_f16_sdwa v23, v19 dst_sel:WORD_0 dst_unused:UNUSED_PAD src0_sel:WORD_0
	v_exp_f16_sdwa v24, v20 dst_sel:WORD_0 dst_unused:UNUSED_PAD src0_sel:WORD_0
	v_exp_f16_sdwa v25, v21 dst_sel:WORD_0 dst_unused:UNUSED_PAD src0_sel:WORD_0
	v_exp_f16_sdwa v22, v18 dst_sel:WORD_1 dst_unused:UNUSED_PRESERVE src0_sel:WORD_1
	v_exp_f16_sdwa v23, v19 dst_sel:WORD_1 dst_unused:UNUSED_PRESERVE src0_sel:WORD_1
	v_exp_f16_sdwa v24, v20 dst_sel:WORD_1 dst_unused:UNUSED_PRESERVE src0_sel:WORD_1
	v_exp_f16_sdwa v25, v21 dst_sel:WORD_1 dst_unused:UNUSED_PRESERVE src0_sel:WORD_1
	s_nop 0
	v_pk_add_f16 v17, v17, v25
	v_pk_add_f16 v16, v16, v24
	v_pk_add_f16 v15, v15, v23
	v_pk_add_f16 v14, v14, v22
	v_pk_fma_f16 v21, v105, v25, v13
	v_pk_fma_f16 v20, v104, v24, v12
	v_pk_fma_f16 v19, v103, v23, v11
	v_pk_fma_f16 v18, v102, v22, v10
	v_mov_b32_e32 v13, v5
	v_mov_b32_e32 v12, v4
	v_mov_b32_e32 v11, v3
	v_mov_b32_e32 v10, v2

amdhsa.kernels:
  - .agpr_count:     0
    .args:
      - .actual_access:  read_only
        .address_space:  global
        .offset:         0
        .size:           8
        .value_kind:     global_buffer
      - .actual_access:  read_only
        .address_space:  global
        .offset:         8
        .size:           8
        .value_kind:     global_buffer
      - .actual_access:  read_only
        .address_space:  global
        .offset:         16
        .size:           8
        .value_kind:     global_buffer
      - .actual_access:  read_only
        .address_space:  global
        .offset:         24
        .size:           8
        .value_kind:     global_buffer
      - .actual_access:  read_only
        .address_space:  global
        .offset:         32
        .size:           8
        .value_kind:     global_buffer
      - .actual_access:  read_only
        .address_space:  global
        .offset:         40
        .size:           8
        .value_kind:     global_buffer
      - .actual_access:  read_only
        .address_space:  global
        .offset:         48
        .size:           8
        .value_kind:     global_buffer
      - .actual_access:  read_only
        .address_space:  global
        .offset:         56
        .size:           8
        .value_kind:     global_buffer
      - .actual_access:  write_only
        .address_space:  global
        .offset:         64
        .size:           8
        .value_kind:     global_buffer
      - .actual_access:  write_only
        .address_space:  global
        .offset:         72
        .size:           8
        .value_kind:     global_buffer
      - .actual_access:  write_only
        .address_space:  global
        .offset:         80
        .size:           8
        .value_kind:     global_buffer
      - .actual_access:  write_only
        .address_space:  global
        .offset:         88
        .size:           8
        .value_kind:     global_buffer
    .group_segment_fixed_size: 0
    .kernarg_segment_align: 8
    .kernarg_segment_size: 96
    .language:       OpenCL C
    .language_version:
      - 2
      - 0
    .max_flat_workgroup_size: 256
    .name:           _Z8k_prep_wPKfS0_S0_S0_S0_S0_S0_S0_PDF16_PfS1_S1_
    .private_segment_fixed_size: 0
    .sgpr_count:     23
    .sgpr_spill_count: 0
    .symbol:         _Z8k_prep_wPKfS0_S0_S0_S0_S0_S0_S0_PDF16_PfS1_S1_.kd
    .uniform_work_group_size: 1
    .uses_dynamic_stack: false
    .vgpr_count:     15
    .vgpr_spill_count: 0
    .wavefront_size: 64
  - .agpr_count:     0
    .args:
      - .actual_access:  read_only
        .address_space:  global
        .offset:         0
        .size:           8
        .value_kind:     global_buffer
      - .actual_access:  read_only
        .address_space:  global
        .offset:         8
        .size:           8
        .value_kind:     global_buffer
      - .actual_access:  read_only
        .address_space:  global
        .offset:         16
        .size:           8
        .value_kind:     global_buffer
      - .actual_access:  read_only
        .address_space:  global
        .offset:         24
        .size:           8
        .value_kind:     global_buffer
      - .actual_access:  write_only
        .address_space:  global
        .offset:         32
        .size:           8
        .value_kind:     global_buffer
      - .actual_access:  read_only
        .address_space:  global
        .offset:         40
        .size:           8
        .value_kind:     global_buffer
      - .actual_access:  read_only
        .address_space:  global
        .offset:         48
        .size:           8
        .value_kind:     global_buffer
      - .actual_access:  write_only
        .address_space:  global
        .offset:         56
        .size:           8
        .value_kind:     global_buffer
      - .offset:         64
        .size:           4
        .value_kind:     by_value
      - .offset:         68
        .size:           4
        .value_kind:     by_value
    .group_segment_fixed_size: 115712
    .kernarg_segment_align: 8
    .kernarg_segment_size: 72
    .language:       OpenCL C
    .language_version:
      - 2
      - 0
    .max_flat_workgroup_size: 512
    .name:           _Z8k_stageAPKfS0_S0_S0_PDF16_PKDF16_S0_S1_ii
    .private_segment_fixed_size: 0
    .sgpr_count:     28
    .sgpr_spill_count: 0
    .symbol:         _Z8k_stageAPKfS0_S0_S0_PDF16_PKDF16_S0_S1_ii.kd
    .uniform_work_group_size: 1
    .uses_dynamic_stack: false
    .vgpr_count:     251
    .vgpr_spill_count: 0
    .wavefront_size: 64
  - .agpr_count:     112
    .args:
      - .actual_access:  read_only
        .address_space:  global
        .offset:         0
        .size:           8
        .value_kind:     global_buffer
      - .actual_access:  read_only
        .address_space:  global
        .offset:         8
        .size:           8
        .value_kind:     global_buffer
      - .actual_access:  read_only
        .address_space:  global
        .offset:         16
        .size:           8
        .value_kind:     global_buffer
      - .actual_access:  read_only
        .address_space:  global
        .offset:         24
        .size:           8
        .value_kind:     global_buffer
      - .actual_access:  read_only
        .address_space:  global
        .offset:         32
        .size:           8
        .value_kind:     global_buffer
      - .actual_access:  write_only
        .address_space:  global
        .offset:         40
        .size:           8
        .value_kind:     global_buffer
    .group_segment_fixed_size: 107712
    .kernarg_segment_align: 8
    .kernarg_segment_size: 48
    .language:       OpenCL C
    .language_version:
      - 2
      - 0
    .max_flat_workgroup_size: 256
    .name:           _Z7k_conv4PKDF16_S0_S0_PKfS2_Pf
    .private_segment_fixed_size: 0
    .sgpr_count:     36
    .sgpr_spill_count: 0
    .symbol:         _Z7k_conv4PKDF16_S0_S0_PKfS2_Pf.kd
    .uniform_work_group_size: 1
    .uses_dynamic_stack: false
    .vgpr_count:     328
    .vgpr_spill_count: 0
    .wavefront_size: 64
  - .agpr_count:     0
    .args:
      - .offset:         0
        .size:           112
        .value_kind:     by_value
      - .actual_access:  read_only
        .address_space:  global
        .offset:         112
        .size:           8
        .value_kind:     global_buffer
      - .actual_access:  read_only
        .address_space:  global
        .offset:         120
        .size:           8
        .value_kind:     global_buffer
      - .actual_access:  write_only
        .address_space:  global
        .offset:         128
        .size:           8
        .value_kind:     global_buffer
      - .offset:         136
        .size:           4
        .value_kind:     by_value
      - .offset:         140
        .size:           4
        .value_kind:     by_value
      - .offset:         144
        .size:           4
        .value_kind:     by_value
    .group_segment_fixed_size: 115712
    .kernarg_segment_align: 8
    .kernarg_segment_size: 148
    .language:       OpenCL C
    .language_version:
      - 2
      - 0
    .max_flat_workgroup_size: 512
    .name:           _Z7k_stageILi0ELi8EEv8AttnArgsPKDF16_PKfPDF16_iii
    .private_segment_fixed_size: 0
    .sgpr_count:     41
    .sgpr_spill_count: 0
    .symbol:         _Z7k_stageILi0ELi8EEv8AttnArgsPKDF16_PKfPDF16_iii.kd
    .uniform_work_group_size: 1
    .uses_dynamic_stack: false
    .vgpr_count:     256
    .vgpr_spill_count: 0
    .wavefront_size: 64
  - .agpr_count:     0
    .args:
      - .offset:         0
        .size:           112
        .value_kind:     by_value
      - .actual_access:  read_only
        .address_space:  global
        .offset:         112
        .size:           8
        .value_kind:     global_buffer
      - .actual_access:  read_only
        .address_space:  global
        .offset:         120
        .size:           8
        .value_kind:     global_buffer
      - .actual_access:  write_only
        .address_space:  global
        .offset:         128
        .size:           8
        .value_kind:     global_buffer
      - .offset:         136
        .size:           4
        .value_kind:     by_value
      - .offset:         140
        .size:           4
        .value_kind:     by_value
      - .offset:         144
        .size:           4
        .value_kind:     by_value
    .group_segment_fixed_size: 82944
    .kernarg_segment_align: 8
    .kernarg_segment_size: 148
    .language:       OpenCL C
    .language_version:
      - 2
      - 0
    .max_flat_workgroup_size: 512
    .name:           _Z7k_stageILi1ELi4EEv8AttnArgsPKDF16_PKfPDF16_iii
    .private_segment_fixed_size: 0
    .sgpr_count:     55
    .sgpr_spill_count: 0
    .symbol:         _Z7k_stageILi1ELi4EEv8AttnArgsPKDF16_PKfPDF16_iii.kd
    .uniform_work_group_size: 1
    .uses_dynamic_stack: false
    .vgpr_count:     256
    .vgpr_spill_count: 0
    .wavefront_size: 64
  - .agpr_count:     0
    .args:
      - .offset:         0
        .size:           112
        .value_kind:     by_value
      - .actual_access:  read_only
        .address_space:  global
        .offset:         112
        .size:           8
        .value_kind:     global_buffer
      - .actual_access:  read_only
        .address_space:  global
        .offset:         120
        .size:           8
        .value_kind:     global_buffer
      - .actual_access:  write_only
        .address_space:  global
        .offset:         128
        .size:           8
        .value_kind:     global_buffer
      - .offset:         136
        .size:           4
        .value_kind:     by_value
      - .offset:         140
        .size:           4
        .value_kind:     by_value
      - .offset:         144
        .size:           4
        .value_kind:     by_value
    .group_segment_fixed_size: 82944
    .kernarg_segment_align: 8
    .kernarg_segment_size: 148
    .language:       OpenCL C
    .language_version:
      - 2
      - 0
    .max_flat_workgroup_size: 512
    .name:           _Z7k_stageILi0ELi4EEv8AttnArgsPKDF16_PKfPDF16_iii
    .private_segment_fixed_size: 0
    .sgpr_count:     38
    .sgpr_spill_count: 0
    .symbol:         _Z7k_stageILi0ELi4EEv8AttnArgsPKDF16_PKfPDF16_iii.kd
    .uniform_work_group_size: 1
    .uses_dynamic_stack: false
    .vgpr_count:     246
    .vgpr_spill_count: 0
    .wavefront_size: 64
  - .agpr_count:     0
    .args:
      - .offset:         0
        .size:           112
        .value_kind:     by_value
    .group_segment_fixed_size: 0
    .kernarg_segment_align: 8
    .kernarg_segment_size: 112
    .language:       OpenCL C
    .language_version:
      - 2
      - 0
    .max_flat_workgroup_size: 512
    .name:           _Z7k_attn2ILi2EEv8AttnArgs
    .private_segment_fixed_size: 0
    .sgpr_count:     102
    .sgpr_spill_count: 0
    .symbol:         _Z7k_attn2ILi2EEv8AttnArgs.kd
    .uniform_work_group_size: 1
    .uses_dynamic_stack: false
    .vgpr_count:     252
    .vgpr_spill_count: 0
    .wavefront_size: 64
